# GEMM main loops: removed redundant mid-segment s_setprio 0/1 pairs (on top of barrier edit)
# baseline (speedup 1.0000x reference)
; #define PG8_STAGE(bufoff, gbase, voff) do { _Pragma("unroll") for (int _i = 0; _i < 2; ++_i) \
;         __builtin_amdgcn_global_load_lds((const unsigned*)((const char*)(gbase) + (voff)[_i]), (LAS unsigned*)(lds + (bufoff) + ldsw + _i * 8192), 16, 0, 0); } while (0)
; #define PG8_LDA(dst, b, h) do { _Pragma("unroll") for (int m = 0; m < 4; ++m) _Pragma("unroll") for (int k = 0; k < 2; ++k) dst[m][k] = *(const LAS bf16x8*)(lds + PG8_SA(b, h) + aoff + m * 2048 + k * 1024); } while (0)
; #define PG8_LDB(dst, b, h) do { _Pragma("unroll") for (int n = 0; n < 2; ++n) _Pragma("unroll") for (int k = 0; k < 2; ++k) dst[n][k] = *(const LAS bf16x8*)(lds + PG8_SB(b, h) + boff + n * 2048 + k * 1024); } while (0)
; #define PG8_MMA(ai, bj, At, Bt) do { __builtin_amdgcn_s_setprio(1); _Pragma("unroll") for (int m = 0; m < 4; ++m) _Pragma("unroll") for (int n = 0; n < 2; ++n) _Pragma("unroll") for (int k = 0; k < 2; ++k) \
;         acc[ai][bj][m][n] = __builtin_amdgcn_mfma_f32_16x16x32_bf16(Bt[n][k], At[m][k], acc[ai][bj][m][n], 0, 0, 0); __builtin_amdgcn_s_setprio(0); } while (0)
; #define PG8_BAR __builtin_amdgcn_s_barrier()
; template <class Epi, class Sched>
; __device__ __forceinline__ void gemm_phase(LAS unsigned char* lds, const Gemm g, const Sched& S, const Epi& E, const int tid, unsigned* last_sig = nullptr) {
;     ...
;         const char* nA = has_next ? (const char*)g.A + (size_t)nxt.pm * tstep : cA; const char* nB = has_next ? (const char*)g.Bt + (size_t)nxt.be * g.bstride + (size_t)nxt.pn * tstep : cB;
;         for (int t = 0; t < nt; t += 2) {
;             const bool last = (t == nt - 2);
;             const char* a1 = cA + (size_t)(t + 1) * kstep;
;             const char* a2 = last ? nA : cA + (size_t)(t + 2) * kstep; const char* b2 = last ? nB : cB + (size_t)(t + 2) * kstep;
;             const char* a3 = a2 + kstep; const char* b3 = b2 + kstep;
;             PG8_LDB(B0, 0, 0); PG8_LDB(B1, 0, 1); PG8_SCHED; PG8_LDA(At, 0, 0); PG8_STAGE(PG8_SA(1, 1), a1 + hstep, voffA);
;             PG8_WAIT_V(8); PG8_WAIT_L(0); PG8_BAR; PG8_MMA(0, 0, At, B0); PG8_MMA(0, 1, At, B1); PG8_BAR; PG8_SCHED;
;             PG8_LDA(At, 0, 1); PG8_STAGE(PG8_SB(0, 0), b2, voffB); PG8_STAGE(PG8_SB(0, 1), b2 + hstep, voffB); PG8_STAGE(PG8_SA(0, 0), a2, voffA);
;             PG8_WAIT_V(8); PG8_WAIT_L(0); PG8_BAR; PG8_MMA(1, 0, At, B0); PG8_MMA(1, 1, At, B1); PG8_BAR; PG8_SCHED;
.LBB0_172:
	s_add_u32 s14, s20, 0xfff80080
	s_addc_u32 s15, s21, -1
	s_add_i32 s60, 0, 0x10000
	s_cmp_eq_u32 s59, 28
	s_cselect_b32 s41, s13, s15
	s_cselect_b32 s40, s28, s14
	s_cselect_b32 s23, s11, s58
	s_cselect_b32 s22, s56, s57
	s_add_i32 s14, 0, 0x14000
	v_add_u32_e32 v160, s60, v145
	v_add_u32_e32 v176, s14, v145
	ds_read_b128 v[130:133], v160
	ds_read_b128 v[152:155], v160 offset:1024
	ds_read_b128 v[156:159], v160 offset:2048
	ds_read_b128 v[160:163], v160 offset:3072
	ds_read_b128 v[164:167], v176
	ds_read_b128 v[168:171], v176 offset:1024
	ds_read_b128 v[172:175], v176 offset:2048
	ds_read_b128 v[176:179], v176 offset:3072
	v_lshl_add_u64 v[184:185], s[20:21], 0, v[148:149]
	s_add_i32 m0, s44, 0xc000
	ds_read_b128 v[180:183], v147
	ds_read_b128 v[200:203], v147 offset:1024
	ds_read_b128 v[204:207], v147 offset:2048
	ds_read_b128 v[208:211], v147 offset:3072
	ds_read_b128 v[212:215], v147 offset:4096
	ds_read_b128 v[216:219], v147 offset:5120
	ds_read_b128 v[220:223], v147 offset:6144
	ds_read_b128 v[232:235], v147 offset:7168
	global_load_lds_dwordx4 v[184:185], off
	v_lshl_add_u64 v[184:185], s[20:21], 0, v[150:151]
	s_add_i32 m0, s44, 0xe000
	s_nop 0
	global_load_lds_dwordx4 v[184:185], off
	s_waitcnt vmcnt(8)
	s_waitcnt lgkmcnt(0)
	s_barrier
	s_setprio 1
	s_waitcnt lgkmcnt(0)
	v_mfma_f32_16x16x32_bf16 v[126:129], v[130:133], v[180:183], v[126:129]
	v_mfma_f32_16x16x32_bf16 v[122:125], v[156:159], v[180:183], v[122:125]
	v_mfma_f32_16x16x32_bf16 v[118:121], v[130:133], v[204:207], v[118:121]
	v_mfma_f32_16x16x32_bf16 v[110:113], v[156:159], v[204:207], v[110:113]
	v_mfma_f32_16x16x32_bf16 v[102:105], v[130:133], v[212:215], v[102:105]
	v_mfma_f32_16x16x32_bf16 v[94:97], v[156:159], v[212:215], v[94:97]
	v_mfma_f32_16x16x32_bf16 v[86:89], v[130:133], v[220:223], v[86:89]
	v_mfma_f32_16x16x32_bf16 v[78:81], v[156:159], v[220:223], v[78:81]
	v_mfma_f32_16x16x32_bf16 v[126:129], v[152:155], v[200:203], v[126:129]
	v_mfma_f32_16x16x32_bf16 v[122:125], v[160:163], v[200:203], v[122:125]
	v_mfma_f32_16x16x32_bf16 v[118:121], v[152:155], v[208:211], v[118:121]
	v_mfma_f32_16x16x32_bf16 v[110:113], v[160:163], v[208:211], v[110:113]
	v_mfma_f32_16x16x32_bf16 v[102:105], v[152:155], v[216:219], v[102:105]
	v_mfma_f32_16x16x32_bf16 v[94:97], v[160:163], v[216:219], v[94:97]
	v_mfma_f32_16x16x32_bf16 v[86:89], v[152:155], v[232:235], v[86:89]
	v_mfma_f32_16x16x32_bf16 v[78:81], v[160:163], v[232:235], v[78:81]
	v_mfma_f32_16x16x32_bf16 v[114:117], v[164:167], v[180:183], v[114:117]
	v_mfma_f32_16x16x32_bf16 v[106:109], v[172:175], v[180:183], v[106:109]
	v_mfma_f32_16x16x32_bf16 v[98:101], v[164:167], v[204:207], v[98:101]
	v_mfma_f32_16x16x32_bf16 v[90:93], v[172:175], v[204:207], v[90:93]
	v_mfma_f32_16x16x32_bf16 v[82:85], v[164:167], v[212:215], v[82:85]
	v_mfma_f32_16x16x32_bf16 v[74:77], v[172:175], v[212:215], v[74:77]
	v_mfma_f32_16x16x32_bf16 v[70:73], v[164:167], v[220:223], v[70:73]
	v_mfma_f32_16x16x32_bf16 v[66:69], v[172:175], v[220:223], v[66:69]
	v_mfma_f32_16x16x32_bf16 v[114:117], v[168:171], v[200:203], v[114:117]
	v_mfma_f32_16x16x32_bf16 v[106:109], v[176:179], v[200:203], v[106:109]
	v_mfma_f32_16x16x32_bf16 v[98:101], v[168:171], v[208:211], v[98:101]
	v_mfma_f32_16x16x32_bf16 v[90:93], v[176:179], v[208:211], v[90:93]
	v_mfma_f32_16x16x32_bf16 v[82:85], v[168:171], v[216:219], v[82:85]
	v_mfma_f32_16x16x32_bf16 v[74:77], v[176:179], v[216:219], v[74:77]
	v_mfma_f32_16x16x32_bf16 v[70:73], v[168:171], v[232:235], v[70:73]
	v_mfma_f32_16x16x32_bf16 v[66:69], v[176:179], v[232:235], v[66:69]
	s_setprio 0
	s_barrier
	s_add_i32 s15, s60, s43
	v_lshl_add_u64 v[184:185], s[22:23], 0, v[138:139]
	s_mov_b32 m0, s15
	ds_read_b128 v[180:183], v147 offset:16384
	ds_read_b128 v[200:203], v147 offset:17408
	ds_read_b128 v[204:207], v147 offset:18432
	ds_read_b128 v[208:211], v147 offset:19456
	ds_read_b128 v[212:215], v147 offset:20480
	ds_read_b128 v[216:219], v147 offset:21504
	ds_read_b128 v[220:223], v147 offset:22528
	ds_read_b128 v[232:235], v147 offset:23552
	global_load_lds_dwordx4 v[184:185], off
	s_add_i32 m0, s15, 0x2000
	s_add_u32 s60, s22, 0x80000
	v_lshl_add_u64 v[236:237], s[22:23], 0, v[134:135]
	s_addc_u32 s61, s23, 0
	s_add_i32 s14, s14, s43
	global_load_lds_dwordx4 v[236:237], off
	v_lshl_add_u64 v[238:239], s[60:61], 0, v[138:139]
	s_mov_b32 m0, s14
	v_lshl_add_u64 v[240:241], s[40:41], 0, v[136:137]
	global_load_lds_dwordx4 v[238:239], off
	v_lshl_add_u64 v[238:239], s[60:61], 0, v[134:135]
	s_add_i32 m0, s14, 0x2000
	s_nop 0
	global_load_lds_dwordx4 v[238:239], off
	v_lshl_add_u64 v[238:239], s[40:41], 0, v[140:141]
	s_mov_b32 m0, s44
	s_nop 0
	global_load_lds_dwordx4 v[238:239], off
	s_mov_b32 m0, s45
	s_nop 0
	global_load_lds_dwordx4 v[240:241], off
	s_waitcnt vmcnt(8)
	s_waitcnt lgkmcnt(0)
	s_barrier
; #define PG8_STAGE(bufoff, gbase, voff) do { _Pragma("unroll") for (int _i = 0; _i < 2; ++_i) \
;         __builtin_amdgcn_global_load_lds((const unsigned*)((const char*)(gbase) + (voff)[_i]), (LAS unsigned*)(lds + (bufoff) + ldsw + _i * 8192), 16, 0, 0); } while (0)
; #define PG8_LDA(dst, b, h) do { _Pragma("unroll") for (int m = 0; m < 4; ++m) _Pragma("unroll") for (int k = 0; k < 2; ++k) dst[m][k] = *(const LAS bf16x8*)(lds + PG8_SA(b, h) + aoff + m * 2048 + k * 1024); } while (0)
; #define PG8_LDB(dst, b, h) do { _Pragma("unroll") for (int n = 0; n < 2; ++n) _Pragma("unroll") for (int k = 0; k < 2; ++k) dst[n][k] = *(const LAS bf16x8*)(lds + PG8_SB(b, h) + boff + n * 2048 + k * 1024); } while (0)
; #define PG8_MMA(ai, bj, At, Bt) do { __builtin_amdgcn_s_setprio(1); _Pragma("unroll") for (int m = 0; m < 4; ++m) _Pragma("unroll") for (int n = 0; n < 2; ++n) _Pragma("unroll") for (int k = 0; k < 2; ++k) \
;         acc[ai][bj][m][n] = __builtin_amdgcn_mfma_f32_16x16x32_bf16(Bt[n][k], At[m][k], acc[ai][bj][m][n], 0, 0, 0); __builtin_amdgcn_s_setprio(0); } while (0)
; #define PG8_WAIT_V(n) asm volatile("s_waitcnt vmcnt(" #n ")" ::: "memory")
; #define PG8_WAIT_L(n) asm volatile("s_waitcnt lgkmcnt(" #n ")" ::: "memory")
; #define PG8_BAR __builtin_amdgcn_s_barrier()
; #define PG8_SCHED __builtin_amdgcn_sched_barrier(0)
; template <class Epi, class Sched>
; __device__ __forceinline__ void gemm_phase(LAS unsigned char* lds, const Gemm g, const Sched& S, const Epi& E, const int tid, unsigned* last_sig = nullptr) {
;     ...
;             PG8_WAIT_V(8); PG8_WAIT_L(0); PG8_BAR; PG8_MMA(1, 0, At, B0); PG8_MMA(1, 1, At, B1); PG8_BAR; PG8_SCHED;
;             PG8_LDB(B0, 1, 0); PG8_LDB(B1, 1, 1); PG8_SCHED; PG8_LDA(At, 1, 0); PG8_STAGE(PG8_SA(0, 1), a2 + hstep, voffA);
;             PG8_WAIT_V(8); PG8_WAIT_L(0); PG8_BAR; PG8_MMA(0, 0, At, B0); PG8_MMA(0, 1, At, B1); PG8_BAR; PG8_SCHED;
	s_setprio 1
	s_waitcnt lgkmcnt(0)
	v_mfma_f32_16x16x32_bf16 v[62:65], v[130:133], v[180:183], v[62:65]
	v_mfma_f32_16x16x32_bf16 v[58:61], v[156:159], v[180:183], v[58:61]
	v_mfma_f32_16x16x32_bf16 v[54:57], v[130:133], v[204:207], v[54:57]
	v_mfma_f32_16x16x32_bf16 v[46:49], v[156:159], v[204:207], v[46:49]
	v_mfma_f32_16x16x32_bf16 v[38:41], v[130:133], v[212:215], v[38:41]
	v_mfma_f32_16x16x32_bf16 v[30:33], v[156:159], v[212:215], v[30:33]
	v_mfma_f32_16x16x32_bf16 v[22:25], v[130:133], v[220:223], v[22:25]
	v_mfma_f32_16x16x32_bf16 v[14:17], v[156:159], v[220:223], v[14:17]
	v_mfma_f32_16x16x32_bf16 v[62:65], v[152:155], v[200:203], v[62:65]
	v_mfma_f32_16x16x32_bf16 v[58:61], v[160:163], v[200:203], v[58:61]
	v_mfma_f32_16x16x32_bf16 v[54:57], v[152:155], v[208:211], v[54:57]
	v_mfma_f32_16x16x32_bf16 v[46:49], v[160:163], v[208:211], v[46:49]
	v_mfma_f32_16x16x32_bf16 v[38:41], v[152:155], v[216:219], v[38:41]
	v_mfma_f32_16x16x32_bf16 v[30:33], v[160:163], v[216:219], v[30:33]
	v_mfma_f32_16x16x32_bf16 v[22:25], v[152:155], v[232:235], v[22:25]
	v_mfma_f32_16x16x32_bf16 v[14:17], v[160:163], v[232:235], v[14:17]
	v_mfma_f32_16x16x32_bf16 v[50:53], v[164:167], v[180:183], v[50:53]
	v_mfma_f32_16x16x32_bf16 v[42:45], v[172:175], v[180:183], v[42:45]
	v_mfma_f32_16x16x32_bf16 v[34:37], v[164:167], v[204:207], v[34:37]
	v_mfma_f32_16x16x32_bf16 v[26:29], v[172:175], v[204:207], v[26:29]
	v_mfma_f32_16x16x32_bf16 v[18:21], v[164:167], v[212:215], v[18:21]
	v_mfma_f32_16x16x32_bf16 v[10:13], v[172:175], v[212:215], v[10:13]
	v_mfma_f32_16x16x32_bf16 v[6:9], v[164:167], v[220:223], v[6:9]
	v_mfma_f32_16x16x32_bf16 v[2:5], v[172:175], v[220:223], v[2:5]
	v_mfma_f32_16x16x32_bf16 v[50:53], v[168:171], v[200:203], v[50:53]
	v_mfma_f32_16x16x32_bf16 v[42:45], v[176:179], v[200:203], v[42:45]
	v_mfma_f32_16x16x32_bf16 v[34:37], v[168:171], v[208:211], v[34:37]
	v_mfma_f32_16x16x32_bf16 v[26:29], v[176:179], v[208:211], v[26:29]
	v_mfma_f32_16x16x32_bf16 v[18:21], v[168:171], v[216:219], v[18:21]
	v_mfma_f32_16x16x32_bf16 v[10:13], v[176:179], v[216:219], v[10:13]
	v_mfma_f32_16x16x32_bf16 v[6:9], v[168:171], v[232:235], v[6:9]
	v_mfma_f32_16x16x32_bf16 v[2:5], v[176:179], v[232:235], v[2:5]
	s_setprio 0
	s_barrier
	s_add_i32 s14, 0, 0x18000
	s_add_i32 s15, 0, 0x1c000
	v_add_u32_e32 v160, s14, v145
	v_add_u32_e32 v176, s15, v145
	ds_read_b128 v[130:133], v160
	ds_read_b128 v[152:155], v160 offset:1024
	ds_read_b128 v[156:159], v160 offset:2048
	ds_read_b128 v[160:163], v160 offset:3072
	ds_read_b128 v[164:167], v176
	ds_read_b128 v[168:171], v176 offset:1024
	ds_read_b128 v[172:175], v176 offset:2048
	ds_read_b128 v[176:179], v176 offset:3072
	s_add_u32 s40, s40, 0x80000
	s_addc_u32 s41, s41, 0
	s_mov_b32 m0, s46
	v_lshl_add_u64 v[242:243], s[40:41], 0, v[140:141]
	ds_read_b128 v[180:183], v147 offset:32768
	ds_read_b128 v[200:203], v147 offset:33792
	ds_read_b128 v[204:207], v147 offset:34816
	ds_read_b128 v[208:211], v147 offset:35840
	ds_read_b128 v[212:215], v147 offset:36864
	ds_read_b128 v[216:219], v147 offset:37888
	ds_read_b128 v[220:223], v147 offset:38912
	ds_read_b128 v[232:235], v147 offset:39936
	global_load_lds_dwordx4 v[242:243], off
	v_lshl_add_u64 v[242:243], s[40:41], 0, v[136:137]
	s_mov_b32 m0, s47
	s_nop 0
	global_load_lds_dwordx4 v[242:243], off
	s_waitcnt vmcnt(8)
	s_waitcnt lgkmcnt(0)
	s_barrier
	s_setprio 1
	s_waitcnt lgkmcnt(0)
	v_mfma_f32_16x16x32_bf16 v[126:129], v[130:133], v[180:183], v[126:129]
	v_mfma_f32_16x16x32_bf16 v[122:125], v[156:159], v[180:183], v[122:125]
	v_mfma_f32_16x16x32_bf16 v[118:121], v[130:133], v[204:207], v[118:121]
	v_mfma_f32_16x16x32_bf16 v[110:113], v[156:159], v[204:207], v[110:113]
	v_mfma_f32_16x16x32_bf16 v[102:105], v[130:133], v[212:215], v[102:105]
	v_mfma_f32_16x16x32_bf16 v[94:97], v[156:159], v[212:215], v[94:97]
	v_mfma_f32_16x16x32_bf16 v[86:89], v[130:133], v[220:223], v[86:89]
	v_mfma_f32_16x16x32_bf16 v[78:81], v[156:159], v[220:223], v[78:81]
	v_mfma_f32_16x16x32_bf16 v[126:129], v[152:155], v[200:203], v[126:129]
	v_mfma_f32_16x16x32_bf16 v[122:125], v[160:163], v[200:203], v[122:125]
	v_mfma_f32_16x16x32_bf16 v[118:121], v[152:155], v[208:211], v[118:121]
	v_mfma_f32_16x16x32_bf16 v[110:113], v[160:163], v[208:211], v[110:113]
	v_mfma_f32_16x16x32_bf16 v[102:105], v[152:155], v[216:219], v[102:105]
	v_mfma_f32_16x16x32_bf16 v[94:97], v[160:163], v[216:219], v[94:97]
	v_mfma_f32_16x16x32_bf16 v[86:89], v[152:155], v[232:235], v[86:89]
	v_mfma_f32_16x16x32_bf16 v[78:81], v[160:163], v[232:235], v[78:81]
	v_mfma_f32_16x16x32_bf16 v[114:117], v[164:167], v[180:183], v[114:117]
	v_mfma_f32_16x16x32_bf16 v[106:109], v[172:175], v[180:183], v[106:109]
	v_mfma_f32_16x16x32_bf16 v[98:101], v[164:167], v[204:207], v[98:101]
	v_mfma_f32_16x16x32_bf16 v[90:93], v[172:175], v[204:207], v[90:93]
	v_mfma_f32_16x16x32_bf16 v[82:85], v[164:167], v[212:215], v[82:85]
	v_mfma_f32_16x16x32_bf16 v[74:77], v[172:175], v[212:215], v[74:77]
	v_mfma_f32_16x16x32_bf16 v[70:73], v[164:167], v[220:223], v[70:73]
	v_mfma_f32_16x16x32_bf16 v[66:69], v[172:175], v[220:223], v[66:69]
	v_mfma_f32_16x16x32_bf16 v[114:117], v[168:171], v[200:203], v[114:117]
	v_mfma_f32_16x16x32_bf16 v[106:109], v[176:179], v[200:203], v[106:109]
	v_mfma_f32_16x16x32_bf16 v[98:101], v[168:171], v[208:211], v[98:101]
	v_mfma_f32_16x16x32_bf16 v[90:93], v[176:179], v[208:211], v[90:93]
	v_mfma_f32_16x16x32_bf16 v[82:85], v[168:171], v[216:219], v[82:85]
	v_mfma_f32_16x16x32_bf16 v[74:77], v[176:179], v[216:219], v[74:77]
	v_mfma_f32_16x16x32_bf16 v[70:73], v[168:171], v[232:235], v[70:73]
	v_mfma_f32_16x16x32_bf16 v[66:69], v[176:179], v[232:235], v[66:69]
	s_setprio 0
	s_barrier
; #define PG8_STAGE(bufoff, gbase, voff) do { _Pragma("unroll") for (int _i = 0; _i < 2; ++_i) \
;         __builtin_amdgcn_global_load_lds((const unsigned*)((const char*)(gbase) + (voff)[_i]), (LAS unsigned*)(lds + (bufoff) + ldsw + _i * 8192), 16, 0, 0); } while (0)
; #define PG8_LDA(dst, b, h) do { _Pragma("unroll") for (int m = 0; m < 4; ++m) _Pragma("unroll") for (int k = 0; k < 2; ++k) dst[m][k] = *(const LAS bf16x8*)(lds + PG8_SA(b, h) + aoff + m * 2048 + k * 1024); } while (0)
; #define PG8_MMA(ai, bj, At, Bt) do { __builtin_amdgcn_s_setprio(1); _Pragma("unroll") for (int m = 0; m < 4; ++m) _Pragma("unroll") for (int n = 0; n < 2; ++n) _Pragma("unroll") for (int k = 0; k < 2; ++k) \
;         acc[ai][bj][m][n] = __builtin_amdgcn_mfma_f32_16x16x32_bf16(Bt[n][k], At[m][k], acc[ai][bj][m][n], 0, 0, 0); __builtin_amdgcn_s_setprio(0); } while (0)
; #define PG8_WAIT_V(n) asm volatile("s_waitcnt vmcnt(" #n ")" ::: "memory")
; #define PG8_WAIT_L(n) asm volatile("s_waitcnt lgkmcnt(" #n ")" ::: "memory")
; #define PG8_BAR __builtin_amdgcn_s_barrier()
; #define PG8_SCHED __builtin_amdgcn_sched_barrier(0)
; template <class Epi, class Sched>
; __device__ __forceinline__ void gemm_phase(LAS unsigned char* lds, const Gemm g, const Sched& S, const Epi& E, const int tid, unsigned* last_sig = nullptr) {
;     ...
;             PG8_LDA(At, 1, 1); PG8_STAGE(PG8_SB(1, 0), b3, voffB); PG8_STAGE(PG8_SB(1, 1), b3 + hstep, voffB); PG8_STAGE(PG8_SA(1, 0), a3, voffA);
;             PG8_WAIT_V(8); PG8_WAIT_L(0); PG8_BAR; PG8_MMA(1, 0, At, B0); PG8_MMA(1, 1, At, B1); PG8_BAR; PG8_SCHED;
;         }
;         if (wr == 0) PG8_BAR;
;         E(acc, cur, wr, wc, fr, fq);
;         if (!has_next) break;
	s_add_i32 s14, s14, s43
	v_lshl_add_u64 v[184:185], v[184:185], 0, s[34:35]
	s_mov_b32 m0, s14
	ds_read_b128 v[180:183], v147 offset:49152
	ds_read_b128 v[200:203], v147 offset:50176
	ds_read_b128 v[204:207], v147 offset:51200
	ds_read_b128 v[208:211], v147 offset:52224
	ds_read_b128 v[212:215], v147 offset:53248
	ds_read_b128 v[216:219], v147 offset:54272
	ds_read_b128 v[220:223], v147 offset:55296
	ds_read_b128 v[232:235], v147 offset:56320
	global_load_lds_dwordx4 v[184:185], off
	s_add_i32 m0, s14, 0x2000
	s_add_u32 s22, s22, 0x80080
	v_lshl_add_u64 v[184:185], v[236:237], 0, s[34:35]
	s_addc_u32 s23, s23, 0
	s_add_i32 s14, s15, s43
	global_load_lds_dwordx4 v[184:185], off
	v_lshl_add_u64 v[184:185], s[22:23], 0, v[138:139]
	s_mov_b32 m0, s14
	s_nop 0
	global_load_lds_dwordx4 v[184:185], off
	v_lshl_add_u64 v[184:185], s[22:23], 0, v[134:135]
	s_add_i32 m0, s14, 0x2000
	s_nop 0
	global_load_lds_dwordx4 v[184:185], off
	v_lshl_add_u64 v[184:185], v[238:239], 0, s[34:35]
	s_mov_b32 m0, s49
	s_nop 0
	global_load_lds_dwordx4 v[184:185], off
	v_lshl_add_u64 v[184:185], v[240:241], 0, s[34:35]
	s_mov_b32 m0, s50
	s_nop 0
	global_load_lds_dwordx4 v[184:185], off
	s_waitcnt vmcnt(8)
	s_waitcnt lgkmcnt(0)
	s_barrier
	s_setprio 1
	s_waitcnt lgkmcnt(0)
	v_mfma_f32_16x16x32_bf16 v[62:65], v[130:133], v[180:183], v[62:65]
	v_mfma_f32_16x16x32_bf16 v[58:61], v[156:159], v[180:183], v[58:61]
	v_mfma_f32_16x16x32_bf16 v[54:57], v[130:133], v[204:207], v[54:57]
	v_mfma_f32_16x16x32_bf16 v[46:49], v[156:159], v[204:207], v[46:49]
	v_mfma_f32_16x16x32_bf16 v[38:41], v[130:133], v[212:215], v[38:41]
	v_mfma_f32_16x16x32_bf16 v[30:33], v[156:159], v[212:215], v[30:33]
	v_mfma_f32_16x16x32_bf16 v[22:25], v[130:133], v[220:223], v[22:25]
	v_mfma_f32_16x16x32_bf16 v[14:17], v[156:159], v[220:223], v[14:17]
	v_mfma_f32_16x16x32_bf16 v[62:65], v[152:155], v[200:203], v[62:65]
	v_mfma_f32_16x16x32_bf16 v[58:61], v[160:163], v[200:203], v[58:61]
	v_mfma_f32_16x16x32_bf16 v[54:57], v[152:155], v[208:211], v[54:57]
	v_mfma_f32_16x16x32_bf16 v[46:49], v[160:163], v[208:211], v[46:49]
	v_mfma_f32_16x16x32_bf16 v[38:41], v[152:155], v[216:219], v[38:41]
	v_mfma_f32_16x16x32_bf16 v[30:33], v[160:163], v[216:219], v[30:33]
	v_mfma_f32_16x16x32_bf16 v[22:25], v[152:155], v[232:235], v[22:25]
	v_mfma_f32_16x16x32_bf16 v[14:17], v[160:163], v[232:235], v[14:17]
	v_mfma_f32_16x16x32_bf16 v[50:53], v[164:167], v[180:183], v[50:53]
	v_mfma_f32_16x16x32_bf16 v[42:45], v[172:175], v[180:183], v[42:45]
	v_mfma_f32_16x16x32_bf16 v[34:37], v[164:167], v[204:207], v[34:37]
	v_mfma_f32_16x16x32_bf16 v[26:29], v[172:175], v[204:207], v[26:29]
	v_mfma_f32_16x16x32_bf16 v[18:21], v[164:167], v[212:215], v[18:21]
	v_mfma_f32_16x16x32_bf16 v[10:13], v[172:175], v[212:215], v[10:13]
	v_mfma_f32_16x16x32_bf16 v[6:9], v[164:167], v[220:223], v[6:9]
	v_mfma_f32_16x16x32_bf16 v[2:5], v[172:175], v[220:223], v[2:5]
	v_mfma_f32_16x16x32_bf16 v[50:53], v[168:171], v[200:203], v[50:53]
	v_mfma_f32_16x16x32_bf16 v[42:45], v[176:179], v[200:203], v[42:45]
	v_mfma_f32_16x16x32_bf16 v[34:37], v[168:171], v[208:211], v[34:37]
	v_mfma_f32_16x16x32_bf16 v[26:29], v[176:179], v[208:211], v[26:29]
	v_mfma_f32_16x16x32_bf16 v[18:21], v[168:171], v[216:219], v[18:21]
	v_mfma_f32_16x16x32_bf16 v[10:13], v[176:179], v[216:219], v[10:13]
	v_mfma_f32_16x16x32_bf16 v[6:9], v[168:171], v[232:235], v[6:9]
	v_mfma_f32_16x16x32_bf16 v[2:5], v[176:179], v[232:235], v[2:5]
	s_setprio 0
	s_barrier
	s_add_i32 s59, s59, 2
	s_add_u32 s20, s20, 0x100
	s_addc_u32 s21, s21, 0
	s_add_u32 s57, s57, 0x100
	s_addc_u32 s58, s58, 0
	s_cmp_gt_u32 s59, 29
	s_cbranch_scc0 .LBB0_172
	s_and_b64 vcc, exec, s[8:9]
	s_cbranch_vccnz .LBB0_177
	s_cmp_gt_i32 s54, 3
	s_mov_b64 s[20:21], -1
	s_cbranch_scc1 .LBB0_178

; #define PG8_STAGE(bufoff, gbase, voff) do { _Pragma("unroll") for (int _i = 0; _i < 2; ++_i) \
;         __builtin_amdgcn_global_load_lds((const unsigned*)((const char*)(gbase) + (voff)[_i]), (LAS unsigned*)(lds + (bufoff) + ldsw + _i * 8192), 16, 0, 0); } while (0)
; #define PG8_LDA(dst, b, h) do { _Pragma("unroll") for (int m = 0; m < 4; ++m) _Pragma("unroll") for (int k = 0; k < 2; ++k) dst[m][k] = *(const LAS bf16x8*)(lds + PG8_SA(b, h) + aoff + m * 2048 + k * 1024); } while (0)
; #define PG8_LDB(dst, b, h) do { _Pragma("unroll") for (int n = 0; n < 2; ++n) _Pragma("unroll") for (int k = 0; k < 2; ++k) dst[n][k] = *(const LAS bf16x8*)(lds + PG8_SB(b, h) + boff + n * 2048 + k * 1024); } while (0)
; #define PG8_MMA(ai, bj, At, Bt) do { __builtin_amdgcn_s_setprio(1); _Pragma("unroll") for (int m = 0; m < 4; ++m) _Pragma("unroll") for (int n = 0; n < 2; ++n) _Pragma("unroll") for (int k = 0; k < 2; ++k) \
;         acc[ai][bj][m][n] = __builtin_amdgcn_mfma_f32_16x16x32_bf16(Bt[n][k], At[m][k], acc[ai][bj][m][n], 0, 0, 0); __builtin_amdgcn_s_setprio(0); } while (0)
; #define PG8_WAIT_V(n) asm volatile("s_waitcnt vmcnt(" #n ")" ::: "memory")
; #define PG8_WAIT_L(n) asm volatile("s_waitcnt lgkmcnt(" #n ")" ::: "memory")
; #define PG8_BAR __builtin_amdgcn_s_barrier()
; template <class Epi, class Sched>
; __device__ __forceinline__ void gemm_phase(LAS unsigned char* lds, const Gemm g, const Sched& S, const Epi& E, const int tid, unsigned* last_sig = nullptr) {
;     ...
;         for (int t = 0; t < nt; t += 2) {
;             const bool last = (t == nt - 2);
;             const char* a1 = cA + (size_t)(t + 1) * kstep;
;             const char* a2 = last ? nA : cA + (size_t)(t + 2) * kstep; const char* b2 = last ? nB : cB + (size_t)(t + 2) * kstep;
;             const char* a3 = a2 + kstep; const char* b3 = b2 + kstep;
;             PG8_LDB(B0, 0, 0); PG8_LDB(B1, 0, 1); PG8_SCHED; PG8_LDA(At, 0, 0); PG8_STAGE(PG8_SA(1, 1), a1 + hstep, voffA);
;             PG8_WAIT_V(8); PG8_WAIT_L(0); PG8_BAR; PG8_MMA(0, 0, At, B0); PG8_MMA(0, 1, At, B1); PG8_BAR; PG8_SCHED;
;             PG8_LDA(At, 0, 1); PG8_STAGE(PG8_SB(0, 0), b2, voffB); PG8_STAGE(PG8_SB(0, 1), b2 + hstep, voffB); PG8_STAGE(PG8_SA(0, 0), a2, voffA);
;             PG8_WAIT_V(8); PG8_WAIT_L(0); PG8_BAR; PG8_MMA(1, 0, At, B0); PG8_MMA(1, 1, At, B1); PG8_BAR; PG8_SCHED;
.LBB0_334:
	s_add_u32 s6, s42, s4
	s_addc_u32 s7, s43, s5
	s_add_u32 s6, s6, 0x4cd67100
	s_addc_u32 s7, s7, 0
	s_add_u32 s14, s22, s4
	s_addc_u32 s15, s23, s5
	s_add_i32 s31, 0, 0x10000
	s_cmpk_eq_i32 s4, 0xf00
	s_cselect_b32 s9, s41, s7
	s_cselect_b32 s8, s40, s6
	v_add_u32_e32 v55, s31, v53
	s_cselect_b32 s7, s1, s15
	s_cselect_b32 s6, s0, s14
	s_add_i32 s14, 0, 0x14000
	ds_read_b128 v[148:151], v55
	ds_read_b128 v[154:157], v55 offset:1024
	ds_read_b128 v[158:161], v55 offset:2048
	ds_read_b128 v[162:165], v55 offset:3072
	v_add_u32_e32 v55, s14, v53
	ds_read_b128 v[166:169], v55
	ds_read_b128 v[170:173], v55 offset:1024
	ds_read_b128 v[174:177], v55 offset:2048
	ds_read_b128 v[178:181], v55 offset:3072
	v_lshl_add_u64 v[56:57], v[48:49], 0, s[4:5]
	s_add_i32 m0, s12, 0xc000
	ds_read_b128 v[182:185], v54
	ds_read_b128 v[200:203], v54 offset:1024
	ds_read_b128 v[204:207], v54 offset:2048
	ds_read_b128 v[208:211], v54 offset:3072
	ds_read_b128 v[212:215], v54 offset:4096
	ds_read_b128 v[216:219], v54 offset:5120
	ds_read_b128 v[220:223], v54 offset:6144
	ds_read_b128 v[232:235], v54 offset:7168
	global_load_lds_dwordx4 v[56:57], off
	v_lshl_add_u64 v[56:57], v[50:51], 0, s[4:5]
	s_add_i32 m0, s12, 0xe000
	s_nop 0
	global_load_lds_dwordx4 v[56:57], off
	s_waitcnt vmcnt(8)
	s_waitcnt lgkmcnt(0)
	s_barrier
	s_setprio 1
	s_waitcnt lgkmcnt(0)
	v_mfma_f32_16x16x32_bf16 v[142:145], v[148:151], v[182:185], v[142:145]
	v_mfma_f32_16x16x32_bf16 v[138:141], v[158:161], v[182:185], v[138:141]
	v_mfma_f32_16x16x32_bf16 v[126:129], v[148:151], v[204:207], v[126:129]
	v_mfma_f32_16x16x32_bf16 v[122:125], v[158:161], v[204:207], v[122:125]
	v_mfma_f32_16x16x32_bf16 v[110:113], v[148:151], v[212:215], v[110:113]
	v_mfma_f32_16x16x32_bf16 v[106:109], v[158:161], v[212:215], v[106:109]
	v_mfma_f32_16x16x32_bf16 v[94:97], v[148:151], v[220:223], v[94:97]
	v_mfma_f32_16x16x32_bf16 v[90:93], v[158:161], v[220:223], v[90:93]
	v_mfma_f32_16x16x32_bf16 v[142:145], v[154:157], v[200:203], v[142:145]
	v_mfma_f32_16x16x32_bf16 v[138:141], v[162:165], v[200:203], v[138:141]
	v_mfma_f32_16x16x32_bf16 v[126:129], v[154:157], v[208:211], v[126:129]
	v_mfma_f32_16x16x32_bf16 v[122:125], v[162:165], v[208:211], v[122:125]
	v_mfma_f32_16x16x32_bf16 v[110:113], v[154:157], v[216:219], v[110:113]
	v_mfma_f32_16x16x32_bf16 v[106:109], v[162:165], v[216:219], v[106:109]
	v_mfma_f32_16x16x32_bf16 v[94:97], v[154:157], v[232:235], v[94:97]
	v_mfma_f32_16x16x32_bf16 v[90:93], v[162:165], v[232:235], v[90:93]
	v_mfma_f32_16x16x32_bf16 v[134:137], v[166:169], v[182:185], v[134:137]
	v_mfma_f32_16x16x32_bf16 v[130:133], v[174:177], v[182:185], v[130:133]
	v_mfma_f32_16x16x32_bf16 v[118:121], v[166:169], v[204:207], v[118:121]
	v_mfma_f32_16x16x32_bf16 v[114:117], v[174:177], v[204:207], v[114:117]
	v_mfma_f32_16x16x32_bf16 v[102:105], v[166:169], v[212:215], v[102:105]
	v_mfma_f32_16x16x32_bf16 v[98:101], v[174:177], v[212:215], v[98:101]
	v_mfma_f32_16x16x32_bf16 v[86:89], v[166:169], v[220:223], v[86:89]
	v_mfma_f32_16x16x32_bf16 v[82:85], v[174:177], v[220:223], v[82:85]
	v_mfma_f32_16x16x32_bf16 v[134:137], v[170:173], v[200:203], v[134:137]
	v_mfma_f32_16x16x32_bf16 v[130:133], v[178:181], v[200:203], v[130:133]
	v_mfma_f32_16x16x32_bf16 v[118:121], v[170:173], v[208:211], v[118:121]
	v_mfma_f32_16x16x32_bf16 v[114:117], v[178:181], v[208:211], v[114:117]
	v_mfma_f32_16x16x32_bf16 v[102:105], v[170:173], v[216:219], v[102:105]
	v_mfma_f32_16x16x32_bf16 v[98:101], v[178:181], v[216:219], v[98:101]
	v_mfma_f32_16x16x32_bf16 v[86:89], v[170:173], v[232:235], v[86:89]
	v_mfma_f32_16x16x32_bf16 v[82:85], v[178:181], v[232:235], v[82:85]
	s_setprio 0
	s_barrier
	s_add_i32 s15, s31, s11
	v_lshl_add_u64 v[236:237], s[6:7], 0, v[186:187]
	s_mov_b32 m0, s15
	ds_read_b128 v[182:185], v54 offset:16384
	ds_read_b128 v[200:203], v54 offset:17408
	ds_read_b128 v[204:207], v54 offset:18432
	ds_read_b128 v[208:211], v54 offset:19456
	ds_read_b128 v[212:215], v54 offset:20480
	ds_read_b128 v[216:219], v54 offset:21504
	ds_read_b128 v[220:223], v54 offset:22528
	ds_read_b128 v[232:235], v54 offset:23552
	global_load_lds_dwordx4 v[236:237], off
	s_add_i32 m0, s15, 0x2000
	s_add_u32 s38, s6, 0x80000
	v_lshl_add_u64 v[238:239], s[6:7], 0, v[38:39]
	s_addc_u32 s39, s7, 0
	s_add_i32 s14, s14, s11
	global_load_lds_dwordx4 v[238:239], off
	v_lshl_add_u64 v[56:57], s[38:39], 0, v[186:187]
	s_mov_b32 m0, s14
	v_lshl_add_u64 v[240:241], s[8:9], 0, v[46:47]
	global_load_lds_dwordx4 v[56:57], off
	v_lshl_add_u64 v[56:57], s[38:39], 0, v[38:39]
	s_add_i32 m0, s14, 0x2000
	v_lshl_add_u64 v[242:243], s[8:9], 0, v[40:41]
	global_load_lds_dwordx4 v[56:57], off
	s_mov_b32 m0, s12
	s_nop 0
	global_load_lds_dwordx4 v[240:241], off
	s_mov_b32 m0, s13
	s_nop 0
	global_load_lds_dwordx4 v[242:243], off
	s_waitcnt vmcnt(8)
	s_waitcnt lgkmcnt(0)
	s_barrier
; #define PG8_STAGE(bufoff, gbase, voff) do { _Pragma("unroll") for (int _i = 0; _i < 2; ++_i) \
;         __builtin_amdgcn_global_load_lds((const unsigned*)((const char*)(gbase) + (voff)[_i]), (LAS unsigned*)(lds + (bufoff) + ldsw + _i * 8192), 16, 0, 0); } while (0)
; #define PG8_LDA(dst, b, h) do { _Pragma("unroll") for (int m = 0; m < 4; ++m) _Pragma("unroll") for (int k = 0; k < 2; ++k) dst[m][k] = *(const LAS bf16x8*)(lds + PG8_SA(b, h) + aoff + m * 2048 + k * 1024); } while (0)
; #define PG8_LDB(dst, b, h) do { _Pragma("unroll") for (int n = 0; n < 2; ++n) _Pragma("unroll") for (int k = 0; k < 2; ++k) dst[n][k] = *(const LAS bf16x8*)(lds + PG8_SB(b, h) + boff + n * 2048 + k * 1024); } while (0)
; #define PG8_MMA(ai, bj, At, Bt) do { __builtin_amdgcn_s_setprio(1); _Pragma("unroll") for (int m = 0; m < 4; ++m) _Pragma("unroll") for (int n = 0; n < 2; ++n) _Pragma("unroll") for (int k = 0; k < 2; ++k) \
;         acc[ai][bj][m][n] = __builtin_amdgcn_mfma_f32_16x16x32_bf16(Bt[n][k], At[m][k], acc[ai][bj][m][n], 0, 0, 0); __builtin_amdgcn_s_setprio(0); } while (0)
; #define PG8_WAIT_V(n) asm volatile("s_waitcnt vmcnt(" #n ")" ::: "memory")
; #define PG8_WAIT_L(n) asm volatile("s_waitcnt lgkmcnt(" #n ")" ::: "memory")
; #define PG8_BAR __builtin_amdgcn_s_barrier()
; #define PG8_SCHED __builtin_amdgcn_sched_barrier(0)
; template <class Epi, class Sched>
; __device__ __forceinline__ void gemm_phase(LAS unsigned char* lds, const Gemm g, const Sched& S, const Epi& E, const int tid, unsigned* last_sig = nullptr) {
;     ...
;             PG8_WAIT_V(8); PG8_WAIT_L(0); PG8_BAR; PG8_MMA(1, 0, At, B0); PG8_MMA(1, 1, At, B1); PG8_BAR; PG8_SCHED;
;             PG8_LDB(B0, 1, 0); PG8_LDB(B1, 1, 1); PG8_SCHED; PG8_LDA(At, 1, 0); PG8_STAGE(PG8_SA(0, 1), a2 + hstep, voffA);
;             PG8_WAIT_V(8); PG8_WAIT_L(0); PG8_BAR; PG8_MMA(0, 0, At, B0); PG8_MMA(0, 1, At, B1); PG8_BAR; PG8_SCHED;
	s_setprio 1
	s_waitcnt lgkmcnt(0)
	v_mfma_f32_16x16x32_bf16 v[78:81], v[148:151], v[182:185], v[78:81]
	v_mfma_f32_16x16x32_bf16 v[74:77], v[158:161], v[182:185], v[74:77]
	v_mfma_f32_16x16x32_bf16 v[62:65], v[148:151], v[204:207], v[62:65]
	v_mfma_f32_16x16x32_bf16 v[56:59], v[158:161], v[204:207], v[58:61]
	v_mfma_f32_16x16x32_bf16 v[30:33], v[148:151], v[212:215], v[30:33]
	v_mfma_f32_16x16x32_bf16 v[26:29], v[158:161], v[212:215], v[26:29]
	v_mfma_f32_16x16x32_bf16 v[14:17], v[148:151], v[220:223], v[14:17]
	v_mfma_f32_16x16x32_bf16 v[10:13], v[158:161], v[220:223], v[10:13]
	v_mfma_f32_16x16x32_bf16 v[78:81], v[154:157], v[200:203], v[78:81]
	v_mfma_f32_16x16x32_bf16 v[74:77], v[162:165], v[200:203], v[74:77]
	v_mfma_f32_16x16x32_bf16 v[62:65], v[154:157], v[208:211], v[62:65]
	v_mfma_f32_16x16x32_bf16 v[56:59], v[162:165], v[208:211], v[56:59]
	v_mfma_f32_16x16x32_bf16 v[30:33], v[154:157], v[216:219], v[30:33]
	v_mfma_f32_16x16x32_bf16 v[26:29], v[162:165], v[216:219], v[26:29]
	v_mfma_f32_16x16x32_bf16 v[14:17], v[154:157], v[232:235], v[14:17]
	v_mfma_f32_16x16x32_bf16 v[10:13], v[162:165], v[232:235], v[10:13]
	v_mfma_f32_16x16x32_bf16 v[70:73], v[166:169], v[182:185], v[70:73]
	v_mfma_f32_16x16x32_bf16 v[66:69], v[174:177], v[182:185], v[66:69]
	v_mfma_f32_16x16x32_bf16 v[42:45], v[166:169], v[204:207], v[42:45]
	v_mfma_f32_16x16x32_bf16 v[34:37], v[174:177], v[204:207], v[34:37]
	v_mfma_f32_16x16x32_bf16 v[22:25], v[166:169], v[212:215], v[22:25]
	v_mfma_f32_16x16x32_bf16 v[18:21], v[174:177], v[212:215], v[18:21]
	v_mfma_f32_16x16x32_bf16 v[6:9], v[166:169], v[220:223], v[6:9]
	v_mfma_f32_16x16x32_bf16 v[2:5], v[174:177], v[220:223], v[2:5]
	v_mfma_f32_16x16x32_bf16 v[70:73], v[170:173], v[200:203], v[70:73]
	v_mfma_f32_16x16x32_bf16 v[66:69], v[178:181], v[200:203], v[66:69]
	v_mfma_f32_16x16x32_bf16 v[42:45], v[170:173], v[208:211], v[42:45]
	v_mfma_f32_16x16x32_bf16 v[34:37], v[178:181], v[208:211], v[34:37]
	v_mfma_f32_16x16x32_bf16 v[22:25], v[170:173], v[216:219], v[22:25]
	v_mfma_f32_16x16x32_bf16 v[18:21], v[178:181], v[216:219], v[18:21]
	v_mfma_f32_16x16x32_bf16 v[6:9], v[170:173], v[232:235], v[6:9]
	v_mfma_f32_16x16x32_bf16 v[2:5], v[178:181], v[232:235], v[2:5]
	s_setprio 0
	s_barrier
	s_add_i32 s14, 0, 0x18000
	v_add_u32_e32 v55, s14, v53
	s_add_i32 s15, 0, 0x1c000
	ds_read_b128 v[148:151], v55
	ds_read_b128 v[154:157], v55 offset:1024
	ds_read_b128 v[158:161], v55 offset:2048
	ds_read_b128 v[162:165], v55 offset:3072
	v_add_u32_e32 v55, s15, v53
	ds_read_b128 v[166:169], v55
	ds_read_b128 v[170:173], v55 offset:1024
	ds_read_b128 v[174:177], v55 offset:2048
	ds_read_b128 v[178:181], v55 offset:3072
	s_add_u32 s8, s8, 0x80000
	s_addc_u32 s9, s9, 0
	s_mov_b32 m0, s16
	v_lshl_add_u64 v[60:61], s[8:9], 0, v[46:47]
	ds_read_b128 v[182:185], v54 offset:32768
	ds_read_b128 v[200:203], v54 offset:33792
	ds_read_b128 v[204:207], v54 offset:34816
	ds_read_b128 v[208:211], v54 offset:35840
	ds_read_b128 v[212:215], v54 offset:36864
	ds_read_b128 v[216:219], v54 offset:37888
	ds_read_b128 v[220:223], v54 offset:38912
	ds_read_b128 v[232:235], v54 offset:39936
	global_load_lds_dwordx4 v[60:61], off
	v_lshl_add_u64 v[60:61], s[8:9], 0, v[40:41]
	s_mov_b32 m0, s17
	s_nop 0
	global_load_lds_dwordx4 v[60:61], off
	s_waitcnt vmcnt(8)
	s_waitcnt lgkmcnt(0)
	s_barrier
	s_setprio 1
	s_waitcnt lgkmcnt(0)
	v_mfma_f32_16x16x32_bf16 v[142:145], v[148:151], v[182:185], v[142:145]
	v_mfma_f32_16x16x32_bf16 v[138:141], v[158:161], v[182:185], v[138:141]
	v_mfma_f32_16x16x32_bf16 v[126:129], v[148:151], v[204:207], v[126:129]
	v_mfma_f32_16x16x32_bf16 v[122:125], v[158:161], v[204:207], v[122:125]
	v_mfma_f32_16x16x32_bf16 v[110:113], v[148:151], v[212:215], v[110:113]
	v_mfma_f32_16x16x32_bf16 v[106:109], v[158:161], v[212:215], v[106:109]
	v_mfma_f32_16x16x32_bf16 v[94:97], v[148:151], v[220:223], v[94:97]
	v_mfma_f32_16x16x32_bf16 v[90:93], v[158:161], v[220:223], v[90:93]
	v_mfma_f32_16x16x32_bf16 v[142:145], v[154:157], v[200:203], v[142:145]
	v_mfma_f32_16x16x32_bf16 v[138:141], v[162:165], v[200:203], v[138:141]
	v_mfma_f32_16x16x32_bf16 v[126:129], v[154:157], v[208:211], v[126:129]
	v_mfma_f32_16x16x32_bf16 v[122:125], v[162:165], v[208:211], v[122:125]
	v_mfma_f32_16x16x32_bf16 v[110:113], v[154:157], v[216:219], v[110:113]
	v_mfma_f32_16x16x32_bf16 v[106:109], v[162:165], v[216:219], v[106:109]
	v_mfma_f32_16x16x32_bf16 v[94:97], v[154:157], v[232:235], v[94:97]
	v_mfma_f32_16x16x32_bf16 v[90:93], v[162:165], v[232:235], v[90:93]
	v_mfma_f32_16x16x32_bf16 v[134:137], v[166:169], v[182:185], v[134:137]
	v_mfma_f32_16x16x32_bf16 v[130:133], v[174:177], v[182:185], v[130:133]
	v_mfma_f32_16x16x32_bf16 v[118:121], v[166:169], v[204:207], v[118:121]
	v_mfma_f32_16x16x32_bf16 v[114:117], v[174:177], v[204:207], v[114:117]
	v_mfma_f32_16x16x32_bf16 v[102:105], v[166:169], v[212:215], v[102:105]
	v_mfma_f32_16x16x32_bf16 v[98:101], v[174:177], v[212:215], v[98:101]
	v_mfma_f32_16x16x32_bf16 v[86:89], v[166:169], v[220:223], v[86:89]
	v_mfma_f32_16x16x32_bf16 v[82:85], v[174:177], v[220:223], v[82:85]
	v_mfma_f32_16x16x32_bf16 v[134:137], v[170:173], v[200:203], v[134:137]
	v_mfma_f32_16x16x32_bf16 v[130:133], v[178:181], v[200:203], v[130:133]
	v_mfma_f32_16x16x32_bf16 v[118:121], v[170:173], v[208:211], v[118:121]
	v_mfma_f32_16x16x32_bf16 v[114:117], v[178:181], v[208:211], v[114:117]
	v_mfma_f32_16x16x32_bf16 v[102:105], v[170:173], v[216:219], v[102:105]
	v_mfma_f32_16x16x32_bf16 v[98:101], v[178:181], v[216:219], v[98:101]
	v_mfma_f32_16x16x32_bf16 v[86:89], v[170:173], v[232:235], v[86:89]
	v_mfma_f32_16x16x32_bf16 v[82:85], v[178:181], v[232:235], v[82:85]
	s_setprio 0
	s_barrier
; #define PG8_STAGE(bufoff, gbase, voff) do { _Pragma("unroll") for (int _i = 0; _i < 2; ++_i) \
;         __builtin_amdgcn_global_load_lds((const unsigned*)((const char*)(gbase) + (voff)[_i]), (LAS unsigned*)(lds + (bufoff) + ldsw + _i * 8192), 16, 0, 0); } while (0)
; #define PG8_LDA(dst, b, h) do { _Pragma("unroll") for (int m = 0; m < 4; ++m) _Pragma("unroll") for (int k = 0; k < 2; ++k) dst[m][k] = *(const LAS bf16x8*)(lds + PG8_SA(b, h) + aoff + m * 2048 + k * 1024); } while (0)
; #define PG8_MMA(ai, bj, At, Bt) do { __builtin_amdgcn_s_setprio(1); _Pragma("unroll") for (int m = 0; m < 4; ++m) _Pragma("unroll") for (int n = 0; n < 2; ++n) _Pragma("unroll") for (int k = 0; k < 2; ++k) \
;         acc[ai][bj][m][n] = __builtin_amdgcn_mfma_f32_16x16x32_bf16(Bt[n][k], At[m][k], acc[ai][bj][m][n], 0, 0, 0); __builtin_amdgcn_s_setprio(0); } while (0)
; #define PG8_WAIT_V(n) asm volatile("s_waitcnt vmcnt(" #n ")" ::: "memory")
; #define PG8_WAIT_L(n) asm volatile("s_waitcnt lgkmcnt(" #n ")" ::: "memory")
; #define PG8_BAR __builtin_amdgcn_s_barrier()
; #define PG8_SCHED __builtin_amdgcn_sched_barrier(0)
; template <class Epi, class Sched>
; __device__ __forceinline__ void gemm_phase(LAS unsigned char* lds, const Gemm g, const Sched& S, const Epi& E, const int tid, unsigned* last_sig = nullptr) {
;     ...
;             PG8_LDA(At, 1, 1); PG8_STAGE(PG8_SB(1, 0), b3, voffB); PG8_STAGE(PG8_SB(1, 1), b3 + hstep, voffB); PG8_STAGE(PG8_SA(1, 0), a3, voffA);
;             PG8_WAIT_V(8); PG8_WAIT_L(0); PG8_BAR; PG8_MMA(1, 0, At, B0); PG8_MMA(1, 1, At, B1); PG8_BAR; PG8_SCHED;
;         }
;         if (wr == 0) PG8_BAR;
;         E(acc, cur, wr, wc, fr, fq);
;         if (!has_next) break;
	s_add_i32 s8, s14, s11
	v_lshl_add_u64 v[60:61], v[236:237], 0, s[34:35]
	s_mov_b32 m0, s8
	ds_read_b128 v[182:185], v54 offset:49152
	ds_read_b128 v[200:203], v54 offset:50176
	ds_read_b128 v[204:207], v54 offset:51200
	ds_read_b128 v[208:211], v54 offset:52224
	ds_read_b128 v[212:215], v54 offset:53248
	ds_read_b128 v[216:219], v54 offset:54272
	ds_read_b128 v[220:223], v54 offset:55296
	ds_read_b128 v[232:235], v54 offset:56320
	global_load_lds_dwordx4 v[60:61], off
	s_add_i32 m0, s8, 0x2000
	s_add_u32 s6, s6, 0x80080
	v_lshl_add_u64 v[60:61], v[238:239], 0, s[34:35]
	s_addc_u32 s7, s7, 0
	s_add_i32 s8, s15, s11
	global_load_lds_dwordx4 v[60:61], off
	v_lshl_add_u64 v[60:61], s[6:7], 0, v[186:187]
	s_mov_b32 m0, s8
	s_nop 0
	global_load_lds_dwordx4 v[60:61], off
	v_lshl_add_u64 v[60:61], s[6:7], 0, v[38:39]
	s_add_i32 m0, s8, 0x2000
	s_nop 0
	global_load_lds_dwordx4 v[60:61], off
	v_lshl_add_u64 v[60:61], v[240:241], 0, s[34:35]
	s_mov_b32 m0, s20
	s_nop 0
	global_load_lds_dwordx4 v[60:61], off
	v_lshl_add_u64 v[60:61], v[242:243], 0, s[34:35]
	s_mov_b32 m0, s21
	s_nop 0
	global_load_lds_dwordx4 v[60:61], off
	s_waitcnt vmcnt(8)
	s_waitcnt lgkmcnt(0)
	s_barrier
	s_setprio 1
	s_waitcnt lgkmcnt(0)
	v_mfma_f32_16x16x32_bf16 v[78:81], v[148:151], v[182:185], v[78:81]
	v_mfma_f32_16x16x32_bf16 v[74:77], v[158:161], v[182:185], v[74:77]
	v_mfma_f32_16x16x32_bf16 v[60:63], v[148:151], v[204:207], v[62:65]
	v_mfma_f32_16x16x32_bf16 v[56:59], v[158:161], v[204:207], v[56:59]
	v_mfma_f32_16x16x32_bf16 v[30:33], v[148:151], v[212:215], v[30:33]
	v_mfma_f32_16x16x32_bf16 v[26:29], v[158:161], v[212:215], v[26:29]
	v_mfma_f32_16x16x32_bf16 v[14:17], v[148:151], v[220:223], v[14:17]
	v_mfma_f32_16x16x32_bf16 v[10:13], v[158:161], v[220:223], v[10:13]
	v_mfma_f32_16x16x32_bf16 v[78:81], v[154:157], v[200:203], v[78:81]
	v_mfma_f32_16x16x32_bf16 v[74:77], v[162:165], v[200:203], v[74:77]
	v_mfma_f32_16x16x32_bf16 v[62:65], v[154:157], v[208:211], v[60:63]
	v_mfma_f32_16x16x32_bf16 v[58:61], v[162:165], v[208:211], v[56:59]
	v_mfma_f32_16x16x32_bf16 v[30:33], v[154:157], v[216:219], v[30:33]
	v_mfma_f32_16x16x32_bf16 v[26:29], v[162:165], v[216:219], v[26:29]
	v_mfma_f32_16x16x32_bf16 v[14:17], v[154:157], v[232:235], v[14:17]
	v_mfma_f32_16x16x32_bf16 v[10:13], v[162:165], v[232:235], v[10:13]
	v_mfma_f32_16x16x32_bf16 v[70:73], v[166:169], v[182:185], v[70:73]
	v_mfma_f32_16x16x32_bf16 v[66:69], v[174:177], v[182:185], v[66:69]
	v_mfma_f32_16x16x32_bf16 v[42:45], v[166:169], v[204:207], v[42:45]
	v_mfma_f32_16x16x32_bf16 v[34:37], v[174:177], v[204:207], v[34:37]
	v_mfma_f32_16x16x32_bf16 v[22:25], v[166:169], v[212:215], v[22:25]
	v_mfma_f32_16x16x32_bf16 v[18:21], v[174:177], v[212:215], v[18:21]
	v_mfma_f32_16x16x32_bf16 v[6:9], v[166:169], v[220:223], v[6:9]
	v_mfma_f32_16x16x32_bf16 v[2:5], v[174:177], v[220:223], v[2:5]
	v_mfma_f32_16x16x32_bf16 v[70:73], v[170:173], v[200:203], v[70:73]
	v_mfma_f32_16x16x32_bf16 v[66:69], v[178:181], v[200:203], v[66:69]
	v_mfma_f32_16x16x32_bf16 v[42:45], v[170:173], v[208:211], v[42:45]
	v_mfma_f32_16x16x32_bf16 v[34:37], v[178:181], v[208:211], v[34:37]
	v_mfma_f32_16x16x32_bf16 v[22:25], v[170:173], v[216:219], v[22:25]
	v_mfma_f32_16x16x32_bf16 v[18:21], v[178:181], v[216:219], v[18:21]
	v_mfma_f32_16x16x32_bf16 v[6:9], v[170:173], v[232:235], v[6:9]
	v_mfma_f32_16x16x32_bf16 v[2:5], v[178:181], v[232:235], v[2:5]
	s_setprio 0
	s_barrier
	s_add_i32 s28, s28, 2
	s_add_u32 s4, s4, 0x100
	s_addc_u32 s5, s5, 0
	s_cmp_gt_u32 s28, 29
	s_cbranch_scc0 .LBB0_334
	s_cmpk_lt_u32 s10, 0x100
	v_readlane_b32 s23, v255, 15
	s_cbranch_scc0 .LBB0_337
	s_barrier

; #define PG8_STAGE(bufoff, gbase, voff) do { _Pragma("unroll") for (int _i = 0; _i < 2; ++_i) \
;         __builtin_amdgcn_global_load_lds((const unsigned*)((const char*)(gbase) + (voff)[_i]), (LAS unsigned*)(lds + (bufoff) + ldsw + _i * 8192), 16, 0, 0); } while (0)
; #define PG8_LDA(dst, b, h) do { _Pragma("unroll") for (int m = 0; m < 4; ++m) _Pragma("unroll") for (int k = 0; k < 2; ++k) dst[m][k] = *(const LAS bf16x8*)(lds + PG8_SA(b, h) + aoff + m * 2048 + k * 1024); } while (0)
; #define PG8_LDB(dst, b, h) do { _Pragma("unroll") for (int n = 0; n < 2; ++n) _Pragma("unroll") for (int k = 0; k < 2; ++k) dst[n][k] = *(const LAS bf16x8*)(lds + PG8_SB(b, h) + boff + n * 2048 + k * 1024); } while (0)
; #define PG8_MMA(ai, bj, At, Bt) do { __builtin_amdgcn_s_setprio(1); _Pragma("unroll") for (int m = 0; m < 4; ++m) _Pragma("unroll") for (int n = 0; n < 2; ++n) _Pragma("unroll") for (int k = 0; k < 2; ++k) \
;         acc[ai][bj][m][n] = __builtin_amdgcn_mfma_f32_16x16x32_bf16(Bt[n][k], At[m][k], acc[ai][bj][m][n], 0, 0, 0); __builtin_amdgcn_s_setprio(0); } while (0)
; #define PG8_BAR __builtin_amdgcn_s_barrier()
; template <class Epi, class Sched>
; __device__ __forceinline__ void gemm_phase(LAS unsigned char* lds, const Gemm g, const Sched& S, const Epi& E, const int tid, unsigned* last_sig = nullptr) {
;     ...
;         const char* nA = has_next ? (const char*)g.A + (size_t)nxt.pm * tstep : cA; const char* nB = has_next ? (const char*)g.Bt + (size_t)nxt.be * g.bstride + (size_t)nxt.pn * tstep : cB;
;         for (int t = 0; t < nt; t += 2) {
;             const bool last = (t == nt - 2);
;             const char* a1 = cA + (size_t)(t + 1) * kstep;
;             const char* a2 = last ? nA : cA + (size_t)(t + 2) * kstep; const char* b2 = last ? nB : cB + (size_t)(t + 2) * kstep;
;             const char* a3 = a2 + kstep; const char* b3 = b2 + kstep;
;             PG8_LDB(B0, 0, 0); PG8_LDB(B1, 0, 1); PG8_SCHED; PG8_LDA(At, 0, 0); PG8_STAGE(PG8_SA(1, 1), a1 + hstep, voffA);
;             PG8_WAIT_V(8); PG8_WAIT_L(0); PG8_BAR; PG8_MMA(0, 0, At, B0); PG8_MMA(0, 1, At, B1); PG8_BAR; PG8_SCHED;
;             PG8_LDA(At, 0, 1); PG8_STAGE(PG8_SB(0, 0), b2, voffB); PG8_STAGE(PG8_SB(0, 1), b2 + hstep, voffB); PG8_STAGE(PG8_SA(0, 0), a2, voffA);
;             PG8_WAIT_V(8); PG8_WAIT_L(0); PG8_BAR; PG8_MMA(1, 0, At, B0); PG8_MMA(1, 1, At, B1); PG8_BAR; PG8_SCHED;
.LBB0_598:
	s_add_u32 s14, s20, 0xfffc0080
	s_addc_u32 s15, s21, -1
	s_add_i32 s56, 0, 0x10000
	s_cmp_eq_u32 s55, 12
	s_cselect_b32 s39, s13, s15
	s_cselect_b32 s38, s51, s14
	s_cselect_b32 s23, s11, s54
	s_cselect_b32 s22, s52, s53
	s_add_i32 s57, 0, 0x14000
	v_add_u32_e32 v142, s56, v185
	v_add_u32_e32 v162, s57, v185
	ds_read_b128 v[130:133], v142
	ds_read_b128 v[134:137], v142 offset:1024
	ds_read_b128 v[138:141], v142 offset:2048
	ds_read_b128 v[142:145], v142 offset:3072
	ds_read_b128 v[146:149], v162
	ds_read_b128 v[150:153], v162 offset:1024
	ds_read_b128 v[154:157], v162 offset:2048
	ds_read_b128 v[162:165], v162 offset:3072
	v_lshl_add_u64 v[240:241], s[20:21], 0, v[158:159]
	s_add_i32 m0, s42, 0xc000
	ds_read_b128 v[166:169], v207
	ds_read_b128 v[170:173], v207 offset:1024
	ds_read_b128 v[208:211], v207 offset:2048
	ds_read_b128 v[212:215], v207 offset:3072
	ds_read_b128 v[216:219], v207 offset:4096
	ds_read_b128 v[220:223], v207 offset:5120
	ds_read_b128 v[232:235], v207 offset:6144
	ds_read_b128 v[236:239], v207 offset:7168
	global_load_lds_dwordx4 v[240:241], off
	v_lshl_add_u64 v[240:241], s[20:21], 0, v[160:161]
	s_add_i32 m0, s42, 0xe000
	s_nop 0
	global_load_lds_dwordx4 v[240:241], off
	s_waitcnt vmcnt(8)
	s_waitcnt lgkmcnt(0)
	s_barrier
	s_setprio 1
	s_waitcnt lgkmcnt(0)
	v_mfma_f32_16x16x32_bf16 v[122:125], v[130:133], v[166:169], v[122:125]
	v_mfma_f32_16x16x32_bf16 v[126:129], v[138:141], v[166:169], v[126:129]
	v_mfma_f32_16x16x32_bf16 v[106:109], v[130:133], v[208:211], v[106:109]
	v_mfma_f32_16x16x32_bf16 v[110:113], v[138:141], v[208:211], v[110:113]
	v_mfma_f32_16x16x32_bf16 v[90:93], v[130:133], v[216:219], v[90:93]
	v_mfma_f32_16x16x32_bf16 v[94:97], v[138:141], v[216:219], v[94:97]
	v_mfma_f32_16x16x32_bf16 v[74:77], v[130:133], v[232:235], v[74:77]
	v_mfma_f32_16x16x32_bf16 v[78:81], v[138:141], v[232:235], v[78:81]
	v_mfma_f32_16x16x32_bf16 v[122:125], v[134:137], v[170:173], v[122:125]
	v_mfma_f32_16x16x32_bf16 v[126:129], v[142:145], v[170:173], v[126:129]
	v_mfma_f32_16x16x32_bf16 v[106:109], v[134:137], v[212:215], v[106:109]
	v_mfma_f32_16x16x32_bf16 v[110:113], v[142:145], v[212:215], v[110:113]
	v_mfma_f32_16x16x32_bf16 v[90:93], v[134:137], v[220:223], v[90:93]
	v_mfma_f32_16x16x32_bf16 v[94:97], v[142:145], v[220:223], v[94:97]
	v_mfma_f32_16x16x32_bf16 v[74:77], v[134:137], v[236:239], v[74:77]
	v_mfma_f32_16x16x32_bf16 v[78:81], v[142:145], v[236:239], v[78:81]
	v_mfma_f32_16x16x32_bf16 v[114:117], v[146:149], v[166:169], v[114:117]
	v_mfma_f32_16x16x32_bf16 v[118:121], v[154:157], v[166:169], v[118:121]
	v_mfma_f32_16x16x32_bf16 v[98:101], v[146:149], v[208:211], v[98:101]
	v_mfma_f32_16x16x32_bf16 v[102:105], v[154:157], v[208:211], v[102:105]
	v_mfma_f32_16x16x32_bf16 v[82:85], v[146:149], v[216:219], v[82:85]
	v_mfma_f32_16x16x32_bf16 v[86:89], v[154:157], v[216:219], v[86:89]
	v_mfma_f32_16x16x32_bf16 v[66:69], v[146:149], v[232:235], v[66:69]
	v_mfma_f32_16x16x32_bf16 v[70:73], v[154:157], v[232:235], v[70:73]
	v_mfma_f32_16x16x32_bf16 v[114:117], v[150:153], v[170:173], v[114:117]
	v_mfma_f32_16x16x32_bf16 v[118:121], v[162:165], v[170:173], v[118:121]
	v_mfma_f32_16x16x32_bf16 v[98:101], v[150:153], v[212:215], v[98:101]
	v_mfma_f32_16x16x32_bf16 v[102:105], v[162:165], v[212:215], v[102:105]
	v_mfma_f32_16x16x32_bf16 v[82:85], v[150:153], v[220:223], v[82:85]
	v_mfma_f32_16x16x32_bf16 v[86:89], v[162:165], v[220:223], v[86:89]
	v_mfma_f32_16x16x32_bf16 v[66:69], v[150:153], v[236:239], v[66:69]
	v_mfma_f32_16x16x32_bf16 v[70:73], v[162:165], v[236:239], v[70:73]
	s_setprio 0
	s_barrier
	s_add_i32 s14, s56, s41
	v_lshl_add_u64 v[240:241], s[22:23], 0, v[186:187]
	s_mov_b32 m0, s14
	ds_read_b128 v[166:169], v207 offset:16384
	ds_read_b128 v[170:173], v207 offset:17408
	ds_read_b128 v[208:211], v207 offset:18432
	ds_read_b128 v[212:215], v207 offset:19456
	ds_read_b128 v[216:219], v207 offset:20480
	ds_read_b128 v[220:223], v207 offset:21504
	ds_read_b128 v[232:235], v207 offset:22528
	ds_read_b128 v[236:239], v207 offset:23552
	global_load_lds_dwordx4 v[240:241], off
	s_add_i32 m0, s14, 0x2000
	s_add_u32 s14, s22, 0x40000
	v_lshl_add_u64 v[242:243], s[22:23], 0, v[204:205]
	s_addc_u32 s15, s23, 0
	s_add_i32 s56, s57, s41
	global_load_lds_dwordx4 v[242:243], off
	v_lshl_add_u64 v[244:245], s[14:15], 0, v[186:187]
	s_mov_b32 m0, s56
	v_lshl_add_u64 v[246:247], s[38:39], 0, v[202:203]
	global_load_lds_dwordx4 v[244:245], off
	v_lshl_add_u64 v[244:245], s[14:15], 0, v[204:205]
	s_add_i32 m0, s56, 0x2000
	s_nop 0
	global_load_lds_dwordx4 v[244:245], off
	v_lshl_add_u64 v[244:245], s[38:39], 0, v[200:201]
	s_mov_b32 m0, s42
	s_nop 0
	global_load_lds_dwordx4 v[244:245], off
	s_mov_b32 m0, s43
	s_nop 0
	global_load_lds_dwordx4 v[246:247], off
	s_waitcnt vmcnt(8)
	s_waitcnt lgkmcnt(0)
	s_barrier
; #define PG8_STAGE(bufoff, gbase, voff) do { _Pragma("unroll") for (int _i = 0; _i < 2; ++_i) \
;         __builtin_amdgcn_global_load_lds((const unsigned*)((const char*)(gbase) + (voff)[_i]), (LAS unsigned*)(lds + (bufoff) + ldsw + _i * 8192), 16, 0, 0); } while (0)
; #define PG8_LDA(dst, b, h) do { _Pragma("unroll") for (int m = 0; m < 4; ++m) _Pragma("unroll") for (int k = 0; k < 2; ++k) dst[m][k] = *(const LAS bf16x8*)(lds + PG8_SA(b, h) + aoff + m * 2048 + k * 1024); } while (0)
; #define PG8_LDB(dst, b, h) do { _Pragma("unroll") for (int n = 0; n < 2; ++n) _Pragma("unroll") for (int k = 0; k < 2; ++k) dst[n][k] = *(const LAS bf16x8*)(lds + PG8_SB(b, h) + boff + n * 2048 + k * 1024); } while (0)
; #define PG8_MMA(ai, bj, At, Bt) do { __builtin_amdgcn_s_setprio(1); _Pragma("unroll") for (int m = 0; m < 4; ++m) _Pragma("unroll") for (int n = 0; n < 2; ++n) _Pragma("unroll") for (int k = 0; k < 2; ++k) \
;         acc[ai][bj][m][n] = __builtin_amdgcn_mfma_f32_16x16x32_bf16(Bt[n][k], At[m][k], acc[ai][bj][m][n], 0, 0, 0); __builtin_amdgcn_s_setprio(0); } while (0)
; #define PG8_WAIT_V(n) asm volatile("s_waitcnt vmcnt(" #n ")" ::: "memory")
; #define PG8_WAIT_L(n) asm volatile("s_waitcnt lgkmcnt(" #n ")" ::: "memory")
; #define PG8_BAR __builtin_amdgcn_s_barrier()
; #define PG8_SCHED __builtin_amdgcn_sched_barrier(0)
; template <class Epi, class Sched>
; __device__ __forceinline__ void gemm_phase(LAS unsigned char* lds, const Gemm g, const Sched& S, const Epi& E, const int tid, unsigned* last_sig = nullptr) {
;     ...
;             PG8_WAIT_V(8); PG8_WAIT_L(0); PG8_BAR; PG8_MMA(1, 0, At, B0); PG8_MMA(1, 1, At, B1); PG8_BAR; PG8_SCHED;
;             PG8_LDB(B0, 1, 0); PG8_LDB(B1, 1, 1); PG8_SCHED; PG8_LDA(At, 1, 0); PG8_STAGE(PG8_SA(0, 1), a2 + hstep, voffA);
;             PG8_WAIT_V(8); PG8_WAIT_L(0); PG8_BAR; PG8_MMA(0, 0, At, B0); PG8_MMA(0, 1, At, B1); PG8_BAR; PG8_SCHED;
	s_setprio 1
	s_waitcnt lgkmcnt(0)
	v_mfma_f32_16x16x32_bf16 v[58:61], v[130:133], v[166:169], v[58:61]
	v_mfma_f32_16x16x32_bf16 v[62:65], v[138:141], v[166:169], v[62:65]
	v_mfma_f32_16x16x32_bf16 v[42:45], v[130:133], v[208:211], v[42:45]
	v_mfma_f32_16x16x32_bf16 v[46:49], v[138:141], v[208:211], v[46:49]
	v_mfma_f32_16x16x32_bf16 v[26:29], v[130:133], v[216:219], v[26:29]
	v_mfma_f32_16x16x32_bf16 v[30:33], v[138:141], v[216:219], v[30:33]
	v_mfma_f32_16x16x32_bf16 v[10:13], v[130:133], v[232:235], v[10:13]
	v_mfma_f32_16x16x32_bf16 v[14:17], v[138:141], v[232:235], v[14:17]
	v_mfma_f32_16x16x32_bf16 v[58:61], v[134:137], v[170:173], v[58:61]
	v_mfma_f32_16x16x32_bf16 v[62:65], v[142:145], v[170:173], v[62:65]
	v_mfma_f32_16x16x32_bf16 v[42:45], v[134:137], v[212:215], v[42:45]
	v_mfma_f32_16x16x32_bf16 v[46:49], v[142:145], v[212:215], v[46:49]
	v_mfma_f32_16x16x32_bf16 v[26:29], v[134:137], v[220:223], v[26:29]
	v_mfma_f32_16x16x32_bf16 v[30:33], v[142:145], v[220:223], v[30:33]
	v_mfma_f32_16x16x32_bf16 v[10:13], v[134:137], v[236:239], v[10:13]
	v_mfma_f32_16x16x32_bf16 v[14:17], v[142:145], v[236:239], v[14:17]
	v_mfma_f32_16x16x32_bf16 v[50:53], v[146:149], v[166:169], v[50:53]
	v_mfma_f32_16x16x32_bf16 v[54:57], v[154:157], v[166:169], v[54:57]
	v_mfma_f32_16x16x32_bf16 v[34:37], v[146:149], v[208:211], v[34:37]
	v_mfma_f32_16x16x32_bf16 v[38:41], v[154:157], v[208:211], v[38:41]
	v_mfma_f32_16x16x32_bf16 v[18:21], v[146:149], v[216:219], v[18:21]
	v_mfma_f32_16x16x32_bf16 v[22:25], v[154:157], v[216:219], v[22:25]
	v_mfma_f32_16x16x32_bf16 v[2:5], v[146:149], v[232:235], v[2:5]
	v_mfma_f32_16x16x32_bf16 v[6:9], v[154:157], v[232:235], v[6:9]
	v_mfma_f32_16x16x32_bf16 v[50:53], v[150:153], v[170:173], v[50:53]
	v_mfma_f32_16x16x32_bf16 v[54:57], v[162:165], v[170:173], v[54:57]
	v_mfma_f32_16x16x32_bf16 v[34:37], v[150:153], v[212:215], v[34:37]
	v_mfma_f32_16x16x32_bf16 v[38:41], v[162:165], v[212:215], v[38:41]
	v_mfma_f32_16x16x32_bf16 v[18:21], v[150:153], v[220:223], v[18:21]
	v_mfma_f32_16x16x32_bf16 v[22:25], v[162:165], v[220:223], v[22:25]
	v_mfma_f32_16x16x32_bf16 v[2:5], v[150:153], v[236:239], v[2:5]
	v_mfma_f32_16x16x32_bf16 v[6:9], v[162:165], v[236:239], v[6:9]
	s_setprio 0
	s_barrier
	s_add_i32 s56, 0, 0x18000
	s_add_i32 s57, 0, 0x1c000
	v_add_u32_e32 v142, s56, v185
	v_add_u32_e32 v162, s57, v185
	ds_read_b128 v[130:133], v142
	ds_read_b128 v[134:137], v142 offset:1024
	ds_read_b128 v[138:141], v142 offset:2048
	ds_read_b128 v[142:145], v142 offset:3072
	ds_read_b128 v[146:149], v162
	ds_read_b128 v[150:153], v162 offset:1024
	ds_read_b128 v[154:157], v162 offset:2048
	ds_read_b128 v[162:165], v162 offset:3072
	s_add_u32 s14, s38, 0x40000
	s_addc_u32 s15, s39, 0
	s_mov_b32 m0, s44
	v_lshl_add_u64 v[248:249], s[14:15], 0, v[200:201]
	ds_read_b128 v[166:169], v207 offset:32768
	ds_read_b128 v[170:173], v207 offset:33792
	ds_read_b128 v[208:211], v207 offset:34816
	ds_read_b128 v[212:215], v207 offset:35840
	ds_read_b128 v[216:219], v207 offset:36864
	ds_read_b128 v[220:223], v207 offset:37888
	ds_read_b128 v[232:235], v207 offset:38912
	ds_read_b128 v[236:239], v207 offset:39936
	global_load_lds_dwordx4 v[248:249], off
	v_lshl_add_u64 v[248:249], s[14:15], 0, v[202:203]
	s_mov_b32 m0, s45
	s_nop 0
	global_load_lds_dwordx4 v[248:249], off
	s_waitcnt vmcnt(8)
	s_waitcnt lgkmcnt(0)
	s_barrier
	s_setprio 1
	s_waitcnt lgkmcnt(0)
	v_mfma_f32_16x16x32_bf16 v[122:125], v[130:133], v[166:169], v[122:125]
	v_mfma_f32_16x16x32_bf16 v[126:129], v[138:141], v[166:169], v[126:129]
	v_mfma_f32_16x16x32_bf16 v[106:109], v[130:133], v[208:211], v[106:109]
	v_mfma_f32_16x16x32_bf16 v[110:113], v[138:141], v[208:211], v[110:113]
	v_mfma_f32_16x16x32_bf16 v[90:93], v[130:133], v[216:219], v[90:93]
	v_mfma_f32_16x16x32_bf16 v[94:97], v[138:141], v[216:219], v[94:97]
	v_mfma_f32_16x16x32_bf16 v[74:77], v[130:133], v[232:235], v[74:77]
	v_mfma_f32_16x16x32_bf16 v[78:81], v[138:141], v[232:235], v[78:81]
	v_mfma_f32_16x16x32_bf16 v[122:125], v[134:137], v[170:173], v[122:125]
	v_mfma_f32_16x16x32_bf16 v[126:129], v[142:145], v[170:173], v[126:129]
	v_mfma_f32_16x16x32_bf16 v[106:109], v[134:137], v[212:215], v[106:109]
	v_mfma_f32_16x16x32_bf16 v[110:113], v[142:145], v[212:215], v[110:113]
	v_mfma_f32_16x16x32_bf16 v[90:93], v[134:137], v[220:223], v[90:93]
	v_mfma_f32_16x16x32_bf16 v[94:97], v[142:145], v[220:223], v[94:97]
	v_mfma_f32_16x16x32_bf16 v[74:77], v[134:137], v[236:239], v[74:77]
	v_mfma_f32_16x16x32_bf16 v[78:81], v[142:145], v[236:239], v[78:81]
	v_mfma_f32_16x16x32_bf16 v[114:117], v[146:149], v[166:169], v[114:117]
	v_mfma_f32_16x16x32_bf16 v[118:121], v[154:157], v[166:169], v[118:121]
	v_mfma_f32_16x16x32_bf16 v[98:101], v[146:149], v[208:211], v[98:101]
	v_mfma_f32_16x16x32_bf16 v[102:105], v[154:157], v[208:211], v[102:105]
	v_mfma_f32_16x16x32_bf16 v[82:85], v[146:149], v[216:219], v[82:85]
	v_mfma_f32_16x16x32_bf16 v[86:89], v[154:157], v[216:219], v[86:89]
	v_mfma_f32_16x16x32_bf16 v[66:69], v[146:149], v[232:235], v[66:69]
	v_mfma_f32_16x16x32_bf16 v[70:73], v[154:157], v[232:235], v[70:73]
	v_mfma_f32_16x16x32_bf16 v[114:117], v[150:153], v[170:173], v[114:117]
	v_mfma_f32_16x16x32_bf16 v[118:121], v[162:165], v[170:173], v[118:121]
	v_mfma_f32_16x16x32_bf16 v[98:101], v[150:153], v[212:215], v[98:101]
	v_mfma_f32_16x16x32_bf16 v[102:105], v[162:165], v[212:215], v[102:105]
	v_mfma_f32_16x16x32_bf16 v[82:85], v[150:153], v[220:223], v[82:85]
	v_mfma_f32_16x16x32_bf16 v[86:89], v[162:165], v[220:223], v[86:89]
	v_mfma_f32_16x16x32_bf16 v[66:69], v[150:153], v[236:239], v[66:69]
	v_mfma_f32_16x16x32_bf16 v[70:73], v[162:165], v[236:239], v[70:73]
	s_setprio 0
	s_barrier
; #define PG8_STAGE(bufoff, gbase, voff) do { _Pragma("unroll") for (int _i = 0; _i < 2; ++_i) \
;         __builtin_amdgcn_global_load_lds((const unsigned*)((const char*)(gbase) + (voff)[_i]), (LAS unsigned*)(lds + (bufoff) + ldsw + _i * 8192), 16, 0, 0); } while (0)
; #define PG8_LDA(dst, b, h) do { _Pragma("unroll") for (int m = 0; m < 4; ++m) _Pragma("unroll") for (int k = 0; k < 2; ++k) dst[m][k] = *(const LAS bf16x8*)(lds + PG8_SA(b, h) + aoff + m * 2048 + k * 1024); } while (0)
; #define PG8_MMA(ai, bj, At, Bt) do { __builtin_amdgcn_s_setprio(1); _Pragma("unroll") for (int m = 0; m < 4; ++m) _Pragma("unroll") for (int n = 0; n < 2; ++n) _Pragma("unroll") for (int k = 0; k < 2; ++k) \
;         acc[ai][bj][m][n] = __builtin_amdgcn_mfma_f32_16x16x32_bf16(Bt[n][k], At[m][k], acc[ai][bj][m][n], 0, 0, 0); __builtin_amdgcn_s_setprio(0); } while (0)
; #define PG8_WAIT_V(n) asm volatile("s_waitcnt vmcnt(" #n ")" ::: "memory")
; #define PG8_WAIT_L(n) asm volatile("s_waitcnt lgkmcnt(" #n ")" ::: "memory")
; #define PG8_BAR __builtin_amdgcn_s_barrier()
; #define PG8_SCHED __builtin_amdgcn_sched_barrier(0)
; template <class Epi, class Sched>
; __device__ __forceinline__ void gemm_phase(LAS unsigned char* lds, const Gemm g, const Sched& S, const Epi& E, const int tid, unsigned* last_sig = nullptr) {
;     ...
;             PG8_LDA(At, 1, 1); PG8_STAGE(PG8_SB(1, 0), b3, voffB); PG8_STAGE(PG8_SB(1, 1), b3 + hstep, voffB); PG8_STAGE(PG8_SA(1, 0), a3, voffA);
;             PG8_WAIT_V(8); PG8_WAIT_L(0); PG8_BAR; PG8_MMA(1, 0, At, B0); PG8_MMA(1, 1, At, B1); PG8_BAR; PG8_SCHED;
;         }
;         if (wr == 0) PG8_BAR;
	s_add_i32 s14, s56, s41
	v_lshl_add_u64 v[240:241], v[240:241], 0, s[34:35]
	s_mov_b32 m0, s14
	ds_read_b128 v[166:169], v207 offset:49152
	ds_read_b128 v[170:173], v207 offset:50176
	ds_read_b128 v[208:211], v207 offset:51200
	ds_read_b128 v[212:215], v207 offset:52224
	ds_read_b128 v[216:219], v207 offset:53248
	ds_read_b128 v[220:223], v207 offset:54272
	ds_read_b128 v[232:235], v207 offset:55296
	ds_read_b128 v[236:239], v207 offset:56320
	global_load_lds_dwordx4 v[240:241], off
	s_add_i32 m0, s14, 0x2000
	s_add_u32 s14, s22, 0x40080
	v_lshl_add_u64 v[240:241], v[242:243], 0, s[34:35]
	s_addc_u32 s15, s23, 0
	s_add_i32 s22, s57, s41
	global_load_lds_dwordx4 v[240:241], off
	v_lshl_add_u64 v[240:241], s[14:15], 0, v[186:187]
	s_mov_b32 m0, s22
	s_nop 0
	global_load_lds_dwordx4 v[240:241], off
	v_lshl_add_u64 v[240:241], s[14:15], 0, v[204:205]
	s_add_i32 m0, s22, 0x2000
	s_nop 0
	global_load_lds_dwordx4 v[240:241], off
	v_lshl_add_u64 v[240:241], v[244:245], 0, s[34:35]
	s_mov_b32 m0, s46
	s_nop 0
	global_load_lds_dwordx4 v[240:241], off
	v_lshl_add_u64 v[240:241], v[246:247], 0, s[34:35]
	s_mov_b32 m0, s47
	s_nop 0
	global_load_lds_dwordx4 v[240:241], off
	s_waitcnt vmcnt(8)
	s_waitcnt lgkmcnt(0)
	s_barrier
	s_setprio 1
	s_waitcnt lgkmcnt(0)
	v_mfma_f32_16x16x32_bf16 v[58:61], v[130:133], v[166:169], v[58:61]
	v_mfma_f32_16x16x32_bf16 v[62:65], v[138:141], v[166:169], v[62:65]
	v_mfma_f32_16x16x32_bf16 v[42:45], v[130:133], v[208:211], v[42:45]
	v_mfma_f32_16x16x32_bf16 v[46:49], v[138:141], v[208:211], v[46:49]
	v_mfma_f32_16x16x32_bf16 v[26:29], v[130:133], v[216:219], v[26:29]
	v_mfma_f32_16x16x32_bf16 v[30:33], v[138:141], v[216:219], v[30:33]
	v_mfma_f32_16x16x32_bf16 v[10:13], v[130:133], v[232:235], v[10:13]
	v_mfma_f32_16x16x32_bf16 v[14:17], v[138:141], v[232:235], v[14:17]
	v_mfma_f32_16x16x32_bf16 v[58:61], v[134:137], v[170:173], v[58:61]
	v_mfma_f32_16x16x32_bf16 v[62:65], v[142:145], v[170:173], v[62:65]
	v_mfma_f32_16x16x32_bf16 v[42:45], v[134:137], v[212:215], v[42:45]
	v_mfma_f32_16x16x32_bf16 v[46:49], v[142:145], v[212:215], v[46:49]
	v_mfma_f32_16x16x32_bf16 v[26:29], v[134:137], v[220:223], v[26:29]
	v_mfma_f32_16x16x32_bf16 v[30:33], v[142:145], v[220:223], v[30:33]
	v_mfma_f32_16x16x32_bf16 v[10:13], v[134:137], v[236:239], v[10:13]
	v_mfma_f32_16x16x32_bf16 v[14:17], v[142:145], v[236:239], v[14:17]
	v_mfma_f32_16x16x32_bf16 v[50:53], v[146:149], v[166:169], v[50:53]
	v_mfma_f32_16x16x32_bf16 v[54:57], v[154:157], v[166:169], v[54:57]
	v_mfma_f32_16x16x32_bf16 v[34:37], v[146:149], v[208:211], v[34:37]
	v_mfma_f32_16x16x32_bf16 v[38:41], v[154:157], v[208:211], v[38:41]
	v_mfma_f32_16x16x32_bf16 v[18:21], v[146:149], v[216:219], v[18:21]
	v_mfma_f32_16x16x32_bf16 v[22:25], v[154:157], v[216:219], v[22:25]
	v_mfma_f32_16x16x32_bf16 v[2:5], v[146:149], v[232:235], v[2:5]
	v_mfma_f32_16x16x32_bf16 v[6:9], v[154:157], v[232:235], v[6:9]
	v_mfma_f32_16x16x32_bf16 v[50:53], v[150:153], v[170:173], v[50:53]
	v_mfma_f32_16x16x32_bf16 v[54:57], v[162:165], v[170:173], v[54:57]
	v_mfma_f32_16x16x32_bf16 v[34:37], v[150:153], v[212:215], v[34:37]
	v_mfma_f32_16x16x32_bf16 v[38:41], v[162:165], v[212:215], v[38:41]
	v_mfma_f32_16x16x32_bf16 v[18:21], v[150:153], v[220:223], v[18:21]
	v_mfma_f32_16x16x32_bf16 v[22:25], v[162:165], v[220:223], v[22:25]
	v_mfma_f32_16x16x32_bf16 v[2:5], v[150:153], v[236:239], v[2:5]
	v_mfma_f32_16x16x32_bf16 v[6:9], v[162:165], v[236:239], v[6:9]
	s_setprio 0
	s_barrier
	s_add_i32 s55, s55, 2
	s_add_u32 s20, s20, 0x100
	s_addc_u32 s21, s21, 0
	s_add_u32 s53, s53, 0x100
	s_addc_u32 s54, s54, 0
	s_cmp_gt_u32 s55, 13
	s_cbranch_scc0 .LBB0_598
	s_and_b64 vcc, exec, s[8:9]
	s_cbranch_vccz .LBB0_601
	s_barrier

; #define PG8_STAGE(bufoff, gbase, voff) do { _Pragma("unroll") for (int _i = 0; _i < 2; ++_i) \
;         __builtin_amdgcn_global_load_lds((const unsigned*)((const char*)(gbase) + (voff)[_i]), (LAS unsigned*)(lds + (bufoff) + ldsw + _i * 8192), 16, 0, 0); } while (0)
; #define PG8_LDA(dst, b, h) do { _Pragma("unroll") for (int m = 0; m < 4; ++m) _Pragma("unroll") for (int k = 0; k < 2; ++k) dst[m][k] = *(const LAS bf16x8*)(lds + PG8_SA(b, h) + aoff + m * 2048 + k * 1024); } while (0)
; #define PG8_LDB(dst, b, h) do { _Pragma("unroll") for (int n = 0; n < 2; ++n) _Pragma("unroll") for (int k = 0; k < 2; ++k) dst[n][k] = *(const LAS bf16x8*)(lds + PG8_SB(b, h) + boff + n * 2048 + k * 1024); } while (0)
; #define PG8_MMA(ai, bj, At, Bt) do { __builtin_amdgcn_s_setprio(1); _Pragma("unroll") for (int m = 0; m < 4; ++m) _Pragma("unroll") for (int n = 0; n < 2; ++n) _Pragma("unroll") for (int k = 0; k < 2; ++k) \
;         acc[ai][bj][m][n] = __builtin_amdgcn_mfma_f32_16x16x32_bf16(Bt[n][k], At[m][k], acc[ai][bj][m][n], 0, 0, 0); __builtin_amdgcn_s_setprio(0); } while (0)
; #define PG8_BAR __builtin_amdgcn_s_barrier()
; template <class Epi, class Sched>
; __device__ __forceinline__ void gemm_phase(LAS unsigned char* lds, const Gemm g, const Sched& S, const Epi& E, const int tid, unsigned* last_sig = nullptr) {
;     ...
;         const char* nA = has_next ? (const char*)g.A + (size_t)nxt.pm * tstep : cA; const char* nB = has_next ? (const char*)g.Bt + (size_t)nxt.be * g.bstride + (size_t)nxt.pn * tstep : cB;
;         for (int t = 0; t < nt; t += 2) {
;             const bool last = (t == nt - 2);
;             const char* a1 = cA + (size_t)(t + 1) * kstep;
;             const char* a2 = last ? nA : cA + (size_t)(t + 2) * kstep; const char* b2 = last ? nB : cB + (size_t)(t + 2) * kstep;
;             const char* a3 = a2 + kstep; const char* b3 = b2 + kstep;
;             PG8_LDB(B0, 0, 0); PG8_LDB(B1, 0, 1); PG8_SCHED; PG8_LDA(At, 0, 0); PG8_STAGE(PG8_SA(1, 1), a1 + hstep, voffA);
;             PG8_WAIT_V(8); PG8_WAIT_L(0); PG8_BAR; PG8_MMA(0, 0, At, B0); PG8_MMA(0, 1, At, B1); PG8_BAR; PG8_SCHED;
;             PG8_LDA(At, 0, 1); PG8_STAGE(PG8_SB(0, 0), b2, voffB); PG8_STAGE(PG8_SB(0, 1), b2 + hstep, voffB); PG8_STAGE(PG8_SA(0, 0), a2, voffA);
;             PG8_WAIT_V(8); PG8_WAIT_L(0); PG8_BAR; PG8_MMA(1, 0, At, B0); PG8_MMA(1, 1, At, B1); PG8_BAR; PG8_SCHED;
.LBB0_618:
	s_add_u32 s14, s22, 0xfffc0080
	s_addc_u32 s15, s23, -1
	s_add_i32 s53, 0, 0x10000
	s_cmp_eq_u32 s52, 12
	s_cselect_b32 s41, s11, s15
	s_cselect_b32 s40, s19, s14
	s_cselect_b32 s39, s9, s51
	s_cselect_b32 s38, s49, s50
	s_add_i32 s54, 0, 0x14000
	v_add_u32_e32 v142, s53, v232
	v_add_u32_e32 v158, s54, v232
	ds_read_b128 v[130:133], v142
	ds_read_b128 v[134:137], v142 offset:1024
	ds_read_b128 v[138:141], v142 offset:2048
	ds_read_b128 v[142:145], v142 offset:3072
	ds_read_b128 v[146:149], v158
	ds_read_b128 v[150:153], v158 offset:1024
	ds_read_b128 v[154:157], v158 offset:2048
	ds_read_b128 v[158:161], v158 offset:3072
	v_lshl_add_u64 v[218:219], s[22:23], 0, v[206:207]
	s_add_i32 m0, s21, 0xc000
	ds_read_b128 v[162:165], v234
	ds_read_b128 v[166:169], v234 offset:1024
	ds_read_b128 v[170:173], v234 offset:2048
	ds_read_b128 v[174:177], v234 offset:3072
	ds_read_b128 v[178:181], v234 offset:4096
	ds_read_b128 v[182:185], v234 offset:5120
	ds_read_b128 v[210:213], v234 offset:6144
	ds_read_b128 v[214:217], v234 offset:7168
	global_load_lds_dwordx4 v[218:219], off
	v_lshl_add_u64 v[218:219], s[22:23], 0, v[208:209]
	s_add_i32 m0, s21, 0xe000
	s_nop 0
	global_load_lds_dwordx4 v[218:219], off
	s_waitcnt vmcnt(8)
	s_waitcnt lgkmcnt(0)
	s_barrier
	s_setprio 1
	s_waitcnt lgkmcnt(0)
	v_mfma_f32_16x16x32_bf16 v[122:125], v[130:133], v[162:165], v[122:125]
	v_mfma_f32_16x16x32_bf16 v[126:129], v[138:141], v[162:165], v[126:129]
	v_mfma_f32_16x16x32_bf16 v[106:109], v[130:133], v[170:173], v[106:109]
	v_mfma_f32_16x16x32_bf16 v[110:113], v[138:141], v[170:173], v[110:113]
	v_mfma_f32_16x16x32_bf16 v[90:93], v[130:133], v[178:181], v[90:93]
	v_mfma_f32_16x16x32_bf16 v[94:97], v[138:141], v[178:181], v[94:97]
	v_mfma_f32_16x16x32_bf16 v[74:77], v[130:133], v[210:213], v[74:77]
	v_mfma_f32_16x16x32_bf16 v[78:81], v[138:141], v[210:213], v[78:81]
	v_mfma_f32_16x16x32_bf16 v[122:125], v[134:137], v[166:169], v[122:125]
	v_mfma_f32_16x16x32_bf16 v[126:129], v[142:145], v[166:169], v[126:129]
	v_mfma_f32_16x16x32_bf16 v[106:109], v[134:137], v[174:177], v[106:109]
	v_mfma_f32_16x16x32_bf16 v[110:113], v[142:145], v[174:177], v[110:113]
	v_mfma_f32_16x16x32_bf16 v[90:93], v[134:137], v[182:185], v[90:93]
	v_mfma_f32_16x16x32_bf16 v[94:97], v[142:145], v[182:185], v[94:97]
	v_mfma_f32_16x16x32_bf16 v[74:77], v[134:137], v[214:217], v[74:77]
	v_mfma_f32_16x16x32_bf16 v[78:81], v[142:145], v[214:217], v[78:81]
	v_mfma_f32_16x16x32_bf16 v[114:117], v[146:149], v[162:165], v[114:117]
	v_mfma_f32_16x16x32_bf16 v[118:121], v[154:157], v[162:165], v[118:121]
	v_mfma_f32_16x16x32_bf16 v[98:101], v[146:149], v[170:173], v[98:101]
	v_mfma_f32_16x16x32_bf16 v[102:105], v[154:157], v[170:173], v[102:105]
	v_mfma_f32_16x16x32_bf16 v[82:85], v[146:149], v[178:181], v[82:85]
	v_mfma_f32_16x16x32_bf16 v[86:89], v[154:157], v[178:181], v[86:89]
	v_mfma_f32_16x16x32_bf16 v[66:69], v[146:149], v[210:213], v[66:69]
	v_mfma_f32_16x16x32_bf16 v[70:73], v[154:157], v[210:213], v[70:73]
	v_mfma_f32_16x16x32_bf16 v[114:117], v[150:153], v[166:169], v[114:117]
	v_mfma_f32_16x16x32_bf16 v[118:121], v[158:161], v[166:169], v[118:121]
	v_mfma_f32_16x16x32_bf16 v[98:101], v[150:153], v[174:177], v[98:101]
	v_mfma_f32_16x16x32_bf16 v[102:105], v[158:161], v[174:177], v[102:105]
	v_mfma_f32_16x16x32_bf16 v[82:85], v[150:153], v[182:185], v[82:85]
	v_mfma_f32_16x16x32_bf16 v[86:89], v[158:161], v[182:185], v[86:89]
	v_mfma_f32_16x16x32_bf16 v[66:69], v[150:153], v[214:217], v[66:69]
	v_mfma_f32_16x16x32_bf16 v[70:73], v[158:161], v[214:217], v[70:73]
	s_setprio 0
	s_barrier
	s_add_i32 s14, s53, s42
	v_lshl_add_u64 v[218:219], s[38:39], 0, v[186:187]
	s_mov_b32 m0, s14
	ds_read_b128 v[162:165], v234 offset:16384
	ds_read_b128 v[166:169], v234 offset:17408
	ds_read_b128 v[170:173], v234 offset:18432
	ds_read_b128 v[174:177], v234 offset:19456
	ds_read_b128 v[178:181], v234 offset:20480
	ds_read_b128 v[182:185], v234 offset:21504
	ds_read_b128 v[210:213], v234 offset:22528
	ds_read_b128 v[214:217], v234 offset:23552
	global_load_lds_dwordx4 v[218:219], off
	s_add_i32 m0, s14, 0x2000
	s_add_u32 s14, s38, 0x40000
	v_lshl_add_u64 v[220:221], s[38:39], 0, v[204:205]
	s_addc_u32 s15, s39, 0
	s_add_i32 s53, s54, s42
	global_load_lds_dwordx4 v[220:221], off
	v_lshl_add_u64 v[222:223], s[14:15], 0, v[186:187]
	s_mov_b32 m0, s53
	v_lshl_add_u64 v[236:237], s[40:41], 0, v[202:203]
	global_load_lds_dwordx4 v[222:223], off
	v_lshl_add_u64 v[222:223], s[14:15], 0, v[204:205]
	s_add_i32 m0, s53, 0x2000
	s_nop 0
	global_load_lds_dwordx4 v[222:223], off
	v_lshl_add_u64 v[222:223], s[40:41], 0, v[200:201]
	s_mov_b32 m0, s21
	s_nop 0
	global_load_lds_dwordx4 v[222:223], off
	s_mov_b32 m0, s43
	s_nop 0
	global_load_lds_dwordx4 v[236:237], off
	s_waitcnt vmcnt(8)
	s_waitcnt lgkmcnt(0)
	s_barrier
; #define PG8_STAGE(bufoff, gbase, voff) do { _Pragma("unroll") for (int _i = 0; _i < 2; ++_i) \
;         __builtin_amdgcn_global_load_lds((const unsigned*)((const char*)(gbase) + (voff)[_i]), (LAS unsigned*)(lds + (bufoff) + ldsw + _i * 8192), 16, 0, 0); } while (0)
; #define PG8_LDA(dst, b, h) do { _Pragma("unroll") for (int m = 0; m < 4; ++m) _Pragma("unroll") for (int k = 0; k < 2; ++k) dst[m][k] = *(const LAS bf16x8*)(lds + PG8_SA(b, h) + aoff + m * 2048 + k * 1024); } while (0)
; #define PG8_LDB(dst, b, h) do { _Pragma("unroll") for (int n = 0; n < 2; ++n) _Pragma("unroll") for (int k = 0; k < 2; ++k) dst[n][k] = *(const LAS bf16x8*)(lds + PG8_SB(b, h) + boff + n * 2048 + k * 1024); } while (0)
; #define PG8_MMA(ai, bj, At, Bt) do { __builtin_amdgcn_s_setprio(1); _Pragma("unroll") for (int m = 0; m < 4; ++m) _Pragma("unroll") for (int n = 0; n < 2; ++n) _Pragma("unroll") for (int k = 0; k < 2; ++k) \
;         acc[ai][bj][m][n] = __builtin_amdgcn_mfma_f32_16x16x32_bf16(Bt[n][k], At[m][k], acc[ai][bj][m][n], 0, 0, 0); __builtin_amdgcn_s_setprio(0); } while (0)
; #define PG8_WAIT_V(n) asm volatile("s_waitcnt vmcnt(" #n ")" ::: "memory")
; #define PG8_WAIT_L(n) asm volatile("s_waitcnt lgkmcnt(" #n ")" ::: "memory")
; #define PG8_BAR __builtin_amdgcn_s_barrier()
; #define PG8_SCHED __builtin_amdgcn_sched_barrier(0)
; template <class Epi, class Sched>
; __device__ __forceinline__ void gemm_phase(LAS unsigned char* lds, const Gemm g, const Sched& S, const Epi& E, const int tid, unsigned* last_sig = nullptr) {
;     ...
;             PG8_WAIT_V(8); PG8_WAIT_L(0); PG8_BAR; PG8_MMA(1, 0, At, B0); PG8_MMA(1, 1, At, B1); PG8_BAR; PG8_SCHED;
;             PG8_LDB(B0, 1, 0); PG8_LDB(B1, 1, 1); PG8_SCHED; PG8_LDA(At, 1, 0); PG8_STAGE(PG8_SA(0, 1), a2 + hstep, voffA);
;             PG8_WAIT_V(8); PG8_WAIT_L(0); PG8_BAR; PG8_MMA(0, 0, At, B0); PG8_MMA(0, 1, At, B1); PG8_BAR; PG8_SCHED;
	s_setprio 1
	s_waitcnt lgkmcnt(0)
	v_mfma_f32_16x16x32_bf16 v[58:61], v[130:133], v[162:165], v[58:61]
	v_mfma_f32_16x16x32_bf16 v[62:65], v[138:141], v[162:165], v[62:65]
	v_mfma_f32_16x16x32_bf16 v[42:45], v[130:133], v[170:173], v[42:45]
	v_mfma_f32_16x16x32_bf16 v[46:49], v[138:141], v[170:173], v[46:49]
	v_mfma_f32_16x16x32_bf16 v[26:29], v[130:133], v[178:181], v[26:29]
	v_mfma_f32_16x16x32_bf16 v[30:33], v[138:141], v[178:181], v[30:33]
	v_mfma_f32_16x16x32_bf16 v[10:13], v[130:133], v[210:213], v[10:13]
	v_mfma_f32_16x16x32_bf16 v[14:17], v[138:141], v[210:213], v[14:17]
	v_mfma_f32_16x16x32_bf16 v[58:61], v[134:137], v[166:169], v[58:61]
	v_mfma_f32_16x16x32_bf16 v[62:65], v[142:145], v[166:169], v[62:65]
	v_mfma_f32_16x16x32_bf16 v[42:45], v[134:137], v[174:177], v[42:45]
	v_mfma_f32_16x16x32_bf16 v[46:49], v[142:145], v[174:177], v[46:49]
	v_mfma_f32_16x16x32_bf16 v[26:29], v[134:137], v[182:185], v[26:29]
	v_mfma_f32_16x16x32_bf16 v[30:33], v[142:145], v[182:185], v[30:33]
	v_mfma_f32_16x16x32_bf16 v[10:13], v[134:137], v[214:217], v[10:13]
	v_mfma_f32_16x16x32_bf16 v[14:17], v[142:145], v[214:217], v[14:17]
	v_mfma_f32_16x16x32_bf16 v[50:53], v[146:149], v[162:165], v[50:53]
	v_mfma_f32_16x16x32_bf16 v[54:57], v[154:157], v[162:165], v[54:57]
	v_mfma_f32_16x16x32_bf16 v[34:37], v[146:149], v[170:173], v[34:37]
	v_mfma_f32_16x16x32_bf16 v[38:41], v[154:157], v[170:173], v[38:41]
	v_mfma_f32_16x16x32_bf16 v[18:21], v[146:149], v[178:181], v[18:21]
	v_mfma_f32_16x16x32_bf16 v[22:25], v[154:157], v[178:181], v[22:25]
	v_mfma_f32_16x16x32_bf16 v[2:5], v[146:149], v[210:213], v[2:5]
	v_mfma_f32_16x16x32_bf16 v[6:9], v[154:157], v[210:213], v[6:9]
	v_mfma_f32_16x16x32_bf16 v[50:53], v[150:153], v[166:169], v[50:53]
	v_mfma_f32_16x16x32_bf16 v[54:57], v[158:161], v[166:169], v[54:57]
	v_mfma_f32_16x16x32_bf16 v[34:37], v[150:153], v[174:177], v[34:37]
	v_mfma_f32_16x16x32_bf16 v[38:41], v[158:161], v[174:177], v[38:41]
	v_mfma_f32_16x16x32_bf16 v[18:21], v[150:153], v[182:185], v[18:21]
	v_mfma_f32_16x16x32_bf16 v[22:25], v[158:161], v[182:185], v[22:25]
	v_mfma_f32_16x16x32_bf16 v[2:5], v[150:153], v[214:217], v[2:5]
	v_mfma_f32_16x16x32_bf16 v[6:9], v[158:161], v[214:217], v[6:9]
	s_setprio 0
	s_barrier
	s_add_i32 s53, 0, 0x18000
	s_add_i32 s54, 0, 0x1c000
	v_add_u32_e32 v142, s53, v232
	v_add_u32_e32 v158, s54, v232
	ds_read_b128 v[130:133], v142
	ds_read_b128 v[134:137], v142 offset:1024
	ds_read_b128 v[138:141], v142 offset:2048
	ds_read_b128 v[142:145], v142 offset:3072
	ds_read_b128 v[146:149], v158
	ds_read_b128 v[150:153], v158 offset:1024
	ds_read_b128 v[154:157], v158 offset:2048
	ds_read_b128 v[158:161], v158 offset:3072
	s_add_u32 s14, s40, 0x40000
	s_addc_u32 s15, s41, 0
	s_mov_b32 m0, s44
	v_lshl_add_u64 v[238:239], s[14:15], 0, v[200:201]
	ds_read_b128 v[162:165], v234 offset:32768
	ds_read_b128 v[166:169], v234 offset:33792
	ds_read_b128 v[170:173], v234 offset:34816
	ds_read_b128 v[174:177], v234 offset:35840
	ds_read_b128 v[178:181], v234 offset:36864
	ds_read_b128 v[182:185], v234 offset:37888
	ds_read_b128 v[210:213], v234 offset:38912
	ds_read_b128 v[214:217], v234 offset:39936
	global_load_lds_dwordx4 v[238:239], off
	v_lshl_add_u64 v[238:239], s[14:15], 0, v[202:203]
	s_mov_b32 m0, s45
	s_nop 0
	global_load_lds_dwordx4 v[238:239], off
	s_waitcnt vmcnt(8)
	s_waitcnt lgkmcnt(0)
	s_barrier
	s_setprio 1
	s_waitcnt lgkmcnt(0)
	v_mfma_f32_16x16x32_bf16 v[122:125], v[130:133], v[162:165], v[122:125]
	v_mfma_f32_16x16x32_bf16 v[126:129], v[138:141], v[162:165], v[126:129]
	v_mfma_f32_16x16x32_bf16 v[106:109], v[130:133], v[170:173], v[106:109]
	v_mfma_f32_16x16x32_bf16 v[110:113], v[138:141], v[170:173], v[110:113]
	v_mfma_f32_16x16x32_bf16 v[90:93], v[130:133], v[178:181], v[90:93]
	v_mfma_f32_16x16x32_bf16 v[94:97], v[138:141], v[178:181], v[94:97]
	v_mfma_f32_16x16x32_bf16 v[74:77], v[130:133], v[210:213], v[74:77]
	v_mfma_f32_16x16x32_bf16 v[78:81], v[138:141], v[210:213], v[78:81]
	v_mfma_f32_16x16x32_bf16 v[122:125], v[134:137], v[166:169], v[122:125]
	v_mfma_f32_16x16x32_bf16 v[126:129], v[142:145], v[166:169], v[126:129]
	v_mfma_f32_16x16x32_bf16 v[106:109], v[134:137], v[174:177], v[106:109]
	v_mfma_f32_16x16x32_bf16 v[110:113], v[142:145], v[174:177], v[110:113]
	v_mfma_f32_16x16x32_bf16 v[90:93], v[134:137], v[182:185], v[90:93]
	v_mfma_f32_16x16x32_bf16 v[94:97], v[142:145], v[182:185], v[94:97]
	v_mfma_f32_16x16x32_bf16 v[74:77], v[134:137], v[214:217], v[74:77]
	v_mfma_f32_16x16x32_bf16 v[78:81], v[142:145], v[214:217], v[78:81]
	v_mfma_f32_16x16x32_bf16 v[114:117], v[146:149], v[162:165], v[114:117]
	v_mfma_f32_16x16x32_bf16 v[118:121], v[154:157], v[162:165], v[118:121]
	v_mfma_f32_16x16x32_bf16 v[98:101], v[146:149], v[170:173], v[98:101]
	v_mfma_f32_16x16x32_bf16 v[102:105], v[154:157], v[170:173], v[102:105]
	v_mfma_f32_16x16x32_bf16 v[82:85], v[146:149], v[178:181], v[82:85]
	v_mfma_f32_16x16x32_bf16 v[86:89], v[154:157], v[178:181], v[86:89]
	v_mfma_f32_16x16x32_bf16 v[66:69], v[146:149], v[210:213], v[66:69]
	v_mfma_f32_16x16x32_bf16 v[70:73], v[154:157], v[210:213], v[70:73]
	v_mfma_f32_16x16x32_bf16 v[114:117], v[150:153], v[166:169], v[114:117]
	v_mfma_f32_16x16x32_bf16 v[118:121], v[158:161], v[166:169], v[118:121]
	v_mfma_f32_16x16x32_bf16 v[98:101], v[150:153], v[174:177], v[98:101]
	v_mfma_f32_16x16x32_bf16 v[102:105], v[158:161], v[174:177], v[102:105]
	v_mfma_f32_16x16x32_bf16 v[82:85], v[150:153], v[182:185], v[82:85]
	v_mfma_f32_16x16x32_bf16 v[86:89], v[158:161], v[182:185], v[86:89]
	v_mfma_f32_16x16x32_bf16 v[66:69], v[150:153], v[214:217], v[66:69]
	v_mfma_f32_16x16x32_bf16 v[70:73], v[158:161], v[214:217], v[70:73]
	s_setprio 0
	s_barrier
; #define PG8_STAGE(bufoff, gbase, voff) do { _Pragma("unroll") for (int _i = 0; _i < 2; ++_i) \
;         __builtin_amdgcn_global_load_lds((const unsigned*)((const char*)(gbase) + (voff)[_i]), (LAS unsigned*)(lds + (bufoff) + ldsw + _i * 8192), 16, 0, 0); } while (0)
; #define PG8_LDA(dst, b, h) do { _Pragma("unroll") for (int m = 0; m < 4; ++m) _Pragma("unroll") for (int k = 0; k < 2; ++k) dst[m][k] = *(const LAS bf16x8*)(lds + PG8_SA(b, h) + aoff + m * 2048 + k * 1024); } while (0)
; #define PG8_MMA(ai, bj, At, Bt) do { __builtin_amdgcn_s_setprio(1); _Pragma("unroll") for (int m = 0; m < 4; ++m) _Pragma("unroll") for (int n = 0; n < 2; ++n) _Pragma("unroll") for (int k = 0; k < 2; ++k) \
;         acc[ai][bj][m][n] = __builtin_amdgcn_mfma_f32_16x16x32_bf16(Bt[n][k], At[m][k], acc[ai][bj][m][n], 0, 0, 0); __builtin_amdgcn_s_setprio(0); } while (0)
; #define PG8_WAIT_V(n) asm volatile("s_waitcnt vmcnt(" #n ")" ::: "memory")
; #define PG8_WAIT_L(n) asm volatile("s_waitcnt lgkmcnt(" #n ")" ::: "memory")
; #define PG8_BAR __builtin_amdgcn_s_barrier()
; #define PG8_SCHED __builtin_amdgcn_sched_barrier(0)
; template <class Epi, class Sched>
; __device__ __forceinline__ void gemm_phase(LAS unsigned char* lds, const Gemm g, const Sched& S, const Epi& E, const int tid, unsigned* last_sig = nullptr) {
;     ...
;             PG8_LDA(At, 1, 1); PG8_STAGE(PG8_SB(1, 0), b3, voffB); PG8_STAGE(PG8_SB(1, 1), b3 + hstep, voffB); PG8_STAGE(PG8_SA(1, 0), a3, voffA);
;             PG8_WAIT_V(8); PG8_WAIT_L(0); PG8_BAR; PG8_MMA(1, 0, At, B0); PG8_MMA(1, 1, At, B1); PG8_BAR; PG8_SCHED;
;         }
;         if (wr == 0) PG8_BAR;
	s_add_i32 s14, s53, s42
	v_lshl_add_u64 v[218:219], v[218:219], 0, s[34:35]
	s_mov_b32 m0, s14
	ds_read_b128 v[162:165], v234 offset:49152
	ds_read_b128 v[166:169], v234 offset:50176
	ds_read_b128 v[170:173], v234 offset:51200
	ds_read_b128 v[174:177], v234 offset:52224
	ds_read_b128 v[178:181], v234 offset:53248
	ds_read_b128 v[182:185], v234 offset:54272
	ds_read_b128 v[210:213], v234 offset:55296
	ds_read_b128 v[214:217], v234 offset:56320
	global_load_lds_dwordx4 v[218:219], off
	s_add_i32 m0, s14, 0x2000
	s_add_u32 s14, s38, 0x40080
	v_lshl_add_u64 v[218:219], v[220:221], 0, s[34:35]
	s_addc_u32 s15, s39, 0
	s_add_i32 s38, s54, s42
	global_load_lds_dwordx4 v[218:219], off
	v_lshl_add_u64 v[218:219], s[14:15], 0, v[186:187]
	s_mov_b32 m0, s38
	s_nop 0
	global_load_lds_dwordx4 v[218:219], off
	v_lshl_add_u64 v[218:219], s[14:15], 0, v[204:205]
	s_add_i32 m0, s38, 0x2000
	s_nop 0
	global_load_lds_dwordx4 v[218:219], off
	v_lshl_add_u64 v[218:219], v[222:223], 0, s[34:35]
	s_mov_b32 m0, s46
	s_nop 0
	global_load_lds_dwordx4 v[218:219], off
	v_lshl_add_u64 v[218:219], v[236:237], 0, s[34:35]
	s_mov_b32 m0, s47
	s_nop 0
	global_load_lds_dwordx4 v[218:219], off
	s_waitcnt vmcnt(8)
	s_waitcnt lgkmcnt(0)
	s_barrier
	s_setprio 1
	s_waitcnt lgkmcnt(0)
	v_mfma_f32_16x16x32_bf16 v[58:61], v[130:133], v[162:165], v[58:61]
	v_mfma_f32_16x16x32_bf16 v[62:65], v[138:141], v[162:165], v[62:65]
	v_mfma_f32_16x16x32_bf16 v[42:45], v[130:133], v[170:173], v[42:45]
	v_mfma_f32_16x16x32_bf16 v[46:49], v[138:141], v[170:173], v[46:49]
	v_mfma_f32_16x16x32_bf16 v[26:29], v[130:133], v[178:181], v[26:29]
	v_mfma_f32_16x16x32_bf16 v[30:33], v[138:141], v[178:181], v[30:33]
	v_mfma_f32_16x16x32_bf16 v[10:13], v[130:133], v[210:213], v[10:13]
	v_mfma_f32_16x16x32_bf16 v[14:17], v[138:141], v[210:213], v[14:17]
	v_mfma_f32_16x16x32_bf16 v[58:61], v[134:137], v[166:169], v[58:61]
	v_mfma_f32_16x16x32_bf16 v[62:65], v[142:145], v[166:169], v[62:65]
	v_mfma_f32_16x16x32_bf16 v[42:45], v[134:137], v[174:177], v[42:45]
	v_mfma_f32_16x16x32_bf16 v[46:49], v[142:145], v[174:177], v[46:49]
	v_mfma_f32_16x16x32_bf16 v[26:29], v[134:137], v[182:185], v[26:29]
	v_mfma_f32_16x16x32_bf16 v[30:33], v[142:145], v[182:185], v[30:33]
	v_mfma_f32_16x16x32_bf16 v[10:13], v[134:137], v[214:217], v[10:13]
	v_mfma_f32_16x16x32_bf16 v[14:17], v[142:145], v[214:217], v[14:17]
	v_mfma_f32_16x16x32_bf16 v[50:53], v[146:149], v[162:165], v[50:53]
	v_mfma_f32_16x16x32_bf16 v[54:57], v[154:157], v[162:165], v[54:57]
	v_mfma_f32_16x16x32_bf16 v[34:37], v[146:149], v[170:173], v[34:37]
	v_mfma_f32_16x16x32_bf16 v[38:41], v[154:157], v[170:173], v[38:41]
	v_mfma_f32_16x16x32_bf16 v[18:21], v[146:149], v[178:181], v[18:21]
	v_mfma_f32_16x16x32_bf16 v[22:25], v[154:157], v[178:181], v[22:25]
	v_mfma_f32_16x16x32_bf16 v[2:5], v[146:149], v[210:213], v[2:5]
	v_mfma_f32_16x16x32_bf16 v[6:9], v[154:157], v[210:213], v[6:9]
	v_mfma_f32_16x16x32_bf16 v[50:53], v[150:153], v[166:169], v[50:53]
	v_mfma_f32_16x16x32_bf16 v[54:57], v[158:161], v[166:169], v[54:57]
	v_mfma_f32_16x16x32_bf16 v[34:37], v[150:153], v[174:177], v[34:37]
	v_mfma_f32_16x16x32_bf16 v[38:41], v[158:161], v[174:177], v[38:41]
	v_mfma_f32_16x16x32_bf16 v[18:21], v[150:153], v[182:185], v[18:21]
	v_mfma_f32_16x16x32_bf16 v[22:25], v[158:161], v[182:185], v[22:25]
	v_mfma_f32_16x16x32_bf16 v[2:5], v[150:153], v[214:217], v[2:5]
	v_mfma_f32_16x16x32_bf16 v[6:9], v[158:161], v[214:217], v[6:9]
	s_setprio 0
	s_barrier
	s_add_i32 s52, s52, 2
	s_add_u32 s22, s22, 0x100
	s_addc_u32 s23, s23, 0
	s_add_u32 s50, s50, 0x100
	s_addc_u32 s51, s51, 0
	s_cmp_gt_u32 s52, 13
	s_cbranch_scc0 .LBB0_618
	s_and_b64 vcc, exec, s[6:7]
	s_cbranch_vccz .LBB0_621
	s_barrier

; #define PG8_STAGE(bufoff, gbase, voff) do { _Pragma("unroll") for (int _i = 0; _i < 2; ++_i) \
;         __builtin_amdgcn_global_load_lds((const unsigned*)((const char*)(gbase) + (voff)[_i]), (LAS unsigned*)(lds + (bufoff) + ldsw + _i * 8192), 16, 0, 0); } while (0)
; #define PG8_LDA(dst, b, h) do { _Pragma("unroll") for (int m = 0; m < 4; ++m) _Pragma("unroll") for (int k = 0; k < 2; ++k) dst[m][k] = *(const LAS bf16x8*)(lds + PG8_SA(b, h) + aoff + m * 2048 + k * 1024); } while (0)
; #define PG8_LDB(dst, b, h) do { _Pragma("unroll") for (int n = 0; n < 2; ++n) _Pragma("unroll") for (int k = 0; k < 2; ++k) dst[n][k] = *(const LAS bf16x8*)(lds + PG8_SB(b, h) + boff + n * 2048 + k * 1024); } while (0)
; #define PG8_MMA(ai, bj, At, Bt) do { __builtin_amdgcn_s_setprio(1); _Pragma("unroll") for (int m = 0; m < 4; ++m) _Pragma("unroll") for (int n = 0; n < 2; ++n) _Pragma("unroll") for (int k = 0; k < 2; ++k) \
;         acc[ai][bj][m][n] = __builtin_amdgcn_mfma_f32_16x16x32_bf16(Bt[n][k], At[m][k], acc[ai][bj][m][n], 0, 0, 0); __builtin_amdgcn_s_setprio(0); } while (0)
; #define PG8_BAR __builtin_amdgcn_s_barrier()
; template <class Epi, class Sched>
; __device__ __forceinline__ void gemm_phase(LAS unsigned char* lds, const Gemm g, const Sched& S, const Epi& E, const int tid, unsigned* last_sig = nullptr) {
;     ...
;         const char* nA = has_next ? (const char*)g.A + (size_t)nxt.pm * tstep : cA; const char* nB = has_next ? (const char*)g.Bt + (size_t)nxt.be * g.bstride + (size_t)nxt.pn * tstep : cB;
;         for (int t = 0; t < nt; t += 2) {
;             const bool last = (t == nt - 2);
;             const char* a1 = cA + (size_t)(t + 1) * kstep;
;             const char* a2 = last ? nA : cA + (size_t)(t + 2) * kstep; const char* b2 = last ? nB : cB + (size_t)(t + 2) * kstep;
;             const char* a3 = a2 + kstep; const char* b3 = b2 + kstep;
;             PG8_LDB(B0, 0, 0); PG8_LDB(B1, 0, 1); PG8_SCHED; PG8_LDA(At, 0, 0); PG8_STAGE(PG8_SA(1, 1), a1 + hstep, voffA);
;             PG8_WAIT_V(8); PG8_WAIT_L(0); PG8_BAR; PG8_MMA(0, 0, At, B0); PG8_MMA(0, 1, At, B1); PG8_BAR; PG8_SCHED;
;             PG8_LDA(At, 0, 1); PG8_STAGE(PG8_SB(0, 0), b2, voffB); PG8_STAGE(PG8_SB(0, 1), b2 + hstep, voffB); PG8_STAGE(PG8_SA(0, 0), a2, voffA);
;             PG8_WAIT_V(8); PG8_WAIT_L(0); PG8_BAR; PG8_MMA(1, 0, At, B0); PG8_MMA(1, 1, At, B1); PG8_BAR; PG8_SCHED;
.LBB0_691:
	s_add_u32 s22, s20, 0x100
	s_addc_u32 s23, s21, 0
	s_add_i32 s14, 0, 0x10000
	s_cmp_eq_u32 s56, 28
	s_cselect_b32 s41, s13, s23
	s_cselect_b32 s40, s52, s22
	s_cselect_b32 s39, s11, s55
	s_cselect_b32 s38, s53, s54
	s_add_i32 s57, 0, 0x14000
	v_add_u32_e32 v148, s14, v156
	v_add_u32_e32 v159, s57, v156
	ds_read_b128 v[130:133], v148
	ds_read_b128 v[134:137], v148 offset:1024
	ds_read_b128 v[138:141], v148 offset:2048
	ds_read_b128 v[148:151], v148 offset:3072
	ds_read_b128 v[152:155], v159
	ds_read_b128 v[160:163], v159 offset:1024
	ds_read_b128 v[164:167], v159 offset:2048
	ds_read_b128 v[168:171], v159 offset:3072
	v_lshl_add_u64 v[184:185], s[20:21], 0, v[144:145]
	s_add_i32 m0, s43, 0xc000
	ds_read_b128 v[172:175], v158
	ds_read_b128 v[176:179], v158 offset:1024
	ds_read_b128 v[180:183], v158 offset:2048
	ds_read_b128 v[200:203], v158 offset:3072
	ds_read_b128 v[204:207], v158 offset:4096
	ds_read_b128 v[208:211], v158 offset:5120
	ds_read_b128 v[212:215], v158 offset:6144
	ds_read_b128 v[216:219], v158 offset:7168
	global_load_lds_dwordx4 v[184:185], off
	v_lshl_add_u64 v[184:185], s[20:21], 0, v[146:147]
	s_add_i32 m0, s43, 0xe000
	s_nop 0
	global_load_lds_dwordx4 v[184:185], off
	s_waitcnt vmcnt(8)
	s_waitcnt lgkmcnt(0)
	s_barrier
	s_setprio 1
	s_waitcnt lgkmcnt(0)
	v_mfma_f32_16x16x32_bf16 v[126:129], v[130:133], v[172:175], v[126:129]
	v_mfma_f32_16x16x32_bf16 v[122:125], v[138:141], v[172:175], v[122:125]
	v_mfma_f32_16x16x32_bf16 v[118:121], v[130:133], v[180:183], v[118:121]
	v_mfma_f32_16x16x32_bf16 v[106:109], v[138:141], v[180:183], v[106:109]
	v_mfma_f32_16x16x32_bf16 v[102:105], v[130:133], v[204:207], v[102:105]
	v_mfma_f32_16x16x32_bf16 v[90:93], v[138:141], v[204:207], v[90:93]
	v_mfma_f32_16x16x32_bf16 v[86:89], v[130:133], v[212:215], v[86:89]
	v_mfma_f32_16x16x32_bf16 v[74:77], v[138:141], v[212:215], v[74:77]
	v_mfma_f32_16x16x32_bf16 v[126:129], v[134:137], v[176:179], v[126:129]
	v_mfma_f32_16x16x32_bf16 v[122:125], v[148:151], v[176:179], v[122:125]
	v_mfma_f32_16x16x32_bf16 v[118:121], v[134:137], v[200:203], v[118:121]
	v_mfma_f32_16x16x32_bf16 v[106:109], v[148:151], v[200:203], v[106:109]
	v_mfma_f32_16x16x32_bf16 v[102:105], v[134:137], v[208:211], v[102:105]
	v_mfma_f32_16x16x32_bf16 v[90:93], v[148:151], v[208:211], v[90:93]
	v_mfma_f32_16x16x32_bf16 v[86:89], v[134:137], v[216:219], v[86:89]
	v_mfma_f32_16x16x32_bf16 v[74:77], v[148:151], v[216:219], v[74:77]
	v_mfma_f32_16x16x32_bf16 v[114:117], v[152:155], v[172:175], v[114:117]
	v_mfma_f32_16x16x32_bf16 v[110:113], v[164:167], v[172:175], v[110:113]
	v_mfma_f32_16x16x32_bf16 v[98:101], v[152:155], v[180:183], v[98:101]
	v_mfma_f32_16x16x32_bf16 v[94:97], v[164:167], v[180:183], v[94:97]
	v_mfma_f32_16x16x32_bf16 v[82:85], v[152:155], v[204:207], v[82:85]
	v_mfma_f32_16x16x32_bf16 v[78:81], v[164:167], v[204:207], v[78:81]
	v_mfma_f32_16x16x32_bf16 v[70:73], v[152:155], v[212:215], v[70:73]
	v_mfma_f32_16x16x32_bf16 v[66:69], v[164:167], v[212:215], v[66:69]
	v_mfma_f32_16x16x32_bf16 v[114:117], v[160:163], v[176:179], v[114:117]
	v_mfma_f32_16x16x32_bf16 v[110:113], v[168:171], v[176:179], v[110:113]
	v_mfma_f32_16x16x32_bf16 v[98:101], v[160:163], v[200:203], v[98:101]
	v_mfma_f32_16x16x32_bf16 v[94:97], v[168:171], v[200:203], v[94:97]
	v_mfma_f32_16x16x32_bf16 v[82:85], v[160:163], v[208:211], v[82:85]
	v_mfma_f32_16x16x32_bf16 v[78:81], v[168:171], v[208:211], v[78:81]
	v_mfma_f32_16x16x32_bf16 v[70:73], v[160:163], v[216:219], v[70:73]
	v_mfma_f32_16x16x32_bf16 v[66:69], v[168:171], v[216:219], v[66:69]
	s_setprio 0
	s_barrier
	s_add_i32 s14, s14, s42
	v_lshl_add_u64 v[184:185], s[38:39], 0, v[186:187]
	s_mov_b32 m0, s14
	ds_read_b128 v[172:175], v158 offset:16384
	ds_read_b128 v[176:179], v158 offset:17408
	ds_read_b128 v[180:183], v158 offset:18432
	ds_read_b128 v[200:203], v158 offset:19456
	ds_read_b128 v[204:207], v158 offset:20480
	ds_read_b128 v[208:211], v158 offset:21504
	ds_read_b128 v[212:215], v158 offset:22528
	ds_read_b128 v[216:219], v158 offset:23552
	global_load_lds_dwordx4 v[184:185], off
	s_add_i32 m0, s14, 0x2000
	s_add_u32 s14, s38, 0x80000
	v_lshl_add_u64 v[220:221], s[38:39], 0, v[142:143]
	s_addc_u32 s15, s39, 0
	s_add_i32 s20, s57, s42
	global_load_lds_dwordx4 v[220:221], off
	v_lshl_add_u64 v[222:223], s[14:15], 0, v[186:187]
	s_mov_b32 m0, s20
	v_lshl_add_u64 v[232:233], s[40:41], 0, v[142:143]
	global_load_lds_dwordx4 v[222:223], off
	v_lshl_add_u64 v[222:223], s[14:15], 0, v[142:143]
	s_add_i32 m0, s20, 0x2000
	s_nop 0
	global_load_lds_dwordx4 v[222:223], off
	v_lshl_add_u64 v[222:223], s[40:41], 0, v[186:187]
	s_mov_b32 m0, s43
	s_nop 0
	global_load_lds_dwordx4 v[222:223], off
	s_mov_b32 m0, s44
	s_nop 0
	global_load_lds_dwordx4 v[232:233], off
	s_waitcnt vmcnt(8)
	s_waitcnt lgkmcnt(0)
	s_barrier
; #define PG8_STAGE(bufoff, gbase, voff) do { _Pragma("unroll") for (int _i = 0; _i < 2; ++_i) \
;         __builtin_amdgcn_global_load_lds((const unsigned*)((const char*)(gbase) + (voff)[_i]), (LAS unsigned*)(lds + (bufoff) + ldsw + _i * 8192), 16, 0, 0); } while (0)
; #define PG8_LDA(dst, b, h) do { _Pragma("unroll") for (int m = 0; m < 4; ++m) _Pragma("unroll") for (int k = 0; k < 2; ++k) dst[m][k] = *(const LAS bf16x8*)(lds + PG8_SA(b, h) + aoff + m * 2048 + k * 1024); } while (0)
; #define PG8_LDB(dst, b, h) do { _Pragma("unroll") for (int n = 0; n < 2; ++n) _Pragma("unroll") for (int k = 0; k < 2; ++k) dst[n][k] = *(const LAS bf16x8*)(lds + PG8_SB(b, h) + boff + n * 2048 + k * 1024); } while (0)
; #define PG8_MMA(ai, bj, At, Bt) do { __builtin_amdgcn_s_setprio(1); _Pragma("unroll") for (int m = 0; m < 4; ++m) _Pragma("unroll") for (int n = 0; n < 2; ++n) _Pragma("unroll") for (int k = 0; k < 2; ++k) \
;         acc[ai][bj][m][n] = __builtin_amdgcn_mfma_f32_16x16x32_bf16(Bt[n][k], At[m][k], acc[ai][bj][m][n], 0, 0, 0); __builtin_amdgcn_s_setprio(0); } while (0)
; #define PG8_WAIT_V(n) asm volatile("s_waitcnt vmcnt(" #n ")" ::: "memory")
; #define PG8_WAIT_L(n) asm volatile("s_waitcnt lgkmcnt(" #n ")" ::: "memory")
; #define PG8_BAR __builtin_amdgcn_s_barrier()
; #define PG8_SCHED __builtin_amdgcn_sched_barrier(0)
; template <class Epi, class Sched>
; __device__ __forceinline__ void gemm_phase(LAS unsigned char* lds, const Gemm g, const Sched& S, const Epi& E, const int tid, unsigned* last_sig = nullptr) {
;     ...
;             PG8_WAIT_V(8); PG8_WAIT_L(0); PG8_BAR; PG8_MMA(1, 0, At, B0); PG8_MMA(1, 1, At, B1); PG8_BAR; PG8_SCHED;
;             PG8_LDB(B0, 1, 0); PG8_LDB(B1, 1, 1); PG8_SCHED; PG8_LDA(At, 1, 0); PG8_STAGE(PG8_SA(0, 1), a2 + hstep, voffA);
;             PG8_WAIT_V(8); PG8_WAIT_L(0); PG8_BAR; PG8_MMA(0, 0, At, B0); PG8_MMA(0, 1, At, B1); PG8_BAR; PG8_SCHED;
	s_setprio 1
	s_waitcnt lgkmcnt(0)
	v_mfma_f32_16x16x32_bf16 v[62:65], v[130:133], v[172:175], v[62:65]
	v_mfma_f32_16x16x32_bf16 v[58:61], v[138:141], v[172:175], v[58:61]
	v_mfma_f32_16x16x32_bf16 v[54:57], v[130:133], v[180:183], v[54:57]
	v_mfma_f32_16x16x32_bf16 v[42:45], v[138:141], v[180:183], v[42:45]
	v_mfma_f32_16x16x32_bf16 v[38:41], v[130:133], v[204:207], v[38:41]
	v_mfma_f32_16x16x32_bf16 v[26:29], v[138:141], v[204:207], v[26:29]
	v_mfma_f32_16x16x32_bf16 v[22:25], v[130:133], v[212:215], v[22:25]
	v_mfma_f32_16x16x32_bf16 v[10:13], v[138:141], v[212:215], v[10:13]
	v_mfma_f32_16x16x32_bf16 v[62:65], v[134:137], v[176:179], v[62:65]
	v_mfma_f32_16x16x32_bf16 v[58:61], v[148:151], v[176:179], v[58:61]
	v_mfma_f32_16x16x32_bf16 v[54:57], v[134:137], v[200:203], v[54:57]
	v_mfma_f32_16x16x32_bf16 v[42:45], v[148:151], v[200:203], v[42:45]
	v_mfma_f32_16x16x32_bf16 v[38:41], v[134:137], v[208:211], v[38:41]
	v_mfma_f32_16x16x32_bf16 v[26:29], v[148:151], v[208:211], v[26:29]
	v_mfma_f32_16x16x32_bf16 v[22:25], v[134:137], v[216:219], v[22:25]
	v_mfma_f32_16x16x32_bf16 v[10:13], v[148:151], v[216:219], v[10:13]
	v_mfma_f32_16x16x32_bf16 v[50:53], v[152:155], v[172:175], v[50:53]
	v_mfma_f32_16x16x32_bf16 v[46:49], v[164:167], v[172:175], v[46:49]
	v_mfma_f32_16x16x32_bf16 v[34:37], v[152:155], v[180:183], v[34:37]
	v_mfma_f32_16x16x32_bf16 v[30:33], v[164:167], v[180:183], v[30:33]
	v_mfma_f32_16x16x32_bf16 v[18:21], v[152:155], v[204:207], v[18:21]
	v_mfma_f32_16x16x32_bf16 v[14:17], v[164:167], v[204:207], v[14:17]
	v_mfma_f32_16x16x32_bf16 v[6:9], v[152:155], v[212:215], v[6:9]
	v_mfma_f32_16x16x32_bf16 v[2:5], v[164:167], v[212:215], v[2:5]
	v_mfma_f32_16x16x32_bf16 v[50:53], v[160:163], v[176:179], v[50:53]
	v_mfma_f32_16x16x32_bf16 v[46:49], v[168:171], v[176:179], v[46:49]
	v_mfma_f32_16x16x32_bf16 v[34:37], v[160:163], v[200:203], v[34:37]
	v_mfma_f32_16x16x32_bf16 v[30:33], v[168:171], v[200:203], v[30:33]
	v_mfma_f32_16x16x32_bf16 v[18:21], v[160:163], v[208:211], v[18:21]
	v_mfma_f32_16x16x32_bf16 v[14:17], v[168:171], v[208:211], v[14:17]
	v_mfma_f32_16x16x32_bf16 v[6:9], v[160:163], v[216:219], v[6:9]
	v_mfma_f32_16x16x32_bf16 v[2:5], v[168:171], v[216:219], v[2:5]
	s_setprio 0
	s_barrier
	s_add_i32 s20, 0, 0x18000
	s_add_i32 s21, 0, 0x1c000
	v_add_u32_e32 v148, s20, v156
	v_add_u32_e32 v159, s21, v156
	ds_read_b128 v[130:133], v148
	ds_read_b128 v[134:137], v148 offset:1024
	ds_read_b128 v[138:141], v148 offset:2048
	ds_read_b128 v[148:151], v148 offset:3072
	ds_read_b128 v[152:155], v159
	ds_read_b128 v[160:163], v159 offset:1024
	ds_read_b128 v[164:167], v159 offset:2048
	ds_read_b128 v[168:171], v159 offset:3072
	s_add_u32 s14, s40, 0x80000
	s_addc_u32 s15, s41, 0
	s_mov_b32 m0, s45
	v_lshl_add_u64 v[234:235], s[14:15], 0, v[186:187]
	ds_read_b128 v[172:175], v158 offset:32768
	ds_read_b128 v[176:179], v158 offset:33792
	ds_read_b128 v[180:183], v158 offset:34816
	ds_read_b128 v[200:203], v158 offset:35840
	ds_read_b128 v[204:207], v158 offset:36864
	ds_read_b128 v[208:211], v158 offset:37888
	ds_read_b128 v[212:215], v158 offset:38912
	ds_read_b128 v[216:219], v158 offset:39936
	global_load_lds_dwordx4 v[234:235], off
	v_lshl_add_u64 v[234:235], s[14:15], 0, v[142:143]
	s_mov_b32 m0, s46
	s_nop 0
	global_load_lds_dwordx4 v[234:235], off
	s_waitcnt vmcnt(8)
	s_waitcnt lgkmcnt(0)
	s_barrier
	s_setprio 1
	s_waitcnt lgkmcnt(0)
	v_mfma_f32_16x16x32_bf16 v[126:129], v[130:133], v[172:175], v[126:129]
	v_mfma_f32_16x16x32_bf16 v[122:125], v[138:141], v[172:175], v[122:125]
	v_mfma_f32_16x16x32_bf16 v[118:121], v[130:133], v[180:183], v[118:121]
	v_mfma_f32_16x16x32_bf16 v[106:109], v[138:141], v[180:183], v[106:109]
	v_mfma_f32_16x16x32_bf16 v[102:105], v[130:133], v[204:207], v[102:105]
	v_mfma_f32_16x16x32_bf16 v[90:93], v[138:141], v[204:207], v[90:93]
	v_mfma_f32_16x16x32_bf16 v[86:89], v[130:133], v[212:215], v[86:89]
	v_mfma_f32_16x16x32_bf16 v[74:77], v[138:141], v[212:215], v[74:77]
	v_mfma_f32_16x16x32_bf16 v[126:129], v[134:137], v[176:179], v[126:129]
	v_mfma_f32_16x16x32_bf16 v[122:125], v[148:151], v[176:179], v[122:125]
	v_mfma_f32_16x16x32_bf16 v[118:121], v[134:137], v[200:203], v[118:121]
	v_mfma_f32_16x16x32_bf16 v[106:109], v[148:151], v[200:203], v[106:109]
	v_mfma_f32_16x16x32_bf16 v[102:105], v[134:137], v[208:211], v[102:105]
	v_mfma_f32_16x16x32_bf16 v[90:93], v[148:151], v[208:211], v[90:93]
	v_mfma_f32_16x16x32_bf16 v[86:89], v[134:137], v[216:219], v[86:89]
	v_mfma_f32_16x16x32_bf16 v[74:77], v[148:151], v[216:219], v[74:77]
	v_mfma_f32_16x16x32_bf16 v[114:117], v[152:155], v[172:175], v[114:117]
	v_mfma_f32_16x16x32_bf16 v[110:113], v[164:167], v[172:175], v[110:113]
	v_mfma_f32_16x16x32_bf16 v[98:101], v[152:155], v[180:183], v[98:101]
	v_mfma_f32_16x16x32_bf16 v[94:97], v[164:167], v[180:183], v[94:97]
	v_mfma_f32_16x16x32_bf16 v[82:85], v[152:155], v[204:207], v[82:85]
	v_mfma_f32_16x16x32_bf16 v[78:81], v[164:167], v[204:207], v[78:81]
	v_mfma_f32_16x16x32_bf16 v[70:73], v[152:155], v[212:215], v[70:73]
	v_mfma_f32_16x16x32_bf16 v[66:69], v[164:167], v[212:215], v[66:69]
	v_mfma_f32_16x16x32_bf16 v[114:117], v[160:163], v[176:179], v[114:117]
	v_mfma_f32_16x16x32_bf16 v[110:113], v[168:171], v[176:179], v[110:113]
	v_mfma_f32_16x16x32_bf16 v[98:101], v[160:163], v[200:203], v[98:101]
	v_mfma_f32_16x16x32_bf16 v[94:97], v[168:171], v[200:203], v[94:97]
	v_mfma_f32_16x16x32_bf16 v[82:85], v[160:163], v[208:211], v[82:85]
	v_mfma_f32_16x16x32_bf16 v[78:81], v[168:171], v[208:211], v[78:81]
	v_mfma_f32_16x16x32_bf16 v[70:73], v[160:163], v[216:219], v[70:73]
	v_mfma_f32_16x16x32_bf16 v[66:69], v[168:171], v[216:219], v[66:69]
	s_setprio 0
	s_barrier
; #define PG8_STAGE(bufoff, gbase, voff) do { _Pragma("unroll") for (int _i = 0; _i < 2; ++_i) \
;         __builtin_amdgcn_global_load_lds((const unsigned*)((const char*)(gbase) + (voff)[_i]), (LAS unsigned*)(lds + (bufoff) + ldsw + _i * 8192), 16, 0, 0); } while (0)
; #define PG8_LDA(dst, b, h) do { _Pragma("unroll") for (int m = 0; m < 4; ++m) _Pragma("unroll") for (int k = 0; k < 2; ++k) dst[m][k] = *(const LAS bf16x8*)(lds + PG8_SA(b, h) + aoff + m * 2048 + k * 1024); } while (0)
; #define PG8_MMA(ai, bj, At, Bt) do { __builtin_amdgcn_s_setprio(1); _Pragma("unroll") for (int m = 0; m < 4; ++m) _Pragma("unroll") for (int n = 0; n < 2; ++n) _Pragma("unroll") for (int k = 0; k < 2; ++k) \
;         acc[ai][bj][m][n] = __builtin_amdgcn_mfma_f32_16x16x32_bf16(Bt[n][k], At[m][k], acc[ai][bj][m][n], 0, 0, 0); __builtin_amdgcn_s_setprio(0); } while (0)
; #define PG8_WAIT_V(n) asm volatile("s_waitcnt vmcnt(" #n ")" ::: "memory")
; #define PG8_WAIT_L(n) asm volatile("s_waitcnt lgkmcnt(" #n ")" ::: "memory")
; #define PG8_BAR __builtin_amdgcn_s_barrier()
; #define PG8_SCHED __builtin_amdgcn_sched_barrier(0)
; template <class Epi, class Sched>
; __device__ __forceinline__ void gemm_phase(LAS unsigned char* lds, const Gemm g, const Sched& S, const Epi& E, const int tid, unsigned* last_sig = nullptr) {
;     ...
;             PG8_LDA(At, 1, 1); PG8_STAGE(PG8_SB(1, 0), b3, voffB); PG8_STAGE(PG8_SB(1, 1), b3 + hstep, voffB); PG8_STAGE(PG8_SA(1, 0), a3, voffA);
;             PG8_WAIT_V(8); PG8_WAIT_L(0); PG8_BAR; PG8_MMA(1, 0, At, B0); PG8_MMA(1, 1, At, B1); PG8_BAR; PG8_SCHED;
;         }
;         if (wr == 0) PG8_BAR;
;         E(acc, cur, wr, wc, fr, fq);
;         if (!has_next) break;
	s_add_i32 s14, s20, s42
	v_lshl_add_u64 v[184:185], v[184:185], 0, s[34:35]
	s_mov_b32 m0, s14
	ds_read_b128 v[172:175], v158 offset:49152
	ds_read_b128 v[176:179], v158 offset:50176
	ds_read_b128 v[180:183], v158 offset:51200
	ds_read_b128 v[200:203], v158 offset:52224
	ds_read_b128 v[204:207], v158 offset:53248
	ds_read_b128 v[208:211], v158 offset:54272
	ds_read_b128 v[212:215], v158 offset:55296
	ds_read_b128 v[216:219], v158 offset:56320
	global_load_lds_dwordx4 v[184:185], off
	s_add_i32 m0, s14, 0x2000
	s_add_u32 s14, s38, 0x80080
	v_lshl_add_u64 v[184:185], v[220:221], 0, s[34:35]
	s_addc_u32 s15, s39, 0
	s_add_i32 s20, s21, s42
	global_load_lds_dwordx4 v[184:185], off
	v_lshl_add_u64 v[184:185], s[14:15], 0, v[186:187]
	s_mov_b32 m0, s20
	s_nop 0
	global_load_lds_dwordx4 v[184:185], off
	v_lshl_add_u64 v[184:185], s[14:15], 0, v[142:143]
	s_add_i32 m0, s20, 0x2000
	s_nop 0
	global_load_lds_dwordx4 v[184:185], off
	v_lshl_add_u64 v[184:185], v[222:223], 0, s[34:35]
	s_mov_b32 m0, s47
	s_nop 0
	global_load_lds_dwordx4 v[184:185], off
	v_lshl_add_u64 v[184:185], v[232:233], 0, s[34:35]
	s_mov_b32 m0, s48
	s_nop 0
	global_load_lds_dwordx4 v[184:185], off
	s_waitcnt vmcnt(8)
	s_waitcnt lgkmcnt(0)
	s_barrier
	s_setprio 1
	s_waitcnt lgkmcnt(0)
	v_mfma_f32_16x16x32_bf16 v[62:65], v[130:133], v[172:175], v[62:65]
	v_mfma_f32_16x16x32_bf16 v[58:61], v[138:141], v[172:175], v[58:61]
	v_mfma_f32_16x16x32_bf16 v[54:57], v[130:133], v[180:183], v[54:57]
	v_mfma_f32_16x16x32_bf16 v[42:45], v[138:141], v[180:183], v[42:45]
	v_mfma_f32_16x16x32_bf16 v[38:41], v[130:133], v[204:207], v[38:41]
	v_mfma_f32_16x16x32_bf16 v[26:29], v[138:141], v[204:207], v[26:29]
	v_mfma_f32_16x16x32_bf16 v[22:25], v[130:133], v[212:215], v[22:25]
	v_mfma_f32_16x16x32_bf16 v[10:13], v[138:141], v[212:215], v[10:13]
	v_mfma_f32_16x16x32_bf16 v[62:65], v[134:137], v[176:179], v[62:65]
	v_mfma_f32_16x16x32_bf16 v[58:61], v[148:151], v[176:179], v[58:61]
	v_mfma_f32_16x16x32_bf16 v[54:57], v[134:137], v[200:203], v[54:57]
	v_mfma_f32_16x16x32_bf16 v[42:45], v[148:151], v[200:203], v[42:45]
	v_mfma_f32_16x16x32_bf16 v[38:41], v[134:137], v[208:211], v[38:41]
	v_mfma_f32_16x16x32_bf16 v[26:29], v[148:151], v[208:211], v[26:29]
	v_mfma_f32_16x16x32_bf16 v[22:25], v[134:137], v[216:219], v[22:25]
	v_mfma_f32_16x16x32_bf16 v[10:13], v[148:151], v[216:219], v[10:13]
	v_mfma_f32_16x16x32_bf16 v[50:53], v[152:155], v[172:175], v[50:53]
	v_mfma_f32_16x16x32_bf16 v[46:49], v[164:167], v[172:175], v[46:49]
	v_mfma_f32_16x16x32_bf16 v[34:37], v[152:155], v[180:183], v[34:37]
	v_mfma_f32_16x16x32_bf16 v[30:33], v[164:167], v[180:183], v[30:33]
	v_mfma_f32_16x16x32_bf16 v[18:21], v[152:155], v[204:207], v[18:21]
	v_mfma_f32_16x16x32_bf16 v[14:17], v[164:167], v[204:207], v[14:17]
	v_mfma_f32_16x16x32_bf16 v[6:9], v[152:155], v[212:215], v[6:9]
	v_mfma_f32_16x16x32_bf16 v[2:5], v[164:167], v[212:215], v[2:5]
	v_mfma_f32_16x16x32_bf16 v[50:53], v[160:163], v[176:179], v[50:53]
	v_mfma_f32_16x16x32_bf16 v[46:49], v[168:171], v[176:179], v[46:49]
	v_mfma_f32_16x16x32_bf16 v[34:37], v[160:163], v[200:203], v[34:37]
	v_mfma_f32_16x16x32_bf16 v[30:33], v[168:171], v[200:203], v[30:33]
	v_mfma_f32_16x16x32_bf16 v[18:21], v[160:163], v[208:211], v[18:21]
	v_mfma_f32_16x16x32_bf16 v[14:17], v[168:171], v[208:211], v[14:17]
	v_mfma_f32_16x16x32_bf16 v[6:9], v[160:163], v[216:219], v[6:9]
	v_mfma_f32_16x16x32_bf16 v[2:5], v[168:171], v[216:219], v[2:5]
	s_setprio 0
	s_barrier
	s_add_i32 s56, s56, 2
	s_add_u32 s54, s54, 0x100
	s_addc_u32 s55, s55, 0
	s_cmp_gt_u32 s56, 29
	s_mov_b64 s[20:21], s[22:23]
	s_cbranch_scc0 .LBB0_691
	s_and_b64 vcc, exec, s[8:9]
	s_cbranch_vccz .LBB0_694
	s_barrier

; #define PG8_STAGE(bufoff, gbase, voff) do { _Pragma("unroll") for (int _i = 0; _i < 2; ++_i) \
;         __builtin_amdgcn_global_load_lds((const unsigned*)((const char*)(gbase) + (voff)[_i]), (LAS unsigned*)(lds + (bufoff) + ldsw + _i * 8192), 16, 0, 0); } while (0)
; #define PG8_LDA(dst, b, h) do { _Pragma("unroll") for (int m = 0; m < 4; ++m) _Pragma("unroll") for (int k = 0; k < 2; ++k) dst[m][k] = *(const LAS bf16x8*)(lds + PG8_SA(b, h) + aoff + m * 2048 + k * 1024); } while (0)
; #define PG8_LDB(dst, b, h) do { _Pragma("unroll") for (int n = 0; n < 2; ++n) _Pragma("unroll") for (int k = 0; k < 2; ++k) dst[n][k] = *(const LAS bf16x8*)(lds + PG8_SB(b, h) + boff + n * 2048 + k * 1024); } while (0)
; #define PG8_MMA(ai, bj, At, Bt) do { __builtin_amdgcn_s_setprio(1); _Pragma("unroll") for (int m = 0; m < 4; ++m) _Pragma("unroll") for (int n = 0; n < 2; ++n) _Pragma("unroll") for (int k = 0; k < 2; ++k) \
;         acc[ai][bj][m][n] = __builtin_amdgcn_mfma_f32_16x16x32_bf16(Bt[n][k], At[m][k], acc[ai][bj][m][n], 0, 0, 0); __builtin_amdgcn_s_setprio(0); } while (0)
; #define PG8_BAR __builtin_amdgcn_s_barrier()
; template <class Epi, class Sched>
; __device__ __forceinline__ void gemm_phase(LAS unsigned char* lds, const Gemm g, const Sched& S, const Epi& E, const int tid, unsigned* last_sig = nullptr) {
;     ...
;         const char* nA = has_next ? (const char*)g.A + (size_t)nxt.pm * tstep : cA; const char* nB = has_next ? (const char*)g.Bt + (size_t)nxt.be * g.bstride + (size_t)nxt.pn * tstep : cB;
;         for (int t = 0; t < nt; t += 2) {
;             const bool last = (t == nt - 2);
;             const char* a1 = cA + (size_t)(t + 1) * kstep;
;             const char* a2 = last ? nA : cA + (size_t)(t + 2) * kstep; const char* b2 = last ? nB : cB + (size_t)(t + 2) * kstep;
;             const char* a3 = a2 + kstep; const char* b3 = b2 + kstep;
;             PG8_LDB(B0, 0, 0); PG8_LDB(B1, 0, 1); PG8_SCHED; PG8_LDA(At, 0, 0); PG8_STAGE(PG8_SA(1, 1), a1 + hstep, voffA);
;             PG8_WAIT_V(8); PG8_WAIT_L(0); PG8_BAR; PG8_MMA(0, 0, At, B0); PG8_MMA(0, 1, At, B1); PG8_BAR; PG8_SCHED;
;             PG8_LDA(At, 0, 1); PG8_STAGE(PG8_SB(0, 0), b2, voffB); PG8_STAGE(PG8_SB(0, 1), b2 + hstep, voffB); PG8_STAGE(PG8_SA(0, 0), a2, voffA);
;             PG8_WAIT_V(8); PG8_WAIT_L(0); PG8_BAR; PG8_MMA(1, 0, At, B0); PG8_MMA(1, 1, At, B1); PG8_BAR; PG8_SCHED;
.LBB0_1104:
	s_add_u32 s14, s4, 0xfff80080
	s_addc_u32 s15, s5, -1
	s_add_i32 s59, 0, 0x10000
	s_cmp_eq_u32 s58, 28
	s_cselect_b32 s47, s17, s15
	s_cselect_b32 s46, s19, s14
	v_add_u32_e32 v140, s59, v143
	s_cselect_b32 s45, s21, s57
	s_cselect_b32 s44, s20, s56
	s_add_i32 s60, 0, 0x14000
	ds_read_b128 v[146:149], v140
	ds_read_b128 v[150:153], v140 offset:1024
	ds_read_b128 v[154:157], v140 offset:2048
	ds_read_b128 v[158:161], v140 offset:3072
	v_add_u32_e32 v140, s60, v143
	ds_read_b128 v[162:165], v140
	ds_read_b128 v[166:169], v140 offset:1024
	ds_read_b128 v[170:173], v140 offset:2048
	ds_read_b128 v[174:177], v140 offset:3072
	v_lshl_add_u64 v[140:141], s[4:5], 0, v[136:137]
	s_add_i32 m0, s41, 0xc000
	ds_read_b128 v[178:181], v145
	ds_read_b128 v[182:185], v145 offset:1024
	ds_read_b128 v[200:203], v145 offset:2048
	ds_read_b128 v[204:207], v145 offset:3072
	ds_read_b128 v[208:211], v145 offset:4096
	ds_read_b128 v[212:215], v145 offset:5120
	ds_read_b128 v[216:219], v145 offset:6144
	ds_read_b128 v[220:223], v145 offset:7168
	global_load_lds_dwordx4 v[140:141], off
	v_lshl_add_u64 v[140:141], s[4:5], 0, v[138:139]
	s_add_i32 m0, s41, 0xe000
	s_nop 0
	global_load_lds_dwordx4 v[140:141], off
	s_waitcnt vmcnt(8)
	s_waitcnt lgkmcnt(0)
	s_barrier
	s_setprio 1
	s_waitcnt lgkmcnt(0)
	v_mfma_f32_16x16x32_bf16 v[126:129], v[146:149], v[178:181], v[126:129]
	v_mfma_f32_16x16x32_bf16 v[118:121], v[154:157], v[178:181], v[118:121]
	v_mfma_f32_16x16x32_bf16 v[110:113], v[146:149], v[200:203], v[110:113]
	v_mfma_f32_16x16x32_bf16 v[102:105], v[154:157], v[200:203], v[102:105]
	v_mfma_f32_16x16x32_bf16 v[94:97], v[146:149], v[208:211], v[94:97]
	v_mfma_f32_16x16x32_bf16 v[86:89], v[154:157], v[208:211], v[86:89]
	v_mfma_f32_16x16x32_bf16 v[78:81], v[146:149], v[216:219], v[78:81]
	v_mfma_f32_16x16x32_bf16 v[70:73], v[154:157], v[216:219], v[70:73]
	v_mfma_f32_16x16x32_bf16 v[126:129], v[150:153], v[182:185], v[126:129]
	v_mfma_f32_16x16x32_bf16 v[118:121], v[158:161], v[182:185], v[118:121]
	v_mfma_f32_16x16x32_bf16 v[110:113], v[150:153], v[204:207], v[110:113]
	v_mfma_f32_16x16x32_bf16 v[102:105], v[158:161], v[204:207], v[102:105]
	v_mfma_f32_16x16x32_bf16 v[94:97], v[150:153], v[212:215], v[94:97]
	v_mfma_f32_16x16x32_bf16 v[86:89], v[158:161], v[212:215], v[86:89]
	v_mfma_f32_16x16x32_bf16 v[78:81], v[150:153], v[220:223], v[78:81]
	v_mfma_f32_16x16x32_bf16 v[70:73], v[158:161], v[220:223], v[70:73]
	v_mfma_f32_16x16x32_bf16 v[122:125], v[162:165], v[178:181], v[122:125]
	v_mfma_f32_16x16x32_bf16 v[114:117], v[170:173], v[178:181], v[114:117]
	v_mfma_f32_16x16x32_bf16 v[106:109], v[162:165], v[200:203], v[106:109]
	v_mfma_f32_16x16x32_bf16 v[98:101], v[170:173], v[200:203], v[98:101]
	v_mfma_f32_16x16x32_bf16 v[90:93], v[162:165], v[208:211], v[90:93]
	v_mfma_f32_16x16x32_bf16 v[82:85], v[170:173], v[208:211], v[82:85]
	v_mfma_f32_16x16x32_bf16 v[74:77], v[162:165], v[216:219], v[74:77]
	v_mfma_f32_16x16x32_bf16 v[66:69], v[170:173], v[216:219], v[66:69]
	v_mfma_f32_16x16x32_bf16 v[122:125], v[166:169], v[182:185], v[122:125]
	v_mfma_f32_16x16x32_bf16 v[114:117], v[174:177], v[182:185], v[114:117]
	v_mfma_f32_16x16x32_bf16 v[106:109], v[166:169], v[204:207], v[106:109]
	v_mfma_f32_16x16x32_bf16 v[98:101], v[174:177], v[204:207], v[98:101]
	v_mfma_f32_16x16x32_bf16 v[90:93], v[166:169], v[212:215], v[90:93]
	v_mfma_f32_16x16x32_bf16 v[82:85], v[174:177], v[212:215], v[82:85]
	v_mfma_f32_16x16x32_bf16 v[74:77], v[166:169], v[220:223], v[74:77]
	v_mfma_f32_16x16x32_bf16 v[66:69], v[174:177], v[220:223], v[66:69]
	s_setprio 0
	s_barrier
	s_add_i32 s14, s59, s31
	v_lshl_add_u64 v[140:141], s[44:45], 0, v[186:187]
	s_mov_b32 m0, s14
	ds_read_b128 v[178:181], v145 offset:16384
	ds_read_b128 v[182:185], v145 offset:17408
	ds_read_b128 v[200:203], v145 offset:18432
	ds_read_b128 v[204:207], v145 offset:19456
	ds_read_b128 v[208:211], v145 offset:20480
	ds_read_b128 v[212:215], v145 offset:21504
	ds_read_b128 v[216:219], v145 offset:22528
	ds_read_b128 v[220:223], v145 offset:23552
	global_load_lds_dwordx4 v[140:141], off
	s_add_i32 m0, s14, 0x2000
	s_add_u32 s14, s44, 0x80000
	v_lshl_add_u64 v[232:233], s[44:45], 0, v[132:133]
	s_addc_u32 s15, s45, 0
	s_add_i32 s59, s60, s31
	global_load_lds_dwordx4 v[232:233], off
	v_lshl_add_u64 v[234:235], s[14:15], 0, v[186:187]
	s_mov_b32 m0, s59
	v_lshl_add_u64 v[236:237], s[46:47], 0, v[134:135]
	global_load_lds_dwordx4 v[234:235], off
	v_lshl_add_u64 v[234:235], s[14:15], 0, v[132:133]
	s_add_i32 m0, s59, 0x2000
	s_nop 0
	global_load_lds_dwordx4 v[234:235], off
	v_lshl_add_u64 v[234:235], s[46:47], 0, v[130:131]
	s_mov_b32 m0, s41
	s_nop 0
	global_load_lds_dwordx4 v[234:235], off
	s_mov_b32 m0, s43
	s_nop 0
	global_load_lds_dwordx4 v[236:237], off
	s_waitcnt vmcnt(8)
	s_waitcnt lgkmcnt(0)
	s_barrier
; #define PG8_STAGE(bufoff, gbase, voff) do { _Pragma("unroll") for (int _i = 0; _i < 2; ++_i) \
;         __builtin_amdgcn_global_load_lds((const unsigned*)((const char*)(gbase) + (voff)[_i]), (LAS unsigned*)(lds + (bufoff) + ldsw + _i * 8192), 16, 0, 0); } while (0)
; #define PG8_LDA(dst, b, h) do { _Pragma("unroll") for (int m = 0; m < 4; ++m) _Pragma("unroll") for (int k = 0; k < 2; ++k) dst[m][k] = *(const LAS bf16x8*)(lds + PG8_SA(b, h) + aoff + m * 2048 + k * 1024); } while (0)
; #define PG8_LDB(dst, b, h) do { _Pragma("unroll") for (int n = 0; n < 2; ++n) _Pragma("unroll") for (int k = 0; k < 2; ++k) dst[n][k] = *(const LAS bf16x8*)(lds + PG8_SB(b, h) + boff + n * 2048 + k * 1024); } while (0)
; #define PG8_MMA(ai, bj, At, Bt) do { __builtin_amdgcn_s_setprio(1); _Pragma("unroll") for (int m = 0; m < 4; ++m) _Pragma("unroll") for (int n = 0; n < 2; ++n) _Pragma("unroll") for (int k = 0; k < 2; ++k) \
;         acc[ai][bj][m][n] = __builtin_amdgcn_mfma_f32_16x16x32_bf16(Bt[n][k], At[m][k], acc[ai][bj][m][n], 0, 0, 0); __builtin_amdgcn_s_setprio(0); } while (0)
; #define PG8_WAIT_V(n) asm volatile("s_waitcnt vmcnt(" #n ")" ::: "memory")
; #define PG8_WAIT_L(n) asm volatile("s_waitcnt lgkmcnt(" #n ")" ::: "memory")
; #define PG8_BAR __builtin_amdgcn_s_barrier()
; #define PG8_SCHED __builtin_amdgcn_sched_barrier(0)
; template <class Epi, class Sched>
; __device__ __forceinline__ void gemm_phase(LAS unsigned char* lds, const Gemm g, const Sched& S, const Epi& E, const int tid, unsigned* last_sig = nullptr) {
;     ...
;             PG8_WAIT_V(8); PG8_WAIT_L(0); PG8_BAR; PG8_MMA(1, 0, At, B0); PG8_MMA(1, 1, At, B1); PG8_BAR; PG8_SCHED;
;             PG8_LDB(B0, 1, 0); PG8_LDB(B1, 1, 1); PG8_SCHED; PG8_LDA(At, 1, 0); PG8_STAGE(PG8_SA(0, 1), a2 + hstep, voffA);
;             PG8_WAIT_V(8); PG8_WAIT_L(0); PG8_BAR; PG8_MMA(0, 0, At, B0); PG8_MMA(0, 1, At, B1); PG8_BAR; PG8_SCHED;
	s_setprio 1
	s_waitcnt lgkmcnt(0)
	v_mfma_f32_16x16x32_bf16 v[62:65], v[146:149], v[178:181], v[62:65]
	v_mfma_f32_16x16x32_bf16 v[54:57], v[154:157], v[178:181], v[54:57]
	v_mfma_f32_16x16x32_bf16 v[46:49], v[146:149], v[200:203], v[46:49]
	v_mfma_f32_16x16x32_bf16 v[38:41], v[154:157], v[200:203], v[38:41]
	v_mfma_f32_16x16x32_bf16 v[30:33], v[146:149], v[208:211], v[30:33]
	v_mfma_f32_16x16x32_bf16 v[22:25], v[154:157], v[208:211], v[22:25]
	v_mfma_f32_16x16x32_bf16 v[14:17], v[146:149], v[216:219], v[14:17]
	v_mfma_f32_16x16x32_bf16 v[6:9], v[154:157], v[216:219], v[6:9]
	v_mfma_f32_16x16x32_bf16 v[62:65], v[150:153], v[182:185], v[62:65]
	v_mfma_f32_16x16x32_bf16 v[54:57], v[158:161], v[182:185], v[54:57]
	v_mfma_f32_16x16x32_bf16 v[46:49], v[150:153], v[204:207], v[46:49]
	v_mfma_f32_16x16x32_bf16 v[38:41], v[158:161], v[204:207], v[38:41]
	v_mfma_f32_16x16x32_bf16 v[30:33], v[150:153], v[212:215], v[30:33]
	v_mfma_f32_16x16x32_bf16 v[22:25], v[158:161], v[212:215], v[22:25]
	v_mfma_f32_16x16x32_bf16 v[14:17], v[150:153], v[220:223], v[14:17]
	v_mfma_f32_16x16x32_bf16 v[6:9], v[158:161], v[220:223], v[6:9]
	v_mfma_f32_16x16x32_bf16 v[58:61], v[162:165], v[178:181], v[58:61]
	v_mfma_f32_16x16x32_bf16 v[50:53], v[170:173], v[178:181], v[50:53]
	v_mfma_f32_16x16x32_bf16 v[42:45], v[162:165], v[200:203], v[42:45]
	v_mfma_f32_16x16x32_bf16 v[34:37], v[170:173], v[200:203], v[34:37]
	v_mfma_f32_16x16x32_bf16 v[26:29], v[162:165], v[208:211], v[26:29]
	v_mfma_f32_16x16x32_bf16 v[18:21], v[170:173], v[208:211], v[18:21]
	v_mfma_f32_16x16x32_bf16 v[10:13], v[162:165], v[216:219], v[10:13]
	v_mfma_f32_16x16x32_bf16 v[2:5], v[170:173], v[216:219], v[2:5]
	v_mfma_f32_16x16x32_bf16 v[58:61], v[166:169], v[182:185], v[58:61]
	v_mfma_f32_16x16x32_bf16 v[50:53], v[174:177], v[182:185], v[50:53]
	v_mfma_f32_16x16x32_bf16 v[42:45], v[166:169], v[204:207], v[42:45]
	v_mfma_f32_16x16x32_bf16 v[34:37], v[174:177], v[204:207], v[34:37]
	v_mfma_f32_16x16x32_bf16 v[26:29], v[166:169], v[212:215], v[26:29]
	v_mfma_f32_16x16x32_bf16 v[18:21], v[174:177], v[212:215], v[18:21]
	v_mfma_f32_16x16x32_bf16 v[10:13], v[166:169], v[220:223], v[10:13]
	v_mfma_f32_16x16x32_bf16 v[2:5], v[174:177], v[220:223], v[2:5]
	s_setprio 0
	s_barrier
	s_add_i32 s59, 0, 0x18000
	s_add_i32 s60, 0, 0x1c000
	v_add_u32_e32 v158, s59, v143
	v_add_u32_e32 v174, s60, v143
	ds_read_b128 v[146:149], v158
	ds_read_b128 v[150:153], v158 offset:1024
	ds_read_b128 v[154:157], v158 offset:2048
	ds_read_b128 v[158:161], v158 offset:3072
	ds_read_b128 v[162:165], v174
	ds_read_b128 v[166:169], v174 offset:1024
	ds_read_b128 v[170:173], v174 offset:2048
	ds_read_b128 v[174:177], v174 offset:3072
	s_add_u32 s14, s46, 0x80000
	s_addc_u32 s15, s47, 0
	s_mov_b32 m0, s50
	v_lshl_add_u64 v[238:239], s[14:15], 0, v[130:131]
	ds_read_b128 v[178:181], v145 offset:32768
	ds_read_b128 v[182:185], v145 offset:33792
	ds_read_b128 v[200:203], v145 offset:34816
	ds_read_b128 v[204:207], v145 offset:35840
	ds_read_b128 v[208:211], v145 offset:36864
	ds_read_b128 v[212:215], v145 offset:37888
	ds_read_b128 v[216:219], v145 offset:38912
	ds_read_b128 v[220:223], v145 offset:39936
	global_load_lds_dwordx4 v[238:239], off
	v_lshl_add_u64 v[238:239], s[14:15], 0, v[134:135]
	s_mov_b32 m0, s51
	s_nop 0
	global_load_lds_dwordx4 v[238:239], off
	s_waitcnt vmcnt(8)
	s_waitcnt lgkmcnt(0)
	s_barrier
	s_setprio 1
	s_waitcnt lgkmcnt(0)
	v_mfma_f32_16x16x32_bf16 v[126:129], v[146:149], v[178:181], v[126:129]
	v_mfma_f32_16x16x32_bf16 v[118:121], v[154:157], v[178:181], v[118:121]
	v_mfma_f32_16x16x32_bf16 v[110:113], v[146:149], v[200:203], v[110:113]
	v_mfma_f32_16x16x32_bf16 v[102:105], v[154:157], v[200:203], v[102:105]
	v_mfma_f32_16x16x32_bf16 v[94:97], v[146:149], v[208:211], v[94:97]
	v_mfma_f32_16x16x32_bf16 v[86:89], v[154:157], v[208:211], v[86:89]
	v_mfma_f32_16x16x32_bf16 v[78:81], v[146:149], v[216:219], v[78:81]
	v_mfma_f32_16x16x32_bf16 v[70:73], v[154:157], v[216:219], v[70:73]
	v_mfma_f32_16x16x32_bf16 v[126:129], v[150:153], v[182:185], v[126:129]
	v_mfma_f32_16x16x32_bf16 v[118:121], v[158:161], v[182:185], v[118:121]
	v_mfma_f32_16x16x32_bf16 v[110:113], v[150:153], v[204:207], v[110:113]
	v_mfma_f32_16x16x32_bf16 v[102:105], v[158:161], v[204:207], v[102:105]
	v_mfma_f32_16x16x32_bf16 v[94:97], v[150:153], v[212:215], v[94:97]
	v_mfma_f32_16x16x32_bf16 v[86:89], v[158:161], v[212:215], v[86:89]
	v_mfma_f32_16x16x32_bf16 v[78:81], v[150:153], v[220:223], v[78:81]
	v_mfma_f32_16x16x32_bf16 v[70:73], v[158:161], v[220:223], v[70:73]
	v_mfma_f32_16x16x32_bf16 v[122:125], v[162:165], v[178:181], v[122:125]
	v_mfma_f32_16x16x32_bf16 v[114:117], v[170:173], v[178:181], v[114:117]
	v_mfma_f32_16x16x32_bf16 v[106:109], v[162:165], v[200:203], v[106:109]
	v_mfma_f32_16x16x32_bf16 v[98:101], v[170:173], v[200:203], v[98:101]
	v_mfma_f32_16x16x32_bf16 v[90:93], v[162:165], v[208:211], v[90:93]
	v_mfma_f32_16x16x32_bf16 v[82:85], v[170:173], v[208:211], v[82:85]
	v_mfma_f32_16x16x32_bf16 v[74:77], v[162:165], v[216:219], v[74:77]
	v_mfma_f32_16x16x32_bf16 v[66:69], v[170:173], v[216:219], v[66:69]
	v_mfma_f32_16x16x32_bf16 v[122:125], v[166:169], v[182:185], v[122:125]
	v_mfma_f32_16x16x32_bf16 v[114:117], v[174:177], v[182:185], v[114:117]
	v_mfma_f32_16x16x32_bf16 v[106:109], v[166:169], v[204:207], v[106:109]
	v_mfma_f32_16x16x32_bf16 v[98:101], v[174:177], v[204:207], v[98:101]
	v_mfma_f32_16x16x32_bf16 v[90:93], v[166:169], v[212:215], v[90:93]
	v_mfma_f32_16x16x32_bf16 v[82:85], v[174:177], v[212:215], v[82:85]
	v_mfma_f32_16x16x32_bf16 v[74:77], v[166:169], v[220:223], v[74:77]
	v_mfma_f32_16x16x32_bf16 v[66:69], v[174:177], v[220:223], v[66:69]
	s_setprio 0
	s_barrier
; #define PG8_STAGE(bufoff, gbase, voff) do { _Pragma("unroll") for (int _i = 0; _i < 2; ++_i) \
;         __builtin_amdgcn_global_load_lds((const unsigned*)((const char*)(gbase) + (voff)[_i]), (LAS unsigned*)(lds + (bufoff) + ldsw + _i * 8192), 16, 0, 0); } while (0)
; #define PG8_LDA(dst, b, h) do { _Pragma("unroll") for (int m = 0; m < 4; ++m) _Pragma("unroll") for (int k = 0; k < 2; ++k) dst[m][k] = *(const LAS bf16x8*)(lds + PG8_SA(b, h) + aoff + m * 2048 + k * 1024); } while (0)
; #define PG8_MMA(ai, bj, At, Bt) do { __builtin_amdgcn_s_setprio(1); _Pragma("unroll") for (int m = 0; m < 4; ++m) _Pragma("unroll") for (int n = 0; n < 2; ++n) _Pragma("unroll") for (int k = 0; k < 2; ++k) \
;         acc[ai][bj][m][n] = __builtin_amdgcn_mfma_f32_16x16x32_bf16(Bt[n][k], At[m][k], acc[ai][bj][m][n], 0, 0, 0); __builtin_amdgcn_s_setprio(0); } while (0)
; #define PG8_WAIT_V(n) asm volatile("s_waitcnt vmcnt(" #n ")" ::: "memory")
; #define PG8_WAIT_L(n) asm volatile("s_waitcnt lgkmcnt(" #n ")" ::: "memory")
; #define PG8_BAR __builtin_amdgcn_s_barrier()
; #define PG8_SCHED __builtin_amdgcn_sched_barrier(0)
; template <class Epi, class Sched>
; __device__ __forceinline__ void gemm_phase(LAS unsigned char* lds, const Gemm g, const Sched& S, const Epi& E, const int tid, unsigned* last_sig = nullptr) {
;     ...
;             PG8_LDA(At, 1, 1); PG8_STAGE(PG8_SB(1, 0), b3, voffB); PG8_STAGE(PG8_SB(1, 1), b3 + hstep, voffB); PG8_STAGE(PG8_SA(1, 0), a3, voffA);
;             PG8_WAIT_V(8); PG8_WAIT_L(0); PG8_BAR; PG8_MMA(1, 0, At, B0); PG8_MMA(1, 1, At, B1); PG8_BAR; PG8_SCHED;
;         }
;         if (wr == 0) PG8_BAR;
;         E(acc, cur, wr, wc, fr, fq);
;         if (!has_next) break;
	s_add_i32 s14, s59, s31
	v_lshl_add_u64 v[140:141], v[140:141], 0, s[34:35]
	s_mov_b32 m0, s14
	ds_read_b128 v[178:181], v145 offset:49152
	ds_read_b128 v[182:185], v145 offset:50176
	ds_read_b128 v[200:203], v145 offset:51200
	ds_read_b128 v[204:207], v145 offset:52224
	ds_read_b128 v[208:211], v145 offset:53248
	ds_read_b128 v[212:215], v145 offset:54272
	ds_read_b128 v[216:219], v145 offset:55296
	ds_read_b128 v[220:223], v145 offset:56320
	global_load_lds_dwordx4 v[140:141], off
	s_add_i32 m0, s14, 0x2000
	s_add_u32 s14, s44, 0x80080
	v_lshl_add_u64 v[140:141], v[232:233], 0, s[34:35]
	s_addc_u32 s15, s45, 0
	s_add_i32 s44, s60, s31
	global_load_lds_dwordx4 v[140:141], off
	v_lshl_add_u64 v[140:141], s[14:15], 0, v[186:187]
	s_mov_b32 m0, s44
	s_nop 0
	global_load_lds_dwordx4 v[140:141], off
	v_lshl_add_u64 v[140:141], s[14:15], 0, v[132:133]
	s_add_i32 m0, s44, 0x2000
	s_nop 0
	global_load_lds_dwordx4 v[140:141], off
	v_lshl_add_u64 v[140:141], v[234:235], 0, s[34:35]
	s_mov_b32 m0, s52
	s_nop 0
	global_load_lds_dwordx4 v[140:141], off
	v_lshl_add_u64 v[140:141], v[236:237], 0, s[34:35]
	s_mov_b32 m0, s53
	s_nop 0
	global_load_lds_dwordx4 v[140:141], off
	s_waitcnt vmcnt(8)
	s_waitcnt lgkmcnt(0)
	s_barrier
	s_setprio 1
	s_waitcnt lgkmcnt(0)
	v_mfma_f32_16x16x32_bf16 v[62:65], v[146:149], v[178:181], v[62:65]
	v_mfma_f32_16x16x32_bf16 v[54:57], v[154:157], v[178:181], v[54:57]
	v_mfma_f32_16x16x32_bf16 v[46:49], v[146:149], v[200:203], v[46:49]
	v_mfma_f32_16x16x32_bf16 v[38:41], v[154:157], v[200:203], v[38:41]
	v_mfma_f32_16x16x32_bf16 v[30:33], v[146:149], v[208:211], v[30:33]
	v_mfma_f32_16x16x32_bf16 v[22:25], v[154:157], v[208:211], v[22:25]
	v_mfma_f32_16x16x32_bf16 v[14:17], v[146:149], v[216:219], v[14:17]
	v_mfma_f32_16x16x32_bf16 v[6:9], v[154:157], v[216:219], v[6:9]
	v_mfma_f32_16x16x32_bf16 v[62:65], v[150:153], v[182:185], v[62:65]
	v_mfma_f32_16x16x32_bf16 v[54:57], v[158:161], v[182:185], v[54:57]
	v_mfma_f32_16x16x32_bf16 v[46:49], v[150:153], v[204:207], v[46:49]
	v_mfma_f32_16x16x32_bf16 v[38:41], v[158:161], v[204:207], v[38:41]
	v_mfma_f32_16x16x32_bf16 v[30:33], v[150:153], v[212:215], v[30:33]
	v_mfma_f32_16x16x32_bf16 v[22:25], v[158:161], v[212:215], v[22:25]
	v_mfma_f32_16x16x32_bf16 v[14:17], v[150:153], v[220:223], v[14:17]
	v_mfma_f32_16x16x32_bf16 v[6:9], v[158:161], v[220:223], v[6:9]
	v_mfma_f32_16x16x32_bf16 v[58:61], v[162:165], v[178:181], v[58:61]
	v_mfma_f32_16x16x32_bf16 v[50:53], v[170:173], v[178:181], v[50:53]
	v_mfma_f32_16x16x32_bf16 v[42:45], v[162:165], v[200:203], v[42:45]
	v_mfma_f32_16x16x32_bf16 v[34:37], v[170:173], v[200:203], v[34:37]
	v_mfma_f32_16x16x32_bf16 v[26:29], v[162:165], v[208:211], v[26:29]
	v_mfma_f32_16x16x32_bf16 v[18:21], v[170:173], v[208:211], v[18:21]
	v_mfma_f32_16x16x32_bf16 v[10:13], v[162:165], v[216:219], v[10:13]
	v_mfma_f32_16x16x32_bf16 v[2:5], v[170:173], v[216:219], v[2:5]
	v_mfma_f32_16x16x32_bf16 v[58:61], v[166:169], v[182:185], v[58:61]
	v_mfma_f32_16x16x32_bf16 v[50:53], v[174:177], v[182:185], v[50:53]
	v_mfma_f32_16x16x32_bf16 v[42:45], v[166:169], v[204:207], v[42:45]
	v_mfma_f32_16x16x32_bf16 v[34:37], v[174:177], v[204:207], v[34:37]
	v_mfma_f32_16x16x32_bf16 v[26:29], v[166:169], v[212:215], v[26:29]
	v_mfma_f32_16x16x32_bf16 v[18:21], v[174:177], v[212:215], v[18:21]
	v_mfma_f32_16x16x32_bf16 v[10:13], v[166:169], v[220:223], v[10:13]
	v_mfma_f32_16x16x32_bf16 v[2:5], v[174:177], v[220:223], v[2:5]
	s_setprio 0
	s_barrier
	s_add_i32 s58, s58, 2
	s_add_u32 s4, s4, 0x100
	s_addc_u32 s5, s5, 0
	s_add_u32 s56, s56, 0x100
	s_addc_u32 s57, s57, 0
	s_cmp_gt_u32 s58, 29
	s_cbranch_scc0 .LBB0_1104
	s_and_b64 vcc, exec, s[12:13]
	s_cbranch_vccz .LBB0_1107
	s_barrier

; #define PG8_STAGE(bufoff, gbase, voff) do { _Pragma("unroll") for (int _i = 0; _i < 2; ++_i) \
;         __builtin_amdgcn_global_load_lds((const unsigned*)((const char*)(gbase) + (voff)[_i]), (LAS unsigned*)(lds + (bufoff) + ldsw + _i * 8192), 16, 0, 0); } while (0)
; #define PG8_LDA(dst, b, h) do { _Pragma("unroll") for (int m = 0; m < 4; ++m) _Pragma("unroll") for (int k = 0; k < 2; ++k) dst[m][k] = *(const LAS bf16x8*)(lds + PG8_SA(b, h) + aoff + m * 2048 + k * 1024); } while (0)
; #define PG8_LDB(dst, b, h) do { _Pragma("unroll") for (int n = 0; n < 2; ++n) _Pragma("unroll") for (int k = 0; k < 2; ++k) dst[n][k] = *(const LAS bf16x8*)(lds + PG8_SB(b, h) + boff + n * 2048 + k * 1024); } while (0)
; #define PG8_MMA(ai, bj, At, Bt) do { __builtin_amdgcn_s_setprio(1); _Pragma("unroll") for (int m = 0; m < 4; ++m) _Pragma("unroll") for (int n = 0; n < 2; ++n) _Pragma("unroll") for (int k = 0; k < 2; ++k) \
;         acc[ai][bj][m][n] = __builtin_amdgcn_mfma_f32_16x16x32_bf16(Bt[n][k], At[m][k], acc[ai][bj][m][n], 0, 0, 0); __builtin_amdgcn_s_setprio(0); } while (0)
; #define PG8_BAR __builtin_amdgcn_s_barrier()
; template <class Epi, class Sched>
; __device__ __forceinline__ void gemm_phase(LAS unsigned char* lds, const Gemm g, const Sched& S, const Epi& E, const int tid, unsigned* last_sig = nullptr) {
;     ...
;         const char* nA = has_next ? (const char*)g.A + (size_t)nxt.pm * tstep : cA; const char* nB = has_next ? (const char*)g.Bt + (size_t)nxt.be * g.bstride + (size_t)nxt.pn * tstep : cB;
;         for (int t = 0; t < nt; t += 2) {
;             const bool last = (t == nt - 2);
;             const char* a1 = cA + (size_t)(t + 1) * kstep;
;             const char* a2 = last ? nA : cA + (size_t)(t + 2) * kstep; const char* b2 = last ? nB : cB + (size_t)(t + 2) * kstep;
;             const char* a3 = a2 + kstep; const char* b3 = b2 + kstep;
;             PG8_LDB(B0, 0, 0); PG8_LDB(B1, 0, 1); PG8_SCHED; PG8_LDA(At, 0, 0); PG8_STAGE(PG8_SA(1, 1), a1 + hstep, voffA);
;             PG8_WAIT_V(8); PG8_WAIT_L(0); PG8_BAR; PG8_MMA(0, 0, At, B0); PG8_MMA(0, 1, At, B1); PG8_BAR; PG8_SCHED;
;             PG8_LDA(At, 0, 1); PG8_STAGE(PG8_SB(0, 0), b2, voffB); PG8_STAGE(PG8_SB(0, 1), b2 + hstep, voffB); PG8_STAGE(PG8_SA(0, 0), a2, voffA);
;             PG8_WAIT_V(8); PG8_WAIT_L(0); PG8_BAR; PG8_MMA(1, 0, At, B0); PG8_MMA(1, 1, At, B1); PG8_BAR; PG8_SCHED;
.LBB0_1188:
	s_add_u32 s14, s20, 0xfff80080
	s_addc_u32 s15, s21, -1
	s_add_i32 s55, 0, 0x10000
	s_cmp_eq_u32 s54, 28
	s_cselect_b32 s41, s13, s15
	s_cselect_b32 s40, s50, s14
	v_add_u32_e32 v140, s55, v1
	s_cselect_b32 s23, s11, s53
	s_cselect_b32 s22, s51, s52
	s_add_i32 s56, 0, 0x14000
	ds_read_b128 v[146:149], v140
	ds_read_b128 v[150:153], v140 offset:1024
	ds_read_b128 v[154:157], v140 offset:2048
	ds_read_b128 v[158:161], v140 offset:3072
	v_add_u32_e32 v140, s56, v1
	ds_read_b128 v[162:165], v140
	ds_read_b128 v[166:169], v140 offset:1024
	ds_read_b128 v[170:173], v140 offset:2048
	ds_read_b128 v[174:177], v140 offset:3072
	v_lshl_add_u64 v[140:141], s[20:21], 0, v[136:137]
	s_add_i32 m0, s31, 0xc000
	ds_read_b128 v[178:181], v144
	ds_read_b128 v[182:185], v144 offset:1024
	ds_read_b128 v[200:203], v144 offset:2048
	ds_read_b128 v[204:207], v144 offset:3072
	ds_read_b128 v[208:211], v144 offset:4096
	ds_read_b128 v[212:215], v144 offset:5120
	ds_read_b128 v[216:219], v144 offset:6144
	ds_read_b128 v[220:223], v144 offset:7168
	global_load_lds_dwordx4 v[140:141], off
	v_lshl_add_u64 v[140:141], s[20:21], 0, v[138:139]
	s_add_i32 m0, s31, 0xe000
	s_nop 0
	global_load_lds_dwordx4 v[140:141], off
	s_waitcnt vmcnt(8)
	s_waitcnt lgkmcnt(0)
	s_barrier
	s_setprio 1
	s_waitcnt lgkmcnt(0)
	v_mfma_f32_16x16x32_bf16 v[126:129], v[146:149], v[178:181], v[126:129]
	v_mfma_f32_16x16x32_bf16 v[118:121], v[154:157], v[178:181], v[118:121]
	v_mfma_f32_16x16x32_bf16 v[110:113], v[146:149], v[200:203], v[110:113]
	v_mfma_f32_16x16x32_bf16 v[102:105], v[154:157], v[200:203], v[102:105]
	v_mfma_f32_16x16x32_bf16 v[94:97], v[146:149], v[208:211], v[94:97]
	v_mfma_f32_16x16x32_bf16 v[86:89], v[154:157], v[208:211], v[86:89]
	v_mfma_f32_16x16x32_bf16 v[78:81], v[146:149], v[216:219], v[78:81]
	v_mfma_f32_16x16x32_bf16 v[70:73], v[154:157], v[216:219], v[70:73]
	v_mfma_f32_16x16x32_bf16 v[126:129], v[150:153], v[182:185], v[126:129]
	v_mfma_f32_16x16x32_bf16 v[118:121], v[158:161], v[182:185], v[118:121]
	v_mfma_f32_16x16x32_bf16 v[110:113], v[150:153], v[204:207], v[110:113]
	v_mfma_f32_16x16x32_bf16 v[102:105], v[158:161], v[204:207], v[102:105]
	v_mfma_f32_16x16x32_bf16 v[94:97], v[150:153], v[212:215], v[94:97]
	v_mfma_f32_16x16x32_bf16 v[86:89], v[158:161], v[212:215], v[86:89]
	v_mfma_f32_16x16x32_bf16 v[78:81], v[150:153], v[220:223], v[78:81]
	v_mfma_f32_16x16x32_bf16 v[70:73], v[158:161], v[220:223], v[70:73]
	v_mfma_f32_16x16x32_bf16 v[122:125], v[162:165], v[178:181], v[122:125]
	v_mfma_f32_16x16x32_bf16 v[114:117], v[170:173], v[178:181], v[114:117]
	v_mfma_f32_16x16x32_bf16 v[106:109], v[162:165], v[200:203], v[106:109]
	v_mfma_f32_16x16x32_bf16 v[98:101], v[170:173], v[200:203], v[98:101]
	v_mfma_f32_16x16x32_bf16 v[90:93], v[162:165], v[208:211], v[90:93]
	v_mfma_f32_16x16x32_bf16 v[82:85], v[170:173], v[208:211], v[82:85]
	v_mfma_f32_16x16x32_bf16 v[74:77], v[162:165], v[216:219], v[74:77]
	v_mfma_f32_16x16x32_bf16 v[66:69], v[170:173], v[216:219], v[66:69]
	v_mfma_f32_16x16x32_bf16 v[122:125], v[166:169], v[182:185], v[122:125]
	v_mfma_f32_16x16x32_bf16 v[114:117], v[174:177], v[182:185], v[114:117]
	v_mfma_f32_16x16x32_bf16 v[106:109], v[166:169], v[204:207], v[106:109]
	v_mfma_f32_16x16x32_bf16 v[98:101], v[174:177], v[204:207], v[98:101]
	v_mfma_f32_16x16x32_bf16 v[90:93], v[166:169], v[212:215], v[90:93]
	v_mfma_f32_16x16x32_bf16 v[82:85], v[174:177], v[212:215], v[82:85]
	v_mfma_f32_16x16x32_bf16 v[74:77], v[166:169], v[220:223], v[74:77]
	v_mfma_f32_16x16x32_bf16 v[66:69], v[174:177], v[220:223], v[66:69]
	s_setprio 0
	s_barrier
	s_add_i32 s14, s55, s28
	v_lshl_add_u64 v[140:141], s[22:23], 0, v[186:187]
	s_mov_b32 m0, s14
	ds_read_b128 v[178:181], v144 offset:16384
	ds_read_b128 v[182:185], v144 offset:17408
	ds_read_b128 v[200:203], v144 offset:18432
	ds_read_b128 v[204:207], v144 offset:19456
	ds_read_b128 v[208:211], v144 offset:20480
	ds_read_b128 v[212:215], v144 offset:21504
	ds_read_b128 v[216:219], v144 offset:22528
	ds_read_b128 v[220:223], v144 offset:23552
	global_load_lds_dwordx4 v[140:141], off
	s_add_i32 m0, s14, 0x2000
	s_add_u32 s14, s22, 0x80000
	v_lshl_add_u64 v[232:233], s[22:23], 0, v[130:131]
	s_addc_u32 s15, s23, 0
	s_add_i32 s55, s56, s28
	global_load_lds_dwordx4 v[232:233], off
	v_lshl_add_u64 v[234:235], s[14:15], 0, v[186:187]
	s_mov_b32 m0, s55
	v_lshl_add_u64 v[236:237], s[40:41], 0, v[132:133]
	global_load_lds_dwordx4 v[234:235], off
	v_lshl_add_u64 v[234:235], s[14:15], 0, v[130:131]
	s_add_i32 m0, s55, 0x2000
	s_nop 0
	global_load_lds_dwordx4 v[234:235], off
	v_lshl_add_u64 v[234:235], s[40:41], 0, v[134:135]
	s_mov_b32 m0, s31
	s_nop 0
	global_load_lds_dwordx4 v[234:235], off
	s_mov_b32 m0, s42
	s_nop 0
	global_load_lds_dwordx4 v[236:237], off
	s_waitcnt vmcnt(8)
	s_waitcnt lgkmcnt(0)
	s_barrier
; #define PG8_STAGE(bufoff, gbase, voff) do { _Pragma("unroll") for (int _i = 0; _i < 2; ++_i) \
;         __builtin_amdgcn_global_load_lds((const unsigned*)((const char*)(gbase) + (voff)[_i]), (LAS unsigned*)(lds + (bufoff) + ldsw + _i * 8192), 16, 0, 0); } while (0)
; #define PG8_LDA(dst, b, h) do { _Pragma("unroll") for (int m = 0; m < 4; ++m) _Pragma("unroll") for (int k = 0; k < 2; ++k) dst[m][k] = *(const LAS bf16x8*)(lds + PG8_SA(b, h) + aoff + m * 2048 + k * 1024); } while (0)
; #define PG8_LDB(dst, b, h) do { _Pragma("unroll") for (int n = 0; n < 2; ++n) _Pragma("unroll") for (int k = 0; k < 2; ++k) dst[n][k] = *(const LAS bf16x8*)(lds + PG8_SB(b, h) + boff + n * 2048 + k * 1024); } while (0)
; #define PG8_MMA(ai, bj, At, Bt) do { __builtin_amdgcn_s_setprio(1); _Pragma("unroll") for (int m = 0; m < 4; ++m) _Pragma("unroll") for (int n = 0; n < 2; ++n) _Pragma("unroll") for (int k = 0; k < 2; ++k) \
;         acc[ai][bj][m][n] = __builtin_amdgcn_mfma_f32_16x16x32_bf16(Bt[n][k], At[m][k], acc[ai][bj][m][n], 0, 0, 0); __builtin_amdgcn_s_setprio(0); } while (0)
; #define PG8_WAIT_V(n) asm volatile("s_waitcnt vmcnt(" #n ")" ::: "memory")
; #define PG8_WAIT_L(n) asm volatile("s_waitcnt lgkmcnt(" #n ")" ::: "memory")
; #define PG8_BAR __builtin_amdgcn_s_barrier()
; #define PG8_SCHED __builtin_amdgcn_sched_barrier(0)
; template <class Epi, class Sched>
; __device__ __forceinline__ void gemm_phase(LAS unsigned char* lds, const Gemm g, const Sched& S, const Epi& E, const int tid, unsigned* last_sig = nullptr) {
;     ...
;             PG8_WAIT_V(8); PG8_WAIT_L(0); PG8_BAR; PG8_MMA(1, 0, At, B0); PG8_MMA(1, 1, At, B1); PG8_BAR; PG8_SCHED;
;             PG8_LDB(B0, 1, 0); PG8_LDB(B1, 1, 1); PG8_SCHED; PG8_LDA(At, 1, 0); PG8_STAGE(PG8_SA(0, 1), a2 + hstep, voffA);
;             PG8_WAIT_V(8); PG8_WAIT_L(0); PG8_BAR; PG8_MMA(0, 0, At, B0); PG8_MMA(0, 1, At, B1); PG8_BAR; PG8_SCHED;
	s_setprio 1
	s_waitcnt lgkmcnt(0)
	v_mfma_f32_16x16x32_bf16 v[62:65], v[146:149], v[178:181], v[62:65]
	v_mfma_f32_16x16x32_bf16 v[54:57], v[154:157], v[178:181], v[54:57]
	v_mfma_f32_16x16x32_bf16 v[46:49], v[146:149], v[200:203], v[46:49]
	v_mfma_f32_16x16x32_bf16 v[38:41], v[154:157], v[200:203], v[38:41]
	v_mfma_f32_16x16x32_bf16 v[30:33], v[146:149], v[208:211], v[30:33]
	v_mfma_f32_16x16x32_bf16 v[22:25], v[154:157], v[208:211], v[22:25]
	v_mfma_f32_16x16x32_bf16 v[14:17], v[146:149], v[216:219], v[14:17]
	v_mfma_f32_16x16x32_bf16 v[6:9], v[154:157], v[216:219], v[6:9]
	v_mfma_f32_16x16x32_bf16 v[62:65], v[150:153], v[182:185], v[62:65]
	v_mfma_f32_16x16x32_bf16 v[54:57], v[158:161], v[182:185], v[54:57]
	v_mfma_f32_16x16x32_bf16 v[46:49], v[150:153], v[204:207], v[46:49]
	v_mfma_f32_16x16x32_bf16 v[38:41], v[158:161], v[204:207], v[38:41]
	v_mfma_f32_16x16x32_bf16 v[30:33], v[150:153], v[212:215], v[30:33]
	v_mfma_f32_16x16x32_bf16 v[22:25], v[158:161], v[212:215], v[22:25]
	v_mfma_f32_16x16x32_bf16 v[14:17], v[150:153], v[220:223], v[14:17]
	v_mfma_f32_16x16x32_bf16 v[6:9], v[158:161], v[220:223], v[6:9]
	v_mfma_f32_16x16x32_bf16 v[58:61], v[162:165], v[178:181], v[58:61]
	v_mfma_f32_16x16x32_bf16 v[50:53], v[170:173], v[178:181], v[50:53]
	v_mfma_f32_16x16x32_bf16 v[42:45], v[162:165], v[200:203], v[42:45]
	v_mfma_f32_16x16x32_bf16 v[34:37], v[170:173], v[200:203], v[34:37]
	v_mfma_f32_16x16x32_bf16 v[26:29], v[162:165], v[208:211], v[26:29]
	v_mfma_f32_16x16x32_bf16 v[18:21], v[170:173], v[208:211], v[18:21]
	v_mfma_f32_16x16x32_bf16 v[10:13], v[162:165], v[216:219], v[10:13]
	v_mfma_f32_16x16x32_bf16 v[2:5], v[170:173], v[216:219], v[2:5]
	v_mfma_f32_16x16x32_bf16 v[58:61], v[166:169], v[182:185], v[58:61]
	v_mfma_f32_16x16x32_bf16 v[50:53], v[174:177], v[182:185], v[50:53]
	v_mfma_f32_16x16x32_bf16 v[42:45], v[166:169], v[204:207], v[42:45]
	v_mfma_f32_16x16x32_bf16 v[34:37], v[174:177], v[204:207], v[34:37]
	v_mfma_f32_16x16x32_bf16 v[26:29], v[166:169], v[212:215], v[26:29]
	v_mfma_f32_16x16x32_bf16 v[18:21], v[174:177], v[212:215], v[18:21]
	v_mfma_f32_16x16x32_bf16 v[10:13], v[166:169], v[220:223], v[10:13]
	v_mfma_f32_16x16x32_bf16 v[2:5], v[174:177], v[220:223], v[2:5]
	s_setprio 0
	s_barrier
	s_add_i32 s55, 0, 0x18000
	v_add_u32_e32 v145, s55, v1
	s_add_i32 s56, 0, 0x1c000
	ds_read_b128 v[146:149], v145
	ds_read_b128 v[150:153], v145 offset:1024
	ds_read_b128 v[154:157], v145 offset:2048
	ds_read_b128 v[158:161], v145 offset:3072
	v_add_u32_e32 v145, s56, v1
	ds_read_b128 v[162:165], v145
	ds_read_b128 v[166:169], v145 offset:1024
	ds_read_b128 v[170:173], v145 offset:2048
	ds_read_b128 v[174:177], v145 offset:3072
	s_add_u32 s14, s40, 0x80000
	s_addc_u32 s15, s41, 0
	s_mov_b32 m0, s43
	v_lshl_add_u64 v[238:239], s[14:15], 0, v[134:135]
	ds_read_b128 v[178:181], v144 offset:32768
	ds_read_b128 v[182:185], v144 offset:33792
	ds_read_b128 v[200:203], v144 offset:34816
	ds_read_b128 v[204:207], v144 offset:35840
	ds_read_b128 v[208:211], v144 offset:36864
	ds_read_b128 v[212:215], v144 offset:37888
	ds_read_b128 v[216:219], v144 offset:38912
	ds_read_b128 v[220:223], v144 offset:39936
	global_load_lds_dwordx4 v[238:239], off
	v_lshl_add_u64 v[238:239], s[14:15], 0, v[132:133]
	s_mov_b32 m0, s44
	s_nop 0
	global_load_lds_dwordx4 v[238:239], off
	s_waitcnt vmcnt(8)
	s_waitcnt lgkmcnt(0)
	s_barrier
	s_setprio 1
	s_waitcnt lgkmcnt(0)
	v_mfma_f32_16x16x32_bf16 v[126:129], v[146:149], v[178:181], v[126:129]
	v_mfma_f32_16x16x32_bf16 v[118:121], v[154:157], v[178:181], v[118:121]
	v_mfma_f32_16x16x32_bf16 v[110:113], v[146:149], v[200:203], v[110:113]
	v_mfma_f32_16x16x32_bf16 v[102:105], v[154:157], v[200:203], v[102:105]
	v_mfma_f32_16x16x32_bf16 v[94:97], v[146:149], v[208:211], v[94:97]
	v_mfma_f32_16x16x32_bf16 v[86:89], v[154:157], v[208:211], v[86:89]
	v_mfma_f32_16x16x32_bf16 v[78:81], v[146:149], v[216:219], v[78:81]
	v_mfma_f32_16x16x32_bf16 v[70:73], v[154:157], v[216:219], v[70:73]
	v_mfma_f32_16x16x32_bf16 v[126:129], v[150:153], v[182:185], v[126:129]
	v_mfma_f32_16x16x32_bf16 v[118:121], v[158:161], v[182:185], v[118:121]
	v_mfma_f32_16x16x32_bf16 v[110:113], v[150:153], v[204:207], v[110:113]
	v_mfma_f32_16x16x32_bf16 v[102:105], v[158:161], v[204:207], v[102:105]
	v_mfma_f32_16x16x32_bf16 v[94:97], v[150:153], v[212:215], v[94:97]
	v_mfma_f32_16x16x32_bf16 v[86:89], v[158:161], v[212:215], v[86:89]
	v_mfma_f32_16x16x32_bf16 v[78:81], v[150:153], v[220:223], v[78:81]
	v_mfma_f32_16x16x32_bf16 v[70:73], v[158:161], v[220:223], v[70:73]
	v_mfma_f32_16x16x32_bf16 v[122:125], v[162:165], v[178:181], v[122:125]
	v_mfma_f32_16x16x32_bf16 v[114:117], v[170:173], v[178:181], v[114:117]
	v_mfma_f32_16x16x32_bf16 v[106:109], v[162:165], v[200:203], v[106:109]
	v_mfma_f32_16x16x32_bf16 v[98:101], v[170:173], v[200:203], v[98:101]
	v_mfma_f32_16x16x32_bf16 v[90:93], v[162:165], v[208:211], v[90:93]
	v_mfma_f32_16x16x32_bf16 v[82:85], v[170:173], v[208:211], v[82:85]
	v_mfma_f32_16x16x32_bf16 v[74:77], v[162:165], v[216:219], v[74:77]
	v_mfma_f32_16x16x32_bf16 v[66:69], v[170:173], v[216:219], v[66:69]
	v_mfma_f32_16x16x32_bf16 v[122:125], v[166:169], v[182:185], v[122:125]
	v_mfma_f32_16x16x32_bf16 v[114:117], v[174:177], v[182:185], v[114:117]
	v_mfma_f32_16x16x32_bf16 v[106:109], v[166:169], v[204:207], v[106:109]
	v_mfma_f32_16x16x32_bf16 v[98:101], v[174:177], v[204:207], v[98:101]
	v_mfma_f32_16x16x32_bf16 v[90:93], v[166:169], v[212:215], v[90:93]
	v_mfma_f32_16x16x32_bf16 v[82:85], v[174:177], v[212:215], v[82:85]
	v_mfma_f32_16x16x32_bf16 v[74:77], v[166:169], v[220:223], v[74:77]
	v_mfma_f32_16x16x32_bf16 v[66:69], v[174:177], v[220:223], v[66:69]
	s_setprio 0
	s_barrier
; #define PG8_STAGE(bufoff, gbase, voff) do { _Pragma("unroll") for (int _i = 0; _i < 2; ++_i) \
;         __builtin_amdgcn_global_load_lds((const unsigned*)((const char*)(gbase) + (voff)[_i]), (LAS unsigned*)(lds + (bufoff) + ldsw + _i * 8192), 16, 0, 0); } while (0)
; #define PG8_LDA(dst, b, h) do { _Pragma("unroll") for (int m = 0; m < 4; ++m) _Pragma("unroll") for (int k = 0; k < 2; ++k) dst[m][k] = *(const LAS bf16x8*)(lds + PG8_SA(b, h) + aoff + m * 2048 + k * 1024); } while (0)
; #define PG8_MMA(ai, bj, At, Bt) do { __builtin_amdgcn_s_setprio(1); _Pragma("unroll") for (int m = 0; m < 4; ++m) _Pragma("unroll") for (int n = 0; n < 2; ++n) _Pragma("unroll") for (int k = 0; k < 2; ++k) \
;         acc[ai][bj][m][n] = __builtin_amdgcn_mfma_f32_16x16x32_bf16(Bt[n][k], At[m][k], acc[ai][bj][m][n], 0, 0, 0); __builtin_amdgcn_s_setprio(0); } while (0)
; #define PG8_WAIT_V(n) asm volatile("s_waitcnt vmcnt(" #n ")" ::: "memory")
; #define PG8_WAIT_L(n) asm volatile("s_waitcnt lgkmcnt(" #n ")" ::: "memory")
; #define PG8_BAR __builtin_amdgcn_s_barrier()
; #define PG8_SCHED __builtin_amdgcn_sched_barrier(0)
; template <class Epi, class Sched>
; __device__ __forceinline__ void gemm_phase(LAS unsigned char* lds, const Gemm g, const Sched& S, const Epi& E, const int tid, unsigned* last_sig = nullptr) {
;     ...
;             PG8_LDA(At, 1, 1); PG8_STAGE(PG8_SB(1, 0), b3, voffB); PG8_STAGE(PG8_SB(1, 1), b3 + hstep, voffB); PG8_STAGE(PG8_SA(1, 0), a3, voffA);
;             PG8_WAIT_V(8); PG8_WAIT_L(0); PG8_BAR; PG8_MMA(1, 0, At, B0); PG8_MMA(1, 1, At, B1); PG8_BAR; PG8_SCHED;
;         }
;         if (wr == 0) PG8_BAR;
;         E(acc, cur, wr, wc, fr, fq);
;         if (!has_next) break;
	s_add_i32 s14, s55, s28
	v_lshl_add_u64 v[140:141], v[140:141], 0, s[34:35]
	s_mov_b32 m0, s14
	ds_read_b128 v[178:181], v144 offset:49152
	ds_read_b128 v[182:185], v144 offset:50176
	ds_read_b128 v[200:203], v144 offset:51200
	ds_read_b128 v[204:207], v144 offset:52224
	ds_read_b128 v[208:211], v144 offset:53248
	ds_read_b128 v[212:215], v144 offset:54272
	ds_read_b128 v[216:219], v144 offset:55296
	ds_read_b128 v[220:223], v144 offset:56320
	global_load_lds_dwordx4 v[140:141], off
	s_add_i32 m0, s14, 0x2000
	s_add_u32 s14, s22, 0x80080
	v_lshl_add_u64 v[140:141], v[232:233], 0, s[34:35]
	s_addc_u32 s15, s23, 0
	s_add_i32 s22, s56, s28
	global_load_lds_dwordx4 v[140:141], off
	v_lshl_add_u64 v[140:141], s[14:15], 0, v[186:187]
	s_mov_b32 m0, s22
	s_nop 0
	global_load_lds_dwordx4 v[140:141], off
	v_lshl_add_u64 v[140:141], s[14:15], 0, v[130:131]
	s_add_i32 m0, s22, 0x2000
	s_nop 0
	global_load_lds_dwordx4 v[140:141], off
	v_lshl_add_u64 v[140:141], v[234:235], 0, s[34:35]
	s_mov_b32 m0, s45
	s_nop 0
	global_load_lds_dwordx4 v[140:141], off
	v_lshl_add_u64 v[140:141], v[236:237], 0, s[34:35]
	s_mov_b32 m0, s46
	s_nop 0
	global_load_lds_dwordx4 v[140:141], off
	s_waitcnt vmcnt(8)
	s_waitcnt lgkmcnt(0)
	s_barrier
	s_setprio 1
	s_waitcnt lgkmcnt(0)
	v_mfma_f32_16x16x32_bf16 v[62:65], v[146:149], v[178:181], v[62:65]
	v_mfma_f32_16x16x32_bf16 v[54:57], v[154:157], v[178:181], v[54:57]
	v_mfma_f32_16x16x32_bf16 v[46:49], v[146:149], v[200:203], v[46:49]
	v_mfma_f32_16x16x32_bf16 v[38:41], v[154:157], v[200:203], v[38:41]
	v_mfma_f32_16x16x32_bf16 v[30:33], v[146:149], v[208:211], v[30:33]
	v_mfma_f32_16x16x32_bf16 v[22:25], v[154:157], v[208:211], v[22:25]
	v_mfma_f32_16x16x32_bf16 v[14:17], v[146:149], v[216:219], v[14:17]
	v_mfma_f32_16x16x32_bf16 v[6:9], v[154:157], v[216:219], v[6:9]
	v_mfma_f32_16x16x32_bf16 v[62:65], v[150:153], v[182:185], v[62:65]
	v_mfma_f32_16x16x32_bf16 v[54:57], v[158:161], v[182:185], v[54:57]
	v_mfma_f32_16x16x32_bf16 v[46:49], v[150:153], v[204:207], v[46:49]
	v_mfma_f32_16x16x32_bf16 v[38:41], v[158:161], v[204:207], v[38:41]
	v_mfma_f32_16x16x32_bf16 v[30:33], v[150:153], v[212:215], v[30:33]
	v_mfma_f32_16x16x32_bf16 v[22:25], v[158:161], v[212:215], v[22:25]
	v_mfma_f32_16x16x32_bf16 v[14:17], v[150:153], v[220:223], v[14:17]
	v_mfma_f32_16x16x32_bf16 v[6:9], v[158:161], v[220:223], v[6:9]
	v_mfma_f32_16x16x32_bf16 v[58:61], v[162:165], v[178:181], v[58:61]
	v_mfma_f32_16x16x32_bf16 v[50:53], v[170:173], v[178:181], v[50:53]
	v_mfma_f32_16x16x32_bf16 v[42:45], v[162:165], v[200:203], v[42:45]
	v_mfma_f32_16x16x32_bf16 v[34:37], v[170:173], v[200:203], v[34:37]
	v_mfma_f32_16x16x32_bf16 v[26:29], v[162:165], v[208:211], v[26:29]
	v_mfma_f32_16x16x32_bf16 v[18:21], v[170:173], v[208:211], v[18:21]
	v_mfma_f32_16x16x32_bf16 v[10:13], v[162:165], v[216:219], v[10:13]
	v_mfma_f32_16x16x32_bf16 v[2:5], v[170:173], v[216:219], v[2:5]
	v_mfma_f32_16x16x32_bf16 v[58:61], v[166:169], v[182:185], v[58:61]
	v_mfma_f32_16x16x32_bf16 v[50:53], v[174:177], v[182:185], v[50:53]
	v_mfma_f32_16x16x32_bf16 v[42:45], v[166:169], v[204:207], v[42:45]
	v_mfma_f32_16x16x32_bf16 v[34:37], v[174:177], v[204:207], v[34:37]
	v_mfma_f32_16x16x32_bf16 v[26:29], v[166:169], v[212:215], v[26:29]
	v_mfma_f32_16x16x32_bf16 v[18:21], v[174:177], v[212:215], v[18:21]
	v_mfma_f32_16x16x32_bf16 v[10:13], v[166:169], v[220:223], v[10:13]
	v_mfma_f32_16x16x32_bf16 v[2:5], v[174:177], v[220:223], v[2:5]
	s_setprio 0
	s_barrier
	s_add_i32 s54, s54, 2
	s_add_u32 s20, s20, 0x100
	s_addc_u32 s21, s21, 0
	s_add_u32 s52, s52, 0x100
	s_addc_u32 s53, s53, 0
	s_cmp_gt_u32 s54, 29
	s_cbranch_scc0 .LBB0_1188
	s_and_b64 vcc, exec, s[8:9]
	s_cbranch_vccz .LBB0_1191
	s_barrier

; #define PG8_STAGE(bufoff, gbase, voff) do { _Pragma("unroll") for (int _i = 0; _i < 2; ++_i) \
;         __builtin_amdgcn_global_load_lds((const unsigned*)((const char*)(gbase) + (voff)[_i]), (LAS unsigned*)(lds + (bufoff) + ldsw + _i * 8192), 16, 0, 0); } while (0)
; #define PG8_LDA(dst, b, h) do { _Pragma("unroll") for (int m = 0; m < 4; ++m) _Pragma("unroll") for (int k = 0; k < 2; ++k) dst[m][k] = *(const LAS bf16x8*)(lds + PG8_SA(b, h) + aoff + m * 2048 + k * 1024); } while (0)
; #define PG8_LDB(dst, b, h) do { _Pragma("unroll") for (int n = 0; n < 2; ++n) _Pragma("unroll") for (int k = 0; k < 2; ++k) dst[n][k] = *(const LAS bf16x8*)(lds + PG8_SB(b, h) + boff + n * 2048 + k * 1024); } while (0)
; #define PG8_MMA(ai, bj, At, Bt) do { __builtin_amdgcn_s_setprio(1); _Pragma("unroll") for (int m = 0; m < 4; ++m) _Pragma("unroll") for (int n = 0; n < 2; ++n) _Pragma("unroll") for (int k = 0; k < 2; ++k) \
;         acc[ai][bj][m][n] = __builtin_amdgcn_mfma_f32_16x16x32_bf16(Bt[n][k], At[m][k], acc[ai][bj][m][n], 0, 0, 0); __builtin_amdgcn_s_setprio(0); } while (0)
; #define PG8_BAR __builtin_amdgcn_s_barrier()
; template <class Epi, class Sched>
; __device__ __forceinline__ void gemm_phase(LAS unsigned char* lds, const Gemm g, const Sched& S, const Epi& E, const int tid, unsigned* last_sig = nullptr) {
;     ...
;         const char* nA = has_next ? (const char*)g.A + (size_t)nxt.pm * tstep : cA; const char* nB = has_next ? (const char*)g.Bt + (size_t)nxt.be * g.bstride + (size_t)nxt.pn * tstep : cB;
;         for (int t = 0; t < nt; t += 2) {
;             const bool last = (t == nt - 2);
;             const char* a1 = cA + (size_t)(t + 1) * kstep;
;             const char* a2 = last ? nA : cA + (size_t)(t + 2) * kstep; const char* b2 = last ? nB : cB + (size_t)(t + 2) * kstep;
;             const char* a3 = a2 + kstep; const char* b3 = b2 + kstep;
;             PG8_LDB(B0, 0, 0); PG8_LDB(B1, 0, 1); PG8_SCHED; PG8_LDA(At, 0, 0); PG8_STAGE(PG8_SA(1, 1), a1 + hstep, voffA);
;             PG8_WAIT_V(8); PG8_WAIT_L(0); PG8_BAR; PG8_MMA(0, 0, At, B0); PG8_MMA(0, 1, At, B1); PG8_BAR; PG8_SCHED;
;             PG8_LDA(At, 0, 1); PG8_STAGE(PG8_SB(0, 0), b2, voffB); PG8_STAGE(PG8_SB(0, 1), b2 + hstep, voffB); PG8_STAGE(PG8_SA(0, 0), a2, voffA);
;             PG8_WAIT_V(8); PG8_WAIT_L(0); PG8_BAR; PG8_MMA(1, 0, At, B0); PG8_MMA(1, 1, At, B1); PG8_BAR; PG8_SCHED;
.LBB0_1262:
	s_add_u32 s18, s16, 0x100
	s_addc_u32 s19, s17, 0
	s_add_i32 s14, 0, 0x10000
	s_cmp_eq_u32 s56, 52
	s_cselect_b32 s23, s5, s19
	s_cselect_b32 s22, s4, s18
	s_cselect_b32 s21, s13, s55
	s_cselect_b32 s20, s12, s54
	s_add_i32 s57, 0, 0x14000
	v_add_u32_e32 v156, s14, v141
	v_add_u32_e32 v172, s57, v141
	ds_read_b128 v[144:147], v156
	ds_read_b128 v[148:151], v156 offset:1024
	ds_read_b128 v[152:155], v156 offset:2048
	ds_read_b128 v[156:159], v156 offset:3072
	ds_read_b128 v[160:163], v172
	ds_read_b128 v[164:167], v172 offset:1024
	ds_read_b128 v[168:171], v172 offset:2048
	ds_read_b128 v[172:175], v172 offset:3072
	v_lshl_add_u64 v[184:185], s[16:17], 0, v[136:137]
	s_add_i32 m0, s42, 0xc000
	ds_read_b128 v[176:179], v143
	ds_read_b128 v[180:183], v143 offset:1024
	ds_read_b128 v[200:203], v143 offset:2048
	ds_read_b128 v[204:207], v143 offset:3072
	ds_read_b128 v[208:211], v143 offset:4096
	ds_read_b128 v[212:215], v143 offset:5120
	ds_read_b128 v[216:219], v143 offset:6144
	ds_read_b128 v[220:223], v143 offset:7168
	global_load_lds_dwordx4 v[184:185], off
	v_lshl_add_u64 v[184:185], s[16:17], 0, v[138:139]
	s_add_i32 m0, s42, 0xe000
	s_nop 0
	global_load_lds_dwordx4 v[184:185], off
	s_waitcnt vmcnt(8)
	s_waitcnt lgkmcnt(0)
	s_barrier
	s_setprio 1
	s_waitcnt lgkmcnt(0)
	v_mfma_f32_16x16x32_bf16 v[126:129], v[144:147], v[176:179], v[126:129]
	v_mfma_f32_16x16x32_bf16 v[122:125], v[152:155], v[176:179], v[122:125]
	v_mfma_f32_16x16x32_bf16 v[118:121], v[144:147], v[200:203], v[118:121]
	v_mfma_f32_16x16x32_bf16 v[114:117], v[152:155], v[200:203], v[114:117]
	v_mfma_f32_16x16x32_bf16 v[102:105], v[144:147], v[208:211], v[102:105]
	v_mfma_f32_16x16x32_bf16 v[98:101], v[152:155], v[208:211], v[98:101]
	v_mfma_f32_16x16x32_bf16 v[86:89], v[144:147], v[216:219], v[86:89]
	v_mfma_f32_16x16x32_bf16 v[82:85], v[152:155], v[216:219], v[82:85]
	v_mfma_f32_16x16x32_bf16 v[126:129], v[148:151], v[180:183], v[126:129]
	v_mfma_f32_16x16x32_bf16 v[122:125], v[156:159], v[180:183], v[122:125]
	v_mfma_f32_16x16x32_bf16 v[118:121], v[148:151], v[204:207], v[118:121]
	v_mfma_f32_16x16x32_bf16 v[114:117], v[156:159], v[204:207], v[114:117]
	v_mfma_f32_16x16x32_bf16 v[102:105], v[148:151], v[212:215], v[102:105]
	v_mfma_f32_16x16x32_bf16 v[98:101], v[156:159], v[212:215], v[98:101]
	v_mfma_f32_16x16x32_bf16 v[86:89], v[148:151], v[220:223], v[86:89]
	v_mfma_f32_16x16x32_bf16 v[82:85], v[156:159], v[220:223], v[82:85]
	v_mfma_f32_16x16x32_bf16 v[110:113], v[160:163], v[176:179], v[110:113]
	v_mfma_f32_16x16x32_bf16 v[106:109], v[168:171], v[176:179], v[106:109]
	v_mfma_f32_16x16x32_bf16 v[94:97], v[160:163], v[200:203], v[94:97]
	v_mfma_f32_16x16x32_bf16 v[90:93], v[168:171], v[200:203], v[90:93]
	v_mfma_f32_16x16x32_bf16 v[78:81], v[160:163], v[208:211], v[78:81]
	v_mfma_f32_16x16x32_bf16 v[74:77], v[168:171], v[208:211], v[74:77]
	v_mfma_f32_16x16x32_bf16 v[70:73], v[160:163], v[216:219], v[70:73]
	v_mfma_f32_16x16x32_bf16 v[66:69], v[168:171], v[216:219], v[66:69]
	v_mfma_f32_16x16x32_bf16 v[110:113], v[164:167], v[180:183], v[110:113]
	v_mfma_f32_16x16x32_bf16 v[106:109], v[172:175], v[180:183], v[106:109]
	v_mfma_f32_16x16x32_bf16 v[94:97], v[164:167], v[204:207], v[94:97]
	v_mfma_f32_16x16x32_bf16 v[90:93], v[172:175], v[204:207], v[90:93]
	v_mfma_f32_16x16x32_bf16 v[78:81], v[164:167], v[212:215], v[78:81]
	v_mfma_f32_16x16x32_bf16 v[74:77], v[172:175], v[212:215], v[74:77]
	v_mfma_f32_16x16x32_bf16 v[70:73], v[164:167], v[220:223], v[70:73]
	v_mfma_f32_16x16x32_bf16 v[66:69], v[172:175], v[220:223], v[66:69]
	s_setprio 0
	s_barrier
	s_add_i32 s14, s14, s40
	v_lshl_add_u64 v[184:185], s[20:21], 0, v[186:187]
	s_mov_b32 m0, s14
	ds_read_b128 v[176:179], v143 offset:16384
	ds_read_b128 v[180:183], v143 offset:17408
	ds_read_b128 v[200:203], v143 offset:18432
	ds_read_b128 v[204:207], v143 offset:19456
	ds_read_b128 v[208:211], v143 offset:20480
	ds_read_b128 v[212:215], v143 offset:21504
	ds_read_b128 v[216:219], v143 offset:22528
	ds_read_b128 v[220:223], v143 offset:23552
	global_load_lds_dwordx4 v[184:185], off
	s_add_i32 m0, s14, 0x2000
	s_add_u32 s14, s20, 0xe0000
	v_lshl_add_u64 v[232:233], s[20:21], 0, v[134:135]
	s_addc_u32 s15, s21, 0
	s_add_i32 s16, s57, s40
	global_load_lds_dwordx4 v[232:233], off
	v_lshl_add_u64 v[234:235], s[14:15], 0, v[186:187]
	s_mov_b32 m0, s16
	v_lshl_add_u64 v[236:237], s[22:23], 0, v[132:133]
	global_load_lds_dwordx4 v[234:235], off
	v_lshl_add_u64 v[234:235], s[14:15], 0, v[134:135]
	s_add_i32 m0, s16, 0x2000
	s_nop 0
	global_load_lds_dwordx4 v[234:235], off
	v_lshl_add_u64 v[234:235], s[22:23], 0, v[130:131]
	s_mov_b32 m0, s42
	s_nop 0
	global_load_lds_dwordx4 v[234:235], off
	s_mov_b32 m0, s43
	s_nop 0
	global_load_lds_dwordx4 v[236:237], off
	s_waitcnt vmcnt(8)
	s_waitcnt lgkmcnt(0)
	s_barrier
; #define PG8_STAGE(bufoff, gbase, voff) do { _Pragma("unroll") for (int _i = 0; _i < 2; ++_i) \
;         __builtin_amdgcn_global_load_lds((const unsigned*)((const char*)(gbase) + (voff)[_i]), (LAS unsigned*)(lds + (bufoff) + ldsw + _i * 8192), 16, 0, 0); } while (0)
; #define PG8_LDA(dst, b, h) do { _Pragma("unroll") for (int m = 0; m < 4; ++m) _Pragma("unroll") for (int k = 0; k < 2; ++k) dst[m][k] = *(const LAS bf16x8*)(lds + PG8_SA(b, h) + aoff + m * 2048 + k * 1024); } while (0)
; #define PG8_LDB(dst, b, h) do { _Pragma("unroll") for (int n = 0; n < 2; ++n) _Pragma("unroll") for (int k = 0; k < 2; ++k) dst[n][k] = *(const LAS bf16x8*)(lds + PG8_SB(b, h) + boff + n * 2048 + k * 1024); } while (0)
; #define PG8_MMA(ai, bj, At, Bt) do { __builtin_amdgcn_s_setprio(1); _Pragma("unroll") for (int m = 0; m < 4; ++m) _Pragma("unroll") for (int n = 0; n < 2; ++n) _Pragma("unroll") for (int k = 0; k < 2; ++k) \
;         acc[ai][bj][m][n] = __builtin_amdgcn_mfma_f32_16x16x32_bf16(Bt[n][k], At[m][k], acc[ai][bj][m][n], 0, 0, 0); __builtin_amdgcn_s_setprio(0); } while (0)
; #define PG8_WAIT_V(n) asm volatile("s_waitcnt vmcnt(" #n ")" ::: "memory")
; #define PG8_WAIT_L(n) asm volatile("s_waitcnt lgkmcnt(" #n ")" ::: "memory")
; #define PG8_BAR __builtin_amdgcn_s_barrier()
; #define PG8_SCHED __builtin_amdgcn_sched_barrier(0)
; template <class Epi, class Sched>
; __device__ __forceinline__ void gemm_phase(LAS unsigned char* lds, const Gemm g, const Sched& S, const Epi& E, const int tid, unsigned* last_sig = nullptr) {
;     ...
;             PG8_WAIT_V(8); PG8_WAIT_L(0); PG8_BAR; PG8_MMA(1, 0, At, B0); PG8_MMA(1, 1, At, B1); PG8_BAR; PG8_SCHED;
;             PG8_LDB(B0, 1, 0); PG8_LDB(B1, 1, 1); PG8_SCHED; PG8_LDA(At, 1, 0); PG8_STAGE(PG8_SA(0, 1), a2 + hstep, voffA);
;             PG8_WAIT_V(8); PG8_WAIT_L(0); PG8_BAR; PG8_MMA(0, 0, At, B0); PG8_MMA(0, 1, At, B1); PG8_BAR; PG8_SCHED;
	s_setprio 1
	s_waitcnt lgkmcnt(0)
	v_mfma_f32_16x16x32_bf16 v[62:65], v[144:147], v[176:179], v[62:65]
	v_mfma_f32_16x16x32_bf16 v[58:61], v[152:155], v[176:179], v[58:61]
	v_mfma_f32_16x16x32_bf16 v[54:57], v[144:147], v[200:203], v[54:57]
	v_mfma_f32_16x16x32_bf16 v[50:53], v[152:155], v[200:203], v[50:53]
	v_mfma_f32_16x16x32_bf16 v[38:41], v[144:147], v[208:211], v[38:41]
	v_mfma_f32_16x16x32_bf16 v[34:37], v[152:155], v[208:211], v[34:37]
	v_mfma_f32_16x16x32_bf16 v[22:25], v[144:147], v[216:219], v[22:25]
	v_mfma_f32_16x16x32_bf16 v[18:21], v[152:155], v[216:219], v[18:21]
	v_mfma_f32_16x16x32_bf16 v[62:65], v[148:151], v[180:183], v[62:65]
	v_mfma_f32_16x16x32_bf16 v[58:61], v[156:159], v[180:183], v[58:61]
	v_mfma_f32_16x16x32_bf16 v[54:57], v[148:151], v[204:207], v[54:57]
	v_mfma_f32_16x16x32_bf16 v[50:53], v[156:159], v[204:207], v[50:53]
	v_mfma_f32_16x16x32_bf16 v[38:41], v[148:151], v[212:215], v[38:41]
	v_mfma_f32_16x16x32_bf16 v[34:37], v[156:159], v[212:215], v[34:37]
	v_mfma_f32_16x16x32_bf16 v[22:25], v[148:151], v[220:223], v[22:25]
	v_mfma_f32_16x16x32_bf16 v[18:21], v[156:159], v[220:223], v[18:21]
	v_mfma_f32_16x16x32_bf16 v[46:49], v[160:163], v[176:179], v[46:49]
	v_mfma_f32_16x16x32_bf16 v[42:45], v[168:171], v[176:179], v[42:45]
	v_mfma_f32_16x16x32_bf16 v[30:33], v[160:163], v[200:203], v[30:33]
	v_mfma_f32_16x16x32_bf16 v[26:29], v[168:171], v[200:203], v[26:29]
	v_mfma_f32_16x16x32_bf16 v[14:17], v[160:163], v[208:211], v[14:17]
	v_mfma_f32_16x16x32_bf16 v[10:13], v[168:171], v[208:211], v[10:13]
	v_mfma_f32_16x16x32_bf16 v[6:9], v[160:163], v[216:219], v[6:9]
	v_mfma_f32_16x16x32_bf16 v[2:5], v[168:171], v[216:219], v[2:5]
	v_mfma_f32_16x16x32_bf16 v[46:49], v[164:167], v[180:183], v[46:49]
	v_mfma_f32_16x16x32_bf16 v[42:45], v[172:175], v[180:183], v[42:45]
	v_mfma_f32_16x16x32_bf16 v[30:33], v[164:167], v[204:207], v[30:33]
	v_mfma_f32_16x16x32_bf16 v[26:29], v[172:175], v[204:207], v[26:29]
	v_mfma_f32_16x16x32_bf16 v[14:17], v[164:167], v[212:215], v[14:17]
	v_mfma_f32_16x16x32_bf16 v[10:13], v[172:175], v[212:215], v[10:13]
	v_mfma_f32_16x16x32_bf16 v[6:9], v[164:167], v[220:223], v[6:9]
	v_mfma_f32_16x16x32_bf16 v[2:5], v[172:175], v[220:223], v[2:5]
	s_setprio 0
	s_barrier
	s_add_i32 s16, 0, 0x18000
	s_add_i32 s17, 0, 0x1c000
	v_add_u32_e32 v156, s16, v141
	v_add_u32_e32 v172, s17, v141
	ds_read_b128 v[144:147], v156
	ds_read_b128 v[148:151], v156 offset:1024
	ds_read_b128 v[152:155], v156 offset:2048
	ds_read_b128 v[156:159], v156 offset:3072
	ds_read_b128 v[160:163], v172
	ds_read_b128 v[164:167], v172 offset:1024
	ds_read_b128 v[168:171], v172 offset:2048
	ds_read_b128 v[172:175], v172 offset:3072
	s_add_u32 s14, s22, 0xe0000
	s_addc_u32 s15, s23, 0
	s_mov_b32 m0, s44
	v_lshl_add_u64 v[238:239], s[14:15], 0, v[130:131]
	ds_read_b128 v[176:179], v143 offset:32768
	ds_read_b128 v[180:183], v143 offset:33792
	ds_read_b128 v[200:203], v143 offset:34816
	ds_read_b128 v[204:207], v143 offset:35840
	ds_read_b128 v[208:211], v143 offset:36864
	ds_read_b128 v[212:215], v143 offset:37888
	ds_read_b128 v[216:219], v143 offset:38912
	ds_read_b128 v[220:223], v143 offset:39936
	global_load_lds_dwordx4 v[238:239], off
	v_lshl_add_u64 v[238:239], s[14:15], 0, v[132:133]
	s_mov_b32 m0, s45
	s_nop 0
	global_load_lds_dwordx4 v[238:239], off
	s_waitcnt vmcnt(8)
	s_waitcnt lgkmcnt(0)
	s_barrier
	s_setprio 1
	s_waitcnt lgkmcnt(0)
	v_mfma_f32_16x16x32_bf16 v[126:129], v[144:147], v[176:179], v[126:129]
	v_mfma_f32_16x16x32_bf16 v[122:125], v[152:155], v[176:179], v[122:125]
	v_mfma_f32_16x16x32_bf16 v[118:121], v[144:147], v[200:203], v[118:121]
	v_mfma_f32_16x16x32_bf16 v[114:117], v[152:155], v[200:203], v[114:117]
	v_mfma_f32_16x16x32_bf16 v[102:105], v[144:147], v[208:211], v[102:105]
	v_mfma_f32_16x16x32_bf16 v[98:101], v[152:155], v[208:211], v[98:101]
	v_mfma_f32_16x16x32_bf16 v[86:89], v[144:147], v[216:219], v[86:89]
	v_mfma_f32_16x16x32_bf16 v[82:85], v[152:155], v[216:219], v[82:85]
	v_mfma_f32_16x16x32_bf16 v[126:129], v[148:151], v[180:183], v[126:129]
	v_mfma_f32_16x16x32_bf16 v[122:125], v[156:159], v[180:183], v[122:125]
	v_mfma_f32_16x16x32_bf16 v[118:121], v[148:151], v[204:207], v[118:121]
	v_mfma_f32_16x16x32_bf16 v[114:117], v[156:159], v[204:207], v[114:117]
	v_mfma_f32_16x16x32_bf16 v[102:105], v[148:151], v[212:215], v[102:105]
	v_mfma_f32_16x16x32_bf16 v[98:101], v[156:159], v[212:215], v[98:101]
	v_mfma_f32_16x16x32_bf16 v[86:89], v[148:151], v[220:223], v[86:89]
	v_mfma_f32_16x16x32_bf16 v[82:85], v[156:159], v[220:223], v[82:85]
	v_mfma_f32_16x16x32_bf16 v[110:113], v[160:163], v[176:179], v[110:113]
	v_mfma_f32_16x16x32_bf16 v[106:109], v[168:171], v[176:179], v[106:109]
	v_mfma_f32_16x16x32_bf16 v[94:97], v[160:163], v[200:203], v[94:97]
	v_mfma_f32_16x16x32_bf16 v[90:93], v[168:171], v[200:203], v[90:93]
	v_mfma_f32_16x16x32_bf16 v[78:81], v[160:163], v[208:211], v[78:81]
	v_mfma_f32_16x16x32_bf16 v[74:77], v[168:171], v[208:211], v[74:77]
	v_mfma_f32_16x16x32_bf16 v[70:73], v[160:163], v[216:219], v[70:73]
	v_mfma_f32_16x16x32_bf16 v[66:69], v[168:171], v[216:219], v[66:69]
	v_mfma_f32_16x16x32_bf16 v[110:113], v[164:167], v[180:183], v[110:113]
	v_mfma_f32_16x16x32_bf16 v[106:109], v[172:175], v[180:183], v[106:109]
	v_mfma_f32_16x16x32_bf16 v[94:97], v[164:167], v[204:207], v[94:97]
	v_mfma_f32_16x16x32_bf16 v[90:93], v[172:175], v[204:207], v[90:93]
	v_mfma_f32_16x16x32_bf16 v[78:81], v[164:167], v[212:215], v[78:81]
	v_mfma_f32_16x16x32_bf16 v[74:77], v[172:175], v[212:215], v[74:77]
	v_mfma_f32_16x16x32_bf16 v[70:73], v[164:167], v[220:223], v[70:73]
	v_mfma_f32_16x16x32_bf16 v[66:69], v[172:175], v[220:223], v[66:69]
	s_setprio 0
	s_barrier
; #define PG8_STAGE(bufoff, gbase, voff) do { _Pragma("unroll") for (int _i = 0; _i < 2; ++_i) \
;         __builtin_amdgcn_global_load_lds((const unsigned*)((const char*)(gbase) + (voff)[_i]), (LAS unsigned*)(lds + (bufoff) + ldsw + _i * 8192), 16, 0, 0); } while (0)
; #define PG8_LDA(dst, b, h) do { _Pragma("unroll") for (int m = 0; m < 4; ++m) _Pragma("unroll") for (int k = 0; k < 2; ++k) dst[m][k] = *(const LAS bf16x8*)(lds + PG8_SA(b, h) + aoff + m * 2048 + k * 1024); } while (0)
; #define PG8_MMA(ai, bj, At, Bt) do { __builtin_amdgcn_s_setprio(1); _Pragma("unroll") for (int m = 0; m < 4; ++m) _Pragma("unroll") for (int n = 0; n < 2; ++n) _Pragma("unroll") for (int k = 0; k < 2; ++k) \
;         acc[ai][bj][m][n] = __builtin_amdgcn_mfma_f32_16x16x32_bf16(Bt[n][k], At[m][k], acc[ai][bj][m][n], 0, 0, 0); __builtin_amdgcn_s_setprio(0); } while (0)
; #define PG8_WAIT_V(n) asm volatile("s_waitcnt vmcnt(" #n ")" ::: "memory")
; #define PG8_WAIT_L(n) asm volatile("s_waitcnt lgkmcnt(" #n ")" ::: "memory")
; #define PG8_BAR __builtin_amdgcn_s_barrier()
; #define PG8_SCHED __builtin_amdgcn_sched_barrier(0)
; template <class Epi, class Sched>
; __device__ __forceinline__ void gemm_phase(LAS unsigned char* lds, const Gemm g, const Sched& S, const Epi& E, const int tid, unsigned* last_sig = nullptr) {
;     ...
;             PG8_LDA(At, 1, 1); PG8_STAGE(PG8_SB(1, 0), b3, voffB); PG8_STAGE(PG8_SB(1, 1), b3 + hstep, voffB); PG8_STAGE(PG8_SA(1, 0), a3, voffA);
;             PG8_WAIT_V(8); PG8_WAIT_L(0); PG8_BAR; PG8_MMA(1, 0, At, B0); PG8_MMA(1, 1, At, B1); PG8_BAR; PG8_SCHED;
;         }
;         if (wr == 0) PG8_BAR;
	s_add_i32 s14, s16, s40
	v_lshl_add_u64 v[184:185], v[184:185], 0, s[34:35]
	s_mov_b32 m0, s14
	ds_read_b128 v[176:179], v143 offset:49152
	ds_read_b128 v[180:183], v143 offset:50176
	ds_read_b128 v[200:203], v143 offset:51200
	ds_read_b128 v[204:207], v143 offset:52224
	ds_read_b128 v[208:211], v143 offset:53248
	ds_read_b128 v[212:215], v143 offset:54272
	ds_read_b128 v[216:219], v143 offset:55296
	ds_read_b128 v[220:223], v143 offset:56320
	global_load_lds_dwordx4 v[184:185], off
	s_add_i32 m0, s14, 0x2000
	s_add_u32 s14, s20, 0xe0080
	v_lshl_add_u64 v[184:185], v[232:233], 0, s[34:35]
	s_addc_u32 s15, s21, 0
	s_add_i32 s16, s17, s40
	global_load_lds_dwordx4 v[184:185], off
	v_lshl_add_u64 v[184:185], s[14:15], 0, v[186:187]
	s_mov_b32 m0, s16
	s_nop 0
	global_load_lds_dwordx4 v[184:185], off
	v_lshl_add_u64 v[184:185], s[14:15], 0, v[134:135]
	s_add_i32 m0, s16, 0x2000
	s_nop 0
	global_load_lds_dwordx4 v[184:185], off
	v_lshl_add_u64 v[184:185], v[234:235], 0, s[34:35]
	s_mov_b32 m0, s47
	s_nop 0
	global_load_lds_dwordx4 v[184:185], off
	v_lshl_add_u64 v[184:185], v[236:237], 0, s[34:35]
	s_mov_b32 m0, s49
	s_nop 0
	global_load_lds_dwordx4 v[184:185], off
	s_waitcnt vmcnt(8)
	s_waitcnt lgkmcnt(0)
	s_barrier
	s_setprio 1
	s_waitcnt lgkmcnt(0)
	v_mfma_f32_16x16x32_bf16 v[62:65], v[144:147], v[176:179], v[62:65]
	v_mfma_f32_16x16x32_bf16 v[58:61], v[152:155], v[176:179], v[58:61]
	v_mfma_f32_16x16x32_bf16 v[54:57], v[144:147], v[200:203], v[54:57]
	v_mfma_f32_16x16x32_bf16 v[50:53], v[152:155], v[200:203], v[50:53]
	v_mfma_f32_16x16x32_bf16 v[38:41], v[144:147], v[208:211], v[38:41]
	v_mfma_f32_16x16x32_bf16 v[34:37], v[152:155], v[208:211], v[34:37]
	v_mfma_f32_16x16x32_bf16 v[22:25], v[144:147], v[216:219], v[22:25]
	v_mfma_f32_16x16x32_bf16 v[18:21], v[152:155], v[216:219], v[18:21]
	v_mfma_f32_16x16x32_bf16 v[62:65], v[148:151], v[180:183], v[62:65]
	v_mfma_f32_16x16x32_bf16 v[58:61], v[156:159], v[180:183], v[58:61]
	v_mfma_f32_16x16x32_bf16 v[54:57], v[148:151], v[204:207], v[54:57]
	v_mfma_f32_16x16x32_bf16 v[50:53], v[156:159], v[204:207], v[50:53]
	v_mfma_f32_16x16x32_bf16 v[38:41], v[148:151], v[212:215], v[38:41]
	v_mfma_f32_16x16x32_bf16 v[34:37], v[156:159], v[212:215], v[34:37]
	v_mfma_f32_16x16x32_bf16 v[22:25], v[148:151], v[220:223], v[22:25]
	v_mfma_f32_16x16x32_bf16 v[18:21], v[156:159], v[220:223], v[18:21]
	v_mfma_f32_16x16x32_bf16 v[46:49], v[160:163], v[176:179], v[46:49]
	v_mfma_f32_16x16x32_bf16 v[42:45], v[168:171], v[176:179], v[42:45]
	v_mfma_f32_16x16x32_bf16 v[30:33], v[160:163], v[200:203], v[30:33]
	v_mfma_f32_16x16x32_bf16 v[26:29], v[168:171], v[200:203], v[26:29]
	v_mfma_f32_16x16x32_bf16 v[14:17], v[160:163], v[208:211], v[14:17]
	v_mfma_f32_16x16x32_bf16 v[10:13], v[168:171], v[208:211], v[10:13]
	v_mfma_f32_16x16x32_bf16 v[6:9], v[160:163], v[216:219], v[6:9]
	v_mfma_f32_16x16x32_bf16 v[2:5], v[168:171], v[216:219], v[2:5]
	v_mfma_f32_16x16x32_bf16 v[46:49], v[164:167], v[180:183], v[46:49]
	v_mfma_f32_16x16x32_bf16 v[42:45], v[172:175], v[180:183], v[42:45]
	v_mfma_f32_16x16x32_bf16 v[30:33], v[164:167], v[204:207], v[30:33]
	v_mfma_f32_16x16x32_bf16 v[26:29], v[172:175], v[204:207], v[26:29]
	v_mfma_f32_16x16x32_bf16 v[14:17], v[164:167], v[212:215], v[14:17]
	v_mfma_f32_16x16x32_bf16 v[10:13], v[172:175], v[212:215], v[10:13]
	v_mfma_f32_16x16x32_bf16 v[6:9], v[164:167], v[220:223], v[6:9]
	v_mfma_f32_16x16x32_bf16 v[2:5], v[172:175], v[220:223], v[2:5]
	s_setprio 0
	s_barrier
	s_add_i32 s56, s56, 2
	s_add_u32 s54, s54, 0x100
	s_addc_u32 s55, s55, 0
	s_cmp_gt_u32 s56, 53
	s_mov_b64 s[16:17], s[18:19]
	s_cbranch_scc0 .LBB0_1262
	s_and_b64 vcc, exec, s[10:11]
	s_cbranch_vccz .LBB0_1265
	s_barrier

; #define PG8_STAGE(bufoff, gbase, voff) do { _Pragma("unroll") for (int _i = 0; _i < 2; ++_i) \
;         __builtin_amdgcn_global_load_lds((const unsigned*)((const char*)(gbase) + (voff)[_i]), (LAS unsigned*)(lds + (bufoff) + ldsw + _i * 8192), 16, 0, 0); } while (0)
; #define PG8_LDA(dst, b, h) do { _Pragma("unroll") for (int m = 0; m < 4; ++m) _Pragma("unroll") for (int k = 0; k < 2; ++k) dst[m][k] = *(const LAS bf16x8*)(lds + PG8_SA(b, h) + aoff + m * 2048 + k * 1024); } while (0)
; #define PG8_LDB(dst, b, h) do { _Pragma("unroll") for (int n = 0; n < 2; ++n) _Pragma("unroll") for (int k = 0; k < 2; ++k) dst[n][k] = *(const LAS bf16x8*)(lds + PG8_SB(b, h) + boff + n * 2048 + k * 1024); } while (0)
; #define PG8_MMA(ai, bj, At, Bt) do { __builtin_amdgcn_s_setprio(1); _Pragma("unroll") for (int m = 0; m < 4; ++m) _Pragma("unroll") for (int n = 0; n < 2; ++n) _Pragma("unroll") for (int k = 0; k < 2; ++k) \
;         acc[ai][bj][m][n] = __builtin_amdgcn_mfma_f32_16x16x32_bf16(Bt[n][k], At[m][k], acc[ai][bj][m][n], 0, 0, 0); __builtin_amdgcn_s_setprio(0); } while (0)
; #define PG8_WAIT_V(n) asm volatile("s_waitcnt vmcnt(" #n ")" ::: "memory")
; #define PG8_WAIT_L(n) asm volatile("s_waitcnt lgkmcnt(" #n ")" ::: "memory")
; #define PG8_BAR __builtin_amdgcn_s_barrier()
; template <class Epi, class Sched>
; __device__ __forceinline__ void gemm_phase(LAS unsigned char* lds, const Gemm g, const Sched& S, const Epi& E, const int tid, unsigned* last_sig = nullptr) {
;     ...
;         for (int t = 0; t < nt; t += 2) {
;             const bool last = (t == nt - 2);
;             const char* a1 = cA + (size_t)(t + 1) * kstep;
;             const char* a2 = last ? nA : cA + (size_t)(t + 2) * kstep; const char* b2 = last ? nB : cB + (size_t)(t + 2) * kstep;
;             const char* a3 = a2 + kstep; const char* b3 = b2 + kstep;
;             PG8_LDB(B0, 0, 0); PG8_LDB(B1, 0, 1); PG8_SCHED; PG8_LDA(At, 0, 0); PG8_STAGE(PG8_SA(1, 1), a1 + hstep, voffA);
;             PG8_WAIT_V(8); PG8_WAIT_L(0); PG8_BAR; PG8_MMA(0, 0, At, B0); PG8_MMA(0, 1, At, B1); PG8_BAR; PG8_SCHED;
;             PG8_LDA(At, 0, 1); PG8_STAGE(PG8_SB(0, 0), b2, voffB); PG8_STAGE(PG8_SB(0, 1), b2 + hstep, voffB); PG8_STAGE(PG8_SA(0, 0), a2, voffA);
;             PG8_WAIT_V(8); PG8_WAIT_L(0); PG8_BAR; PG8_MMA(1, 0, At, B0); PG8_MMA(1, 1, At, B1); PG8_BAR; PG8_SCHED;
.LBB0_1288:
	s_add_u32 s16, s12, 0x100
	s_addc_u32 s17, s13, 0
	s_add_i32 s14, 0, 0x10000
	s_cmpk_eq_i32 s50, 0x54
	s_cselect_b32 s21, s5, s17
	s_cselect_b32 s20, s4, s16
	v_add_u32_e32 v151, s14, v148
	s_cselect_b32 s19, s11, s49
	s_cselect_b32 s18, s10, s48
	s_add_i32 s15, 0, 0x14000
	ds_read_b128 v[136:139], v151
	ds_read_b128 v[140:143], v151 offset:1024
	ds_read_b128 v[144:147], v151 offset:2048
	ds_read_b128 v[152:155], v151 offset:3072
	v_add_u32_e32 v151, s15, v148
	ds_read_b128 v[156:159], v151
	ds_read_b128 v[160:163], v151 offset:1024
	ds_read_b128 v[164:167], v151 offset:2048
	ds_read_b128 v[168:171], v151 offset:3072
	v_lshl_add_u64 v[184:185], s[12:13], 0, v[132:133]
	s_add_i32 m0, s23, 0xc000
	ds_read_b128 v[172:175], v150
	ds_read_b128 v[176:179], v150 offset:1024
	ds_read_b128 v[180:183], v150 offset:2048
	ds_read_b128 v[200:203], v150 offset:3072
	ds_read_b128 v[204:207], v150 offset:4096
	ds_read_b128 v[208:211], v150 offset:5120
	ds_read_b128 v[212:215], v150 offset:6144
	ds_read_b128 v[216:219], v150 offset:7168
	global_load_lds_dwordx4 v[184:185], off
	v_lshl_add_u64 v[184:185], s[12:13], 0, v[134:135]
	s_add_i32 m0, s23, 0xe000
	s_nop 0
	global_load_lds_dwordx4 v[184:185], off
	s_waitcnt vmcnt(8)
	s_waitcnt lgkmcnt(0)
	s_barrier
	s_setprio 1
	s_waitcnt lgkmcnt(0)
	v_mfma_f32_16x16x32_bf16 v[126:129], v[136:139], v[172:175], v[126:129]
	v_mfma_f32_16x16x32_bf16 v[122:125], v[144:147], v[172:175], v[122:125]
	v_mfma_f32_16x16x32_bf16 v[118:121], v[136:139], v[180:183], v[118:121]
	v_mfma_f32_16x16x32_bf16 v[114:117], v[144:147], v[180:183], v[114:117]
	v_mfma_f32_16x16x32_bf16 v[106:109], v[136:139], v[204:207], v[106:109]
	v_mfma_f32_16x16x32_bf16 v[98:101], v[144:147], v[204:207], v[98:101]
	v_mfma_f32_16x16x32_bf16 v[90:93], v[136:139], v[212:215], v[90:93]
	v_mfma_f32_16x16x32_bf16 v[82:85], v[144:147], v[212:215], v[82:85]
	v_mfma_f32_16x16x32_bf16 v[126:129], v[140:143], v[176:179], v[126:129]
	v_mfma_f32_16x16x32_bf16 v[122:125], v[152:155], v[176:179], v[122:125]
	v_mfma_f32_16x16x32_bf16 v[118:121], v[140:143], v[200:203], v[118:121]
	v_mfma_f32_16x16x32_bf16 v[114:117], v[152:155], v[200:203], v[114:117]
	v_mfma_f32_16x16x32_bf16 v[106:109], v[140:143], v[208:211], v[106:109]
	v_mfma_f32_16x16x32_bf16 v[98:101], v[152:155], v[208:211], v[98:101]
	v_mfma_f32_16x16x32_bf16 v[90:93], v[140:143], v[216:219], v[90:93]
	v_mfma_f32_16x16x32_bf16 v[82:85], v[152:155], v[216:219], v[82:85]
	v_mfma_f32_16x16x32_bf16 v[110:113], v[156:159], v[172:175], v[110:113]
	v_mfma_f32_16x16x32_bf16 v[102:105], v[164:167], v[172:175], v[102:105]
	v_mfma_f32_16x16x32_bf16 v[94:97], v[156:159], v[180:183], v[94:97]
	v_mfma_f32_16x16x32_bf16 v[86:89], v[164:167], v[180:183], v[86:89]
	v_mfma_f32_16x16x32_bf16 v[78:81], v[156:159], v[204:207], v[78:81]
	v_mfma_f32_16x16x32_bf16 v[74:77], v[164:167], v[204:207], v[74:77]
	v_mfma_f32_16x16x32_bf16 v[70:73], v[156:159], v[212:215], v[70:73]
	v_mfma_f32_16x16x32_bf16 v[66:69], v[164:167], v[212:215], v[66:69]
	v_mfma_f32_16x16x32_bf16 v[110:113], v[160:163], v[176:179], v[110:113]
	v_mfma_f32_16x16x32_bf16 v[102:105], v[168:171], v[176:179], v[102:105]
	v_mfma_f32_16x16x32_bf16 v[94:97], v[160:163], v[200:203], v[94:97]
	v_mfma_f32_16x16x32_bf16 v[86:89], v[168:171], v[200:203], v[86:89]
	v_mfma_f32_16x16x32_bf16 v[78:81], v[160:163], v[208:211], v[78:81]
	v_mfma_f32_16x16x32_bf16 v[74:77], v[168:171], v[208:211], v[74:77]
	v_mfma_f32_16x16x32_bf16 v[70:73], v[160:163], v[216:219], v[70:73]
	v_mfma_f32_16x16x32_bf16 v[66:69], v[168:171], v[216:219], v[66:69]
	s_setprio 0
	s_barrier
	s_add_i32 s12, s14, s22
	v_lshl_add_u64 v[184:185], s[18:19], 0, v[186:187]
	s_mov_b32 m0, s12
	ds_read_b128 v[172:175], v150 offset:16384
	ds_read_b128 v[176:179], v150 offset:17408
	ds_read_b128 v[180:183], v150 offset:18432
	ds_read_b128 v[200:203], v150 offset:19456
	ds_read_b128 v[204:207], v150 offset:20480
	ds_read_b128 v[208:211], v150 offset:21504
	ds_read_b128 v[212:215], v150 offset:22528
	ds_read_b128 v[216:219], v150 offset:23552
	global_load_lds_dwordx4 v[184:185], off
	s_add_i32 m0, s12, 0x2000
	s_add_u32 s12, s18, 0x160000
	v_lshl_add_u64 v[220:221], s[18:19], 0, v[130:131]
	s_addc_u32 s13, s19, 0
	s_add_i32 s14, s15, s22
	global_load_lds_dwordx4 v[220:221], off
	v_lshl_add_u64 v[222:223], s[12:13], 0, v[186:187]
	s_mov_b32 m0, s14
	v_lshl_add_u64 v[232:233], s[20:21], 0, v[130:131]
	global_load_lds_dwordx4 v[222:223], off
	v_lshl_add_u64 v[222:223], s[12:13], 0, v[130:131]
	s_add_i32 m0, s14, 0x2000
	s_nop 0
	global_load_lds_dwordx4 v[222:223], off
	v_lshl_add_u64 v[222:223], s[20:21], 0, v[186:187]
	s_mov_b32 m0, s23
	s_nop 0
	global_load_lds_dwordx4 v[222:223], off
	s_mov_b32 m0, s28
	s_nop 0
	global_load_lds_dwordx4 v[232:233], off
	s_waitcnt vmcnt(8)
	s_waitcnt lgkmcnt(0)
	s_barrier
; #define PG8_STAGE(bufoff, gbase, voff) do { _Pragma("unroll") for (int _i = 0; _i < 2; ++_i) \
;         __builtin_amdgcn_global_load_lds((const unsigned*)((const char*)(gbase) + (voff)[_i]), (LAS unsigned*)(lds + (bufoff) + ldsw + _i * 8192), 16, 0, 0); } while (0)
; #define PG8_LDA(dst, b, h) do { _Pragma("unroll") for (int m = 0; m < 4; ++m) _Pragma("unroll") for (int k = 0; k < 2; ++k) dst[m][k] = *(const LAS bf16x8*)(lds + PG8_SA(b, h) + aoff + m * 2048 + k * 1024); } while (0)
; #define PG8_LDB(dst, b, h) do { _Pragma("unroll") for (int n = 0; n < 2; ++n) _Pragma("unroll") for (int k = 0; k < 2; ++k) dst[n][k] = *(const LAS bf16x8*)(lds + PG8_SB(b, h) + boff + n * 2048 + k * 1024); } while (0)
; #define PG8_MMA(ai, bj, At, Bt) do { __builtin_amdgcn_s_setprio(1); _Pragma("unroll") for (int m = 0; m < 4; ++m) _Pragma("unroll") for (int n = 0; n < 2; ++n) _Pragma("unroll") for (int k = 0; k < 2; ++k) \
;         acc[ai][bj][m][n] = __builtin_amdgcn_mfma_f32_16x16x32_bf16(Bt[n][k], At[m][k], acc[ai][bj][m][n], 0, 0, 0); __builtin_amdgcn_s_setprio(0); } while (0)
; #define PG8_WAIT_V(n) asm volatile("s_waitcnt vmcnt(" #n ")" ::: "memory")
; #define PG8_WAIT_L(n) asm volatile("s_waitcnt lgkmcnt(" #n ")" ::: "memory")
; #define PG8_BAR __builtin_amdgcn_s_barrier()
; #define PG8_SCHED __builtin_amdgcn_sched_barrier(0)
; template <class Epi, class Sched>
; __device__ __forceinline__ void gemm_phase(LAS unsigned char* lds, const Gemm g, const Sched& S, const Epi& E, const int tid, unsigned* last_sig = nullptr) {
;     ...
;             PG8_WAIT_V(8); PG8_WAIT_L(0); PG8_BAR; PG8_MMA(1, 0, At, B0); PG8_MMA(1, 1, At, B1); PG8_BAR; PG8_SCHED;
;             PG8_LDB(B0, 1, 0); PG8_LDB(B1, 1, 1); PG8_SCHED; PG8_LDA(At, 1, 0); PG8_STAGE(PG8_SA(0, 1), a2 + hstep, voffA);
;             PG8_WAIT_V(8); PG8_WAIT_L(0); PG8_BAR; PG8_MMA(0, 0, At, B0); PG8_MMA(0, 1, At, B1); PG8_BAR; PG8_SCHED;
	s_setprio 1
	s_waitcnt lgkmcnt(0)
	v_mfma_f32_16x16x32_bf16 v[62:65], v[136:139], v[172:175], v[62:65]
	v_mfma_f32_16x16x32_bf16 v[58:61], v[144:147], v[172:175], v[58:61]
	v_mfma_f32_16x16x32_bf16 v[54:57], v[136:139], v[180:183], v[54:57]
	v_mfma_f32_16x16x32_bf16 v[46:49], v[144:147], v[180:183], v[46:49]
	v_mfma_f32_16x16x32_bf16 v[38:41], v[136:139], v[204:207], v[38:41]
	v_mfma_f32_16x16x32_bf16 v[30:33], v[144:147], v[204:207], v[30:33]
	v_mfma_f32_16x16x32_bf16 v[22:25], v[136:139], v[212:215], v[22:25]
	v_mfma_f32_16x16x32_bf16 v[14:17], v[144:147], v[212:215], v[14:17]
	v_mfma_f32_16x16x32_bf16 v[62:65], v[140:143], v[176:179], v[62:65]
	v_mfma_f32_16x16x32_bf16 v[58:61], v[152:155], v[176:179], v[58:61]
	v_mfma_f32_16x16x32_bf16 v[54:57], v[140:143], v[200:203], v[54:57]
	v_mfma_f32_16x16x32_bf16 v[46:49], v[152:155], v[200:203], v[46:49]
	v_mfma_f32_16x16x32_bf16 v[38:41], v[140:143], v[208:211], v[38:41]
	v_mfma_f32_16x16x32_bf16 v[30:33], v[152:155], v[208:211], v[30:33]
	v_mfma_f32_16x16x32_bf16 v[22:25], v[140:143], v[216:219], v[22:25]
	v_mfma_f32_16x16x32_bf16 v[14:17], v[152:155], v[216:219], v[14:17]
	v_mfma_f32_16x16x32_bf16 v[50:53], v[156:159], v[172:175], v[50:53]
	v_mfma_f32_16x16x32_bf16 v[42:45], v[164:167], v[172:175], v[42:45]
	v_mfma_f32_16x16x32_bf16 v[34:37], v[156:159], v[180:183], v[34:37]
	v_mfma_f32_16x16x32_bf16 v[26:29], v[164:167], v[180:183], v[26:29]
	v_mfma_f32_16x16x32_bf16 v[18:21], v[156:159], v[204:207], v[18:21]
	v_mfma_f32_16x16x32_bf16 v[10:13], v[164:167], v[204:207], v[10:13]
	v_mfma_f32_16x16x32_bf16 v[6:9], v[156:159], v[212:215], v[6:9]
	v_mfma_f32_16x16x32_bf16 v[2:5], v[164:167], v[212:215], v[2:5]
	v_mfma_f32_16x16x32_bf16 v[50:53], v[160:163], v[176:179], v[50:53]
	v_mfma_f32_16x16x32_bf16 v[42:45], v[168:171], v[176:179], v[42:45]
	v_mfma_f32_16x16x32_bf16 v[34:37], v[160:163], v[200:203], v[34:37]
	v_mfma_f32_16x16x32_bf16 v[26:29], v[168:171], v[200:203], v[26:29]
	v_mfma_f32_16x16x32_bf16 v[18:21], v[160:163], v[208:211], v[18:21]
	v_mfma_f32_16x16x32_bf16 v[10:13], v[168:171], v[208:211], v[10:13]
	v_mfma_f32_16x16x32_bf16 v[6:9], v[160:163], v[216:219], v[6:9]
	v_mfma_f32_16x16x32_bf16 v[2:5], v[168:171], v[216:219], v[2:5]
	s_setprio 0
	s_barrier
	s_add_i32 s14, 0, 0x18000
	v_add_u32_e32 v151, s14, v148
	s_add_i32 s15, 0, 0x1c000
	ds_read_b128 v[136:139], v151
	ds_read_b128 v[140:143], v151 offset:1024
	ds_read_b128 v[144:147], v151 offset:2048
	ds_read_b128 v[152:155], v151 offset:3072
	v_add_u32_e32 v151, s15, v148
	ds_read_b128 v[156:159], v151
	ds_read_b128 v[160:163], v151 offset:1024
	ds_read_b128 v[164:167], v151 offset:2048
	ds_read_b128 v[168:171], v151 offset:3072
	s_add_u32 s12, s20, 0x160000
	s_addc_u32 s13, s21, 0
	s_mov_b32 m0, s31
	v_lshl_add_u64 v[234:235], s[12:13], 0, v[186:187]
	ds_read_b128 v[172:175], v150 offset:32768
	ds_read_b128 v[176:179], v150 offset:33792
	ds_read_b128 v[180:183], v150 offset:34816
	ds_read_b128 v[200:203], v150 offset:35840
	ds_read_b128 v[204:207], v150 offset:36864
	ds_read_b128 v[208:211], v150 offset:37888
	ds_read_b128 v[212:215], v150 offset:38912
	ds_read_b128 v[216:219], v150 offset:39936
	global_load_lds_dwordx4 v[234:235], off
	v_lshl_add_u64 v[234:235], s[12:13], 0, v[130:131]
	s_mov_b32 m0, s40
	s_nop 0
	global_load_lds_dwordx4 v[234:235], off
	s_waitcnt vmcnt(8)
	s_waitcnt lgkmcnt(0)
	s_barrier
	s_setprio 1
	s_waitcnt lgkmcnt(0)
	v_mfma_f32_16x16x32_bf16 v[126:129], v[136:139], v[172:175], v[126:129]
	v_mfma_f32_16x16x32_bf16 v[122:125], v[144:147], v[172:175], v[122:125]
	v_mfma_f32_16x16x32_bf16 v[118:121], v[136:139], v[180:183], v[118:121]
	v_mfma_f32_16x16x32_bf16 v[114:117], v[144:147], v[180:183], v[114:117]
	v_mfma_f32_16x16x32_bf16 v[106:109], v[136:139], v[204:207], v[106:109]
	v_mfma_f32_16x16x32_bf16 v[98:101], v[144:147], v[204:207], v[98:101]
	v_mfma_f32_16x16x32_bf16 v[90:93], v[136:139], v[212:215], v[90:93]
	v_mfma_f32_16x16x32_bf16 v[82:85], v[144:147], v[212:215], v[82:85]
	v_mfma_f32_16x16x32_bf16 v[126:129], v[140:143], v[176:179], v[126:129]
	v_mfma_f32_16x16x32_bf16 v[122:125], v[152:155], v[176:179], v[122:125]
	v_mfma_f32_16x16x32_bf16 v[118:121], v[140:143], v[200:203], v[118:121]
	v_mfma_f32_16x16x32_bf16 v[114:117], v[152:155], v[200:203], v[114:117]
	v_mfma_f32_16x16x32_bf16 v[106:109], v[140:143], v[208:211], v[106:109]
	v_mfma_f32_16x16x32_bf16 v[98:101], v[152:155], v[208:211], v[98:101]
	v_mfma_f32_16x16x32_bf16 v[90:93], v[140:143], v[216:219], v[90:93]
	v_mfma_f32_16x16x32_bf16 v[82:85], v[152:155], v[216:219], v[82:85]
	v_mfma_f32_16x16x32_bf16 v[110:113], v[156:159], v[172:175], v[110:113]
	v_mfma_f32_16x16x32_bf16 v[102:105], v[164:167], v[172:175], v[102:105]
	v_mfma_f32_16x16x32_bf16 v[94:97], v[156:159], v[180:183], v[94:97]
	v_mfma_f32_16x16x32_bf16 v[86:89], v[164:167], v[180:183], v[86:89]
	v_mfma_f32_16x16x32_bf16 v[78:81], v[156:159], v[204:207], v[78:81]
	v_mfma_f32_16x16x32_bf16 v[74:77], v[164:167], v[204:207], v[74:77]
	v_mfma_f32_16x16x32_bf16 v[70:73], v[156:159], v[212:215], v[70:73]
	v_mfma_f32_16x16x32_bf16 v[66:69], v[164:167], v[212:215], v[66:69]
	v_mfma_f32_16x16x32_bf16 v[110:113], v[160:163], v[176:179], v[110:113]
	v_mfma_f32_16x16x32_bf16 v[102:105], v[168:171], v[176:179], v[102:105]
	v_mfma_f32_16x16x32_bf16 v[94:97], v[160:163], v[200:203], v[94:97]
	v_mfma_f32_16x16x32_bf16 v[86:89], v[168:171], v[200:203], v[86:89]
	v_mfma_f32_16x16x32_bf16 v[78:81], v[160:163], v[208:211], v[78:81]
	v_mfma_f32_16x16x32_bf16 v[74:77], v[168:171], v[208:211], v[74:77]
	v_mfma_f32_16x16x32_bf16 v[70:73], v[160:163], v[216:219], v[70:73]
	v_mfma_f32_16x16x32_bf16 v[66:69], v[168:171], v[216:219], v[66:69]
	s_setprio 0
	s_barrier
; #define PG8_STAGE(bufoff, gbase, voff) do { _Pragma("unroll") for (int _i = 0; _i < 2; ++_i) \
;         __builtin_amdgcn_global_load_lds((const unsigned*)((const char*)(gbase) + (voff)[_i]), (LAS unsigned*)(lds + (bufoff) + ldsw + _i * 8192), 16, 0, 0); } while (0)
; #define PG8_LDA(dst, b, h) do { _Pragma("unroll") for (int m = 0; m < 4; ++m) _Pragma("unroll") for (int k = 0; k < 2; ++k) dst[m][k] = *(const LAS bf16x8*)(lds + PG8_SA(b, h) + aoff + m * 2048 + k * 1024); } while (0)
; #define PG8_MMA(ai, bj, At, Bt) do { __builtin_amdgcn_s_setprio(1); _Pragma("unroll") for (int m = 0; m < 4; ++m) _Pragma("unroll") for (int n = 0; n < 2; ++n) _Pragma("unroll") for (int k = 0; k < 2; ++k) \
;         acc[ai][bj][m][n] = __builtin_amdgcn_mfma_f32_16x16x32_bf16(Bt[n][k], At[m][k], acc[ai][bj][m][n], 0, 0, 0); __builtin_amdgcn_s_setprio(0); } while (0)
; #define PG8_WAIT_V(n) asm volatile("s_waitcnt vmcnt(" #n ")" ::: "memory")
; #define PG8_WAIT_L(n) asm volatile("s_waitcnt lgkmcnt(" #n ")" ::: "memory")
; #define PG8_BAR __builtin_amdgcn_s_barrier()
; #define PG8_SCHED __builtin_amdgcn_sched_barrier(0)
; template <class Epi, class Sched>
; __device__ __forceinline__ void gemm_phase(LAS unsigned char* lds, const Gemm g, const Sched& S, const Epi& E, const int tid, unsigned* last_sig = nullptr) {
;     ...
;             PG8_LDA(At, 1, 1); PG8_STAGE(PG8_SB(1, 0), b3, voffB); PG8_STAGE(PG8_SB(1, 1), b3 + hstep, voffB); PG8_STAGE(PG8_SA(1, 0), a3, voffA);
;             PG8_WAIT_V(8); PG8_WAIT_L(0); PG8_BAR; PG8_MMA(1, 0, At, B0); PG8_MMA(1, 1, At, B1); PG8_BAR; PG8_SCHED;
;         }
;         if (wr == 0) PG8_BAR;
	s_add_i32 s12, s14, s22
	v_lshl_add_u64 v[184:185], v[184:185], 0, s[34:35]
	s_mov_b32 m0, s12
	ds_read_b128 v[172:175], v150 offset:49152
	ds_read_b128 v[176:179], v150 offset:50176
	ds_read_b128 v[180:183], v150 offset:51200
	ds_read_b128 v[200:203], v150 offset:52224
	ds_read_b128 v[204:207], v150 offset:53248
	ds_read_b128 v[208:211], v150 offset:54272
	ds_read_b128 v[212:215], v150 offset:55296
	ds_read_b128 v[216:219], v150 offset:56320
	global_load_lds_dwordx4 v[184:185], off
	s_add_i32 m0, s12, 0x2000
	s_add_u32 s12, s18, 0x160080
	v_lshl_add_u64 v[184:185], v[220:221], 0, s[34:35]
	s_addc_u32 s13, s19, 0
	s_add_i32 s14, s15, s22
	global_load_lds_dwordx4 v[184:185], off
	v_lshl_add_u64 v[184:185], s[12:13], 0, v[186:187]
	s_mov_b32 m0, s14
	s_nop 0
	global_load_lds_dwordx4 v[184:185], off
	v_lshl_add_u64 v[184:185], s[12:13], 0, v[130:131]
	s_add_i32 m0, s14, 0x2000
	s_nop 0
	global_load_lds_dwordx4 v[184:185], off
	v_lshl_add_u64 v[184:185], v[222:223], 0, s[34:35]
	s_mov_b32 m0, s41
	s_nop 0
	global_load_lds_dwordx4 v[184:185], off
	v_lshl_add_u64 v[184:185], v[232:233], 0, s[34:35]
	s_mov_b32 m0, s42
	s_nop 0
	global_load_lds_dwordx4 v[184:185], off
	s_waitcnt vmcnt(8)
	s_waitcnt lgkmcnt(0)
	s_barrier
	s_setprio 1
	s_waitcnt lgkmcnt(0)
	v_mfma_f32_16x16x32_bf16 v[62:65], v[136:139], v[172:175], v[62:65]
	v_mfma_f32_16x16x32_bf16 v[58:61], v[144:147], v[172:175], v[58:61]
	v_mfma_f32_16x16x32_bf16 v[54:57], v[136:139], v[180:183], v[54:57]
	v_mfma_f32_16x16x32_bf16 v[46:49], v[144:147], v[180:183], v[46:49]
	v_mfma_f32_16x16x32_bf16 v[38:41], v[136:139], v[204:207], v[38:41]
	v_mfma_f32_16x16x32_bf16 v[30:33], v[144:147], v[204:207], v[30:33]
	v_mfma_f32_16x16x32_bf16 v[22:25], v[136:139], v[212:215], v[22:25]
	v_mfma_f32_16x16x32_bf16 v[14:17], v[144:147], v[212:215], v[14:17]
	v_mfma_f32_16x16x32_bf16 v[62:65], v[140:143], v[176:179], v[62:65]
	v_mfma_f32_16x16x32_bf16 v[58:61], v[152:155], v[176:179], v[58:61]
	v_mfma_f32_16x16x32_bf16 v[54:57], v[140:143], v[200:203], v[54:57]
	v_mfma_f32_16x16x32_bf16 v[46:49], v[152:155], v[200:203], v[46:49]
	v_mfma_f32_16x16x32_bf16 v[38:41], v[140:143], v[208:211], v[38:41]
	v_mfma_f32_16x16x32_bf16 v[30:33], v[152:155], v[208:211], v[30:33]
	v_mfma_f32_16x16x32_bf16 v[22:25], v[140:143], v[216:219], v[22:25]
	v_mfma_f32_16x16x32_bf16 v[14:17], v[152:155], v[216:219], v[14:17]
	v_mfma_f32_16x16x32_bf16 v[50:53], v[156:159], v[172:175], v[50:53]
	v_mfma_f32_16x16x32_bf16 v[42:45], v[164:167], v[172:175], v[42:45]
	v_mfma_f32_16x16x32_bf16 v[34:37], v[156:159], v[180:183], v[34:37]
	v_mfma_f32_16x16x32_bf16 v[26:29], v[164:167], v[180:183], v[26:29]
	v_mfma_f32_16x16x32_bf16 v[18:21], v[156:159], v[204:207], v[18:21]
	v_mfma_f32_16x16x32_bf16 v[10:13], v[164:167], v[204:207], v[10:13]
	v_mfma_f32_16x16x32_bf16 v[6:9], v[156:159], v[212:215], v[6:9]
	v_mfma_f32_16x16x32_bf16 v[2:5], v[164:167], v[212:215], v[2:5]
	v_mfma_f32_16x16x32_bf16 v[50:53], v[160:163], v[176:179], v[50:53]
	v_mfma_f32_16x16x32_bf16 v[42:45], v[168:171], v[176:179], v[42:45]
	v_mfma_f32_16x16x32_bf16 v[34:37], v[160:163], v[200:203], v[34:37]
	v_mfma_f32_16x16x32_bf16 v[26:29], v[168:171], v[200:203], v[26:29]
	v_mfma_f32_16x16x32_bf16 v[18:21], v[160:163], v[208:211], v[18:21]
	v_mfma_f32_16x16x32_bf16 v[10:13], v[168:171], v[208:211], v[10:13]
	v_mfma_f32_16x16x32_bf16 v[6:9], v[160:163], v[216:219], v[6:9]
	v_mfma_f32_16x16x32_bf16 v[2:5], v[168:171], v[216:219], v[2:5]
	s_setprio 0
	s_barrier
	s_add_i32 s50, s50, 2
	s_add_u32 s48, s48, 0x100
	s_addc_u32 s49, s49, 0
	s_cmpk_gt_u32 s50, 0x55
	s_mov_b64 s[12:13], s[16:17]
	s_cbranch_scc0 .LBB0_1288
	s_and_b64 vcc, exec, s[8:9]
	s_cbranch_vccz .LBB0_1291
	s_barrier
